# K-loop MFMAs reordered within each 8-MFMA k-step group so consecutive MFMAs share an operand (snake order), on top of early priority drop
# speedup vs baseline: 1.0066x; 1.0040x over previous
; #define PG8_STAGE(bufoff, gbase, voff) do { _Pragma("unroll") for (int _i = 0; _i < 2; ++_i) \
;         __builtin_amdgcn_global_load_lds((const unsigned*)((const char*)(gbase) + (voff)[_i]), (PG8_LAS unsigned*)(lds + (bufoff) + ldsw + _i * 8192), 16, 0, 0); } while (0)
; #define PG8_WAIT_V(n) asm volatile("s_waitcnt vmcnt(" #n ")" ::: "memory")
; #define PG8_WAIT_L(n) asm volatile("s_waitcnt lgkmcnt(" #n ")" ::: "memory")
; #define PG8_BAR __builtin_amdgcn_s_barrier()
; #define PG8_SCHED __builtin_amdgcn_sched_barrier(0)
; template <class Epi, class Sched, bool ALIGN_EPI, bool F8 = false>
; __device__ __forceinline__ void gemm_phase(PG8_LAS unsigned char* lds, const Gemm g, const Sched& S, const Epi& E, int tid) {
;     ...
;             PG8_LDB(B0, 0, 0); PG8_LDB(B1, 0, 1); PG8_SCHED; PG8_LDA(At, 0, 0); PG8_STAGE(PG8_SA(1, 1), a1 + hstepA, voffA);
;             PG8_WAIT_V(8); PG8_WAIT_L(0); PG8_BAR; PG8_MMA(0, 0, At, B0); PG8_MMA(0, 1, At, B1); PG8_BAR; PG8_SCHED;
;             PG8_LDA(At, 0, 1); PG8_STAGE(PG8_SB(0, 0), b2, voffB); PG8_STAGE(PG8_SB(0, 1), b2 + hstepB, voffB); PG8_STAGE(PG8_SA(0, 0), a2, voffA);
;             PG8_WAIT_V(8); PG8_WAIT_L(0); PG8_BAR; PG8_MMA(1, 0, At, B0); PG8_MMA(1, 1, At, B1); PG8_BAR; PG8_SCHED;
.LBB0_592:
	s_add_u32 s14, s10, 0xfff80080
	s_addc_u32 s15, s11, -1
	s_add_i32 s89, 0, 0x10000
	s_cmp_eq_u32 s88, 28
	s_cselect_b32 s39, s7, s15
	s_cselect_b32 s38, s9, s14
	s_cselect_b32 s15, s29, s87
	s_cselect_b32 s14, s31, s86
	s_add_i32 s16, 0, 0x14000
	v_add_u32_e32 v46, s89, v173
	v_add_u32_e32 v170, s16, v173
	ds_read_b128 v[34:37], v46
	ds_read_b128 v[38:41], v46 offset:1024
	ds_read_b128 v[42:45], v46 offset:2048
	ds_read_b128 v[46:49], v46 offset:3072
	ds_read_b128 v[162:165], v170
	ds_read_b128 v[166:169], v170 offset:1024
	ds_read_b128 v[190:193], v170 offset:2048
	ds_read_b128 v[198:201], v170 offset:3072
	v_lshl_add_u64 v[170:171], s[10:11], 0, v[158:159]
	s_add_i32 m0, s5, 0xc000
	ds_read_b128 v[202:205], v174
	ds_read_b128 v[206:209], v174 offset:1024
	ds_read_b128 v[210:213], v174 offset:2048
	ds_read_b128 v[214:217], v174 offset:3072
	ds_read_b128 v[236:239], v174 offset:4096
	ds_read_b128 v[240:243], v174 offset:5120
	ds_read_b128 v[244:247], v174 offset:6144
	ds_read_b128 v[248:251], v174 offset:7168
	global_load_lds_dwordx4 v[170:171], off
	v_lshl_add_u64 v[170:171], s[10:11], 0, v[160:161]
	s_add_i32 m0, s5, 0xe000
	s_nop 0
	global_load_lds_dwordx4 v[170:171], off
	s_waitcnt vmcnt(8)
	s_waitcnt lgkmcnt(0)
	s_barrier
	s_setprio 1
	s_waitcnt lgkmcnt(0)
	v_mfma_f32_16x16x32_bf16 v[142:145], v[34:37], v[202:205], v[142:145]
	v_mfma_f32_16x16x32_bf16 v[138:141], v[42:45], v[202:205], v[138:141]
	v_mfma_f32_16x16x32_bf16 v[122:125], v[42:45], v[210:213], v[122:125]
	v_mfma_f32_16x16x32_bf16 v[126:129], v[34:37], v[210:213], v[126:129]
	v_mfma_f32_16x16x32_bf16 v[110:113], v[34:37], v[236:239], v[110:113]
	v_mfma_f32_16x16x32_bf16 v[106:109], v[42:45], v[236:239], v[106:109]
	v_mfma_f32_16x16x32_bf16 v[90:93], v[42:45], v[244:247], v[90:93]
	v_mfma_f32_16x16x32_bf16 v[94:97], v[34:37], v[244:247], v[94:97]
	v_mfma_f32_16x16x32_bf16 v[142:145], v[38:41], v[206:209], v[142:145]
	v_mfma_f32_16x16x32_bf16 v[138:141], v[46:49], v[206:209], v[138:141]
	v_mfma_f32_16x16x32_bf16 v[122:125], v[46:49], v[214:217], v[122:125]
	v_mfma_f32_16x16x32_bf16 v[126:129], v[38:41], v[214:217], v[126:129]
	v_mfma_f32_16x16x32_bf16 v[110:113], v[38:41], v[240:243], v[110:113]
	v_mfma_f32_16x16x32_bf16 v[106:109], v[46:49], v[240:243], v[106:109]
	v_mfma_f32_16x16x32_bf16 v[90:93], v[46:49], v[248:251], v[90:93]
	v_mfma_f32_16x16x32_bf16 v[94:97], v[38:41], v[248:251], v[94:97]
	s_setprio 0
	s_setprio 1
	v_mfma_f32_16x16x32_bf16 v[134:137], v[162:165], v[202:205], v[134:137]
	v_mfma_f32_16x16x32_bf16 v[130:133], v[190:193], v[202:205], v[130:133]
	v_mfma_f32_16x16x32_bf16 v[114:117], v[190:193], v[210:213], v[114:117]
	v_mfma_f32_16x16x32_bf16 v[118:121], v[162:165], v[210:213], v[118:121]
	v_mfma_f32_16x16x32_bf16 v[102:105], v[162:165], v[236:239], v[102:105]
	v_mfma_f32_16x16x32_bf16 v[98:101], v[190:193], v[236:239], v[98:101]
	v_mfma_f32_16x16x32_bf16 v[82:85], v[190:193], v[244:247], v[82:85]
	v_mfma_f32_16x16x32_bf16 v[86:89], v[162:165], v[244:247], v[86:89]
	v_mfma_f32_16x16x32_bf16 v[134:137], v[166:169], v[206:209], v[134:137]
	v_mfma_f32_16x16x32_bf16 v[130:133], v[198:201], v[206:209], v[130:133]
	v_mfma_f32_16x16x32_bf16 v[114:117], v[198:201], v[214:217], v[114:117]
	v_mfma_f32_16x16x32_bf16 v[118:121], v[166:169], v[214:217], v[118:121]
	s_setprio 0
	v_mfma_f32_16x16x32_bf16 v[102:105], v[166:169], v[240:243], v[102:105]
	v_mfma_f32_16x16x32_bf16 v[98:101], v[198:201], v[240:243], v[98:101]
	v_mfma_f32_16x16x32_bf16 v[82:85], v[198:201], v[248:251], v[82:85]
	v_mfma_f32_16x16x32_bf16 v[86:89], v[166:169], v[248:251], v[86:89]
	s_barrier
	s_add_i32 s89, s89, s4
	v_lshl_add_u64 v[170:171], s[14:15], 0, v[148:149]
	s_mov_b32 m0, s89
	ds_read_b128 v[202:205], v174 offset:16384
	ds_read_b128 v[206:209], v174 offset:17408
	ds_read_b128 v[210:213], v174 offset:18432
	ds_read_b128 v[214:217], v174 offset:19456
	ds_read_b128 v[236:239], v174 offset:20480
	ds_read_b128 v[240:243], v174 offset:21504
	ds_read_b128 v[244:247], v174 offset:22528
	ds_read_b128 v[248:251], v174 offset:23552
	global_load_lds_dwordx4 v[170:171], off
	s_add_i32 m0, s89, 0x2000
	s_add_u32 vcc_lo, s14, 0x80000
	v_lshl_add_u64 v[176:177], s[14:15], 0, v[152:153]
	s_addc_u32 vcc_hi, s15, 0
	s_add_i32 s16, s16, s4
	global_load_lds_dwordx4 v[176:177], off
	v_lshl_add_u64 v[178:179], vcc, 0, v[148:149]
	s_mov_b32 m0, s16
	v_lshl_add_u64 v[180:181], s[38:39], 0, v[150:151]
	global_load_lds_dwordx4 v[178:179], off
	v_lshl_add_u64 v[178:179], vcc, 0, v[152:153]
	s_add_i32 m0, s16, 0x2000
	s_nop 0
	global_load_lds_dwordx4 v[178:179], off
	v_lshl_add_u64 v[178:179], s[38:39], 0, v[146:147]
	s_mov_b32 m0, s5
	s_nop 0
	global_load_lds_dwordx4 v[178:179], off
	s_mov_b32 m0, s22
	s_nop 0
	global_load_lds_dwordx4 v[180:181], off
	s_waitcnt vmcnt(8)
	s_waitcnt lgkmcnt(0)
	s_barrier
; #define PG8_STAGE(bufoff, gbase, voff) do { _Pragma("unroll") for (int _i = 0; _i < 2; ++_i) \
;         __builtin_amdgcn_global_load_lds((const unsigned*)((const char*)(gbase) + (voff)[_i]), (PG8_LAS unsigned*)(lds + (bufoff) + ldsw + _i * 8192), 16, 0, 0); } while (0)
; #define PG8_WAIT_V(n) asm volatile("s_waitcnt vmcnt(" #n ")" ::: "memory")
; #define PG8_WAIT_L(n) asm volatile("s_waitcnt lgkmcnt(" #n ")" ::: "memory")
; #define PG8_BAR __builtin_amdgcn_s_barrier()
; #define PG8_SCHED __builtin_amdgcn_sched_barrier(0)
; template <class Epi, class Sched, bool ALIGN_EPI, bool F8 = false>
; __device__ __forceinline__ void gemm_phase(PG8_LAS unsigned char* lds, const Gemm g, const Sched& S, const Epi& E, int tid) {
;     ...
;             PG8_WAIT_V(8); PG8_WAIT_L(0); PG8_BAR; PG8_MMA(1, 0, At, B0); PG8_MMA(1, 1, At, B1); PG8_BAR; PG8_SCHED;
;             PG8_LDB(B0, 1, 0); PG8_LDB(B1, 1, 1); PG8_SCHED; PG8_LDA(At, 1, 0); PG8_STAGE(PG8_SA(0, 1), a2 + hstepA, voffA);
;             PG8_WAIT_V(8); PG8_WAIT_L(0); PG8_BAR; PG8_MMA(0, 0, At, B0); PG8_MMA(0, 1, At, B1); PG8_BAR; PG8_SCHED;
;             PG8_LDA(At, 1, 1); PG8_STAGE(PG8_SB(1, 0), b3, voffB); PG8_STAGE(PG8_SB(1, 1), b3 + hstepB, voffB); PG8_STAGE(PG8_SA(1, 0), a3, voffA);
	s_setprio 1
	s_waitcnt lgkmcnt(0)
	v_mfma_f32_16x16x32_bf16 v[78:81], v[34:37], v[202:205], v[78:81]
	v_mfma_f32_16x16x32_bf16 v[74:77], v[42:45], v[202:205], v[74:77]
	v_mfma_f32_16x16x32_bf16 v[58:61], v[42:45], v[210:213], v[58:61]
	v_mfma_f32_16x16x32_bf16 v[62:65], v[34:37], v[210:213], v[62:65]
	v_mfma_f32_16x16x32_bf16 v[30:33], v[34:37], v[236:239], v[30:33]
	v_mfma_f32_16x16x32_bf16 v[26:29], v[42:45], v[236:239], v[26:29]
	v_mfma_f32_16x16x32_bf16 v[10:13], v[42:45], v[244:247], v[10:13]
	v_mfma_f32_16x16x32_bf16 v[14:17], v[34:37], v[244:247], v[14:17]
	v_mfma_f32_16x16x32_bf16 v[78:81], v[38:41], v[206:209], v[78:81]
	v_mfma_f32_16x16x32_bf16 v[74:77], v[46:49], v[206:209], v[74:77]
	v_mfma_f32_16x16x32_bf16 v[58:61], v[46:49], v[214:217], v[58:61]
	v_mfma_f32_16x16x32_bf16 v[62:65], v[38:41], v[214:217], v[62:65]
	v_mfma_f32_16x16x32_bf16 v[30:33], v[38:41], v[240:243], v[30:33]
	v_mfma_f32_16x16x32_bf16 v[26:29], v[46:49], v[240:243], v[26:29]
	v_mfma_f32_16x16x32_bf16 v[10:13], v[46:49], v[248:251], v[10:13]
	v_mfma_f32_16x16x32_bf16 v[14:17], v[38:41], v[248:251], v[14:17]
	s_setprio 0
	s_setprio 1
	v_mfma_f32_16x16x32_bf16 v[22:25], v[162:165], v[236:239], v[22:25]
	v_mfma_f32_16x16x32_bf16 v[18:21], v[190:193], v[236:239], v[18:21]
	v_mfma_f32_16x16x32_bf16 v[2:5], v[190:193], v[244:247], v[2:5]
	v_mfma_f32_16x16x32_bf16 v[6:9], v[162:165], v[244:247], v[6:9]
	v_mfma_f32_16x16x32_bf16 v[34:37], v[162:165], v[202:205], v[70:73]
	v_mfma_f32_16x16x32_bf16 v[38:41], v[190:193], v[202:205], v[66:69]
	v_mfma_f32_16x16x32_bf16 v[46:49], v[190:193], v[210:213], v[50:53]
	v_mfma_f32_16x16x32_bf16 v[42:45], v[162:165], v[210:213], v[54:57]
	v_mfma_f32_16x16x32_bf16 v[22:25], v[166:169], v[240:243], v[22:25]
	v_mfma_f32_16x16x32_bf16 v[18:21], v[198:201], v[240:243], v[18:21]
	v_mfma_f32_16x16x32_bf16 v[2:5], v[198:201], v[248:251], v[2:5]
	v_mfma_f32_16x16x32_bf16 v[6:9], v[166:169], v[248:251], v[6:9]
	s_setprio 0
	v_mfma_f32_16x16x32_bf16 v[34:37], v[166:169], v[206:209], v[34:37]
	v_mfma_f32_16x16x32_bf16 v[38:41], v[198:201], v[206:209], v[38:41]
	v_mfma_f32_16x16x32_bf16 v[46:49], v[198:201], v[214:217], v[46:49]
	v_mfma_f32_16x16x32_bf16 v[42:45], v[166:169], v[214:217], v[42:45]
	s_barrier
	s_add_i32 s16, 0, 0x18000
	s_add_i32 s89, 0, 0x1c000
	v_add_u32_e32 v70, s16, v173
	v_add_u32_e32 v175, s89, v173
	ds_read_b128 v[50:53], v70
	ds_read_b128 v[54:57], v70 offset:1024
	ds_read_b128 v[66:69], v70 offset:2048
	ds_read_b128 v[70:73], v70 offset:3072
	ds_read_b128 v[162:165], v175
	ds_read_b128 v[166:169], v175 offset:1024
	ds_read_b128 v[190:193], v175 offset:2048
	ds_read_b128 v[198:201], v175 offset:3072
	s_add_u32 s38, s38, 0x80000
	s_addc_u32 s39, s39, 0
	s_mov_b32 m0, s23
	v_lshl_add_u64 v[182:183], s[38:39], 0, v[146:147]
	ds_read_b128 v[202:205], v174 offset:32768
	ds_read_b128 v[206:209], v174 offset:33792
	ds_read_b128 v[210:213], v174 offset:34816
	ds_read_b128 v[214:217], v174 offset:35840
	ds_read_b128 v[236:239], v174 offset:36864
	ds_read_b128 v[240:243], v174 offset:37888
	ds_read_b128 v[244:247], v174 offset:38912
	ds_read_b128 v[248:251], v174 offset:39936
	global_load_lds_dwordx4 v[182:183], off
	v_lshl_add_u64 v[182:183], s[38:39], 0, v[150:151]
	s_mov_b32 m0, s24
	s_nop 0
	global_load_lds_dwordx4 v[182:183], off
	s_waitcnt vmcnt(8)
	s_waitcnt lgkmcnt(0)
	s_barrier
	s_setprio 1
	s_waitcnt lgkmcnt(0)
	v_mfma_f32_16x16x32_bf16 v[142:145], v[50:53], v[202:205], v[142:145]
	v_mfma_f32_16x16x32_bf16 v[138:141], v[66:69], v[202:205], v[138:141]
	v_mfma_f32_16x16x32_bf16 v[122:125], v[66:69], v[210:213], v[122:125]
	v_mfma_f32_16x16x32_bf16 v[126:129], v[50:53], v[210:213], v[126:129]
	v_mfma_f32_16x16x32_bf16 v[110:113], v[50:53], v[236:239], v[110:113]
	v_mfma_f32_16x16x32_bf16 v[106:109], v[66:69], v[236:239], v[106:109]
	v_mfma_f32_16x16x32_bf16 v[90:93], v[66:69], v[244:247], v[90:93]
	v_mfma_f32_16x16x32_bf16 v[94:97], v[50:53], v[244:247], v[94:97]
	v_mfma_f32_16x16x32_bf16 v[142:145], v[54:57], v[206:209], v[142:145]
	v_mfma_f32_16x16x32_bf16 v[138:141], v[70:73], v[206:209], v[138:141]
	v_mfma_f32_16x16x32_bf16 v[122:125], v[70:73], v[214:217], v[122:125]
	v_mfma_f32_16x16x32_bf16 v[126:129], v[54:57], v[214:217], v[126:129]
	v_mfma_f32_16x16x32_bf16 v[110:113], v[54:57], v[240:243], v[110:113]
	v_mfma_f32_16x16x32_bf16 v[106:109], v[70:73], v[240:243], v[106:109]
	v_mfma_f32_16x16x32_bf16 v[90:93], v[70:73], v[248:251], v[90:93]
	v_mfma_f32_16x16x32_bf16 v[94:97], v[54:57], v[248:251], v[94:97]
	s_setprio 0
	s_setprio 1
	v_mfma_f32_16x16x32_bf16 v[134:137], v[162:165], v[202:205], v[134:137]
	v_mfma_f32_16x16x32_bf16 v[130:133], v[190:193], v[202:205], v[130:133]
	v_mfma_f32_16x16x32_bf16 v[114:117], v[190:193], v[210:213], v[114:117]
	v_mfma_f32_16x16x32_bf16 v[118:121], v[162:165], v[210:213], v[118:121]
	v_mfma_f32_16x16x32_bf16 v[102:105], v[162:165], v[236:239], v[102:105]
	v_mfma_f32_16x16x32_bf16 v[98:101], v[190:193], v[236:239], v[98:101]
	v_mfma_f32_16x16x32_bf16 v[82:85], v[190:193], v[244:247], v[82:85]
	v_mfma_f32_16x16x32_bf16 v[86:89], v[162:165], v[244:247], v[86:89]
	v_mfma_f32_16x16x32_bf16 v[134:137], v[166:169], v[206:209], v[134:137]
	v_mfma_f32_16x16x32_bf16 v[130:133], v[198:201], v[206:209], v[130:133]
	v_mfma_f32_16x16x32_bf16 v[114:117], v[198:201], v[214:217], v[114:117]
	v_mfma_f32_16x16x32_bf16 v[118:121], v[166:169], v[214:217], v[118:121]
	s_setprio 0
	v_mfma_f32_16x16x32_bf16 v[102:105], v[166:169], v[240:243], v[102:105]
	v_mfma_f32_16x16x32_bf16 v[98:101], v[198:201], v[240:243], v[98:101]
	v_mfma_f32_16x16x32_bf16 v[82:85], v[198:201], v[248:251], v[82:85]
	v_mfma_f32_16x16x32_bf16 v[86:89], v[166:169], v[248:251], v[86:89]
	s_barrier
; #define PG8_STAGE(bufoff, gbase, voff) do { _Pragma("unroll") for (int _i = 0; _i < 2; ++_i) \
;         __builtin_amdgcn_global_load_lds((const unsigned*)((const char*)(gbase) + (voff)[_i]), (PG8_LAS unsigned*)(lds + (bufoff) + ldsw + _i * 8192), 16, 0, 0); } while (0)
; #define PG8_WAIT_V(n) asm volatile("s_waitcnt vmcnt(" #n ")" ::: "memory")
; #define PG8_WAIT_L(n) asm volatile("s_waitcnt lgkmcnt(" #n ")" ::: "memory")
; #define PG8_BAR __builtin_amdgcn_s_barrier()
; #define PG8_SCHED __builtin_amdgcn_sched_barrier(0)
; template <class Epi, class Sched, bool ALIGN_EPI, bool F8 = false>
; __device__ __forceinline__ void gemm_phase(PG8_LAS unsigned char* lds, const Gemm g, const Sched& S, const Epi& E, int tid) {
;     ...
;             PG8_LDA(At, 1, 1); PG8_STAGE(PG8_SB(1, 0), b3, voffB); PG8_STAGE(PG8_SB(1, 1), b3 + hstepB, voffB); PG8_STAGE(PG8_SA(1, 0), a3, voffA);
;             PG8_WAIT_V(8); PG8_WAIT_L(0); PG8_BAR; PG8_MMA(1, 0, At, B0); PG8_MMA(1, 1, At, B1); PG8_BAR; PG8_SCHED;
	s_add_i32 s16, s16, s4
	v_lshl_add_u64 v[170:171], v[170:171], 0, s[60:61]
	s_mov_b32 m0, s16
	ds_read_b128 v[202:205], v174 offset:49152
	ds_read_b128 v[206:209], v174 offset:50176
	ds_read_b128 v[210:213], v174 offset:51200
	ds_read_b128 v[214:217], v174 offset:52224
	ds_read_b128 v[236:239], v174 offset:53248
	ds_read_b128 v[240:243], v174 offset:54272
	ds_read_b128 v[244:247], v174 offset:55296
	ds_read_b128 v[248:251], v174 offset:56320
	global_load_lds_dwordx4 v[170:171], off
	s_add_i32 m0, s16, 0x2000
	s_add_u32 s14, s14, 0x80080
	v_lshl_add_u64 v[170:171], v[176:177], 0, s[60:61]
	s_addc_u32 s15, s15, 0
	s_add_i32 s16, s89, s4
	global_load_lds_dwordx4 v[170:171], off
	v_lshl_add_u64 v[170:171], s[14:15], 0, v[148:149]
	s_mov_b32 m0, s16
	s_nop 0
	global_load_lds_dwordx4 v[170:171], off
	v_lshl_add_u64 v[170:171], s[14:15], 0, v[152:153]
	s_add_i32 m0, s16, 0x2000
	s_nop 0
	global_load_lds_dwordx4 v[170:171], off
	v_lshl_add_u64 v[170:171], v[178:179], 0, s[60:61]
	s_mov_b32 m0, s25
	s_nop 0
	global_load_lds_dwordx4 v[170:171], off
	v_lshl_add_u64 v[170:171], v[180:181], 0, s[60:61]
	s_mov_b32 m0, s0
	s_nop 0
	global_load_lds_dwordx4 v[170:171], off
	s_waitcnt vmcnt(8)
	s_waitcnt lgkmcnt(0)
	s_barrier
	s_setprio 1
	s_waitcnt lgkmcnt(0)
	v_mfma_f32_16x16x32_bf16 v[78:81], v[50:53], v[202:205], v[78:81]
	v_mfma_f32_16x16x32_bf16 v[74:77], v[66:69], v[202:205], v[74:77]
	v_mfma_f32_16x16x32_bf16 v[58:61], v[66:69], v[210:213], v[58:61]
	v_mfma_f32_16x16x32_bf16 v[62:65], v[50:53], v[210:213], v[62:65]
	v_mfma_f32_16x16x32_bf16 v[30:33], v[50:53], v[236:239], v[30:33]
	v_mfma_f32_16x16x32_bf16 v[26:29], v[66:69], v[236:239], v[26:29]
	v_mfma_f32_16x16x32_bf16 v[10:13], v[66:69], v[244:247], v[10:13]
	v_mfma_f32_16x16x32_bf16 v[14:17], v[50:53], v[244:247], v[14:17]
	v_mfma_f32_16x16x32_bf16 v[78:81], v[54:57], v[206:209], v[78:81]
	v_mfma_f32_16x16x32_bf16 v[74:77], v[70:73], v[206:209], v[74:77]
	v_mfma_f32_16x16x32_bf16 v[58:61], v[70:73], v[214:217], v[58:61]
	v_mfma_f32_16x16x32_bf16 v[62:65], v[54:57], v[214:217], v[62:65]
	v_mfma_f32_16x16x32_bf16 v[30:33], v[54:57], v[240:243], v[30:33]
	v_mfma_f32_16x16x32_bf16 v[26:29], v[70:73], v[240:243], v[26:29]
	v_mfma_f32_16x16x32_bf16 v[10:13], v[70:73], v[248:251], v[10:13]
	v_mfma_f32_16x16x32_bf16 v[14:17], v[54:57], v[248:251], v[14:17]
	s_setprio 0
	s_setprio 1
	v_mfma_f32_16x16x32_bf16 v[34:37], v[162:165], v[202:205], v[34:37]
	v_mfma_f32_16x16x32_bf16 v[70:73], v[166:169], v[206:209], v[34:37]
	v_mfma_f32_16x16x32_bf16 v[66:69], v[198:201], v[206:209], v[34:37]
	v_mfma_f32_16x16x32_bf16 v[34:37], v[190:193], v[202:205], v[38:41]
	v_mfma_f32_16x16x32_bf16 v[34:37], v[162:165], v[210:213], v[42:45]
	v_mfma_f32_16x16x32_bf16 v[54:57], v[166:169], v[214:217], v[34:37]
	v_mfma_f32_16x16x32_bf16 v[22:25], v[162:165], v[236:239], v[22:25]
	v_mfma_f32_16x16x32_bf16 v[34:37], v[190:193], v[210:213], v[46:49]
	v_mfma_f32_16x16x32_bf16 v[18:21], v[190:193], v[236:239], v[18:21]
	v_mfma_f32_16x16x32_bf16 v[6:9], v[162:165], v[244:247], v[6:9]
	v_mfma_f32_16x16x32_bf16 v[50:53], v[198:201], v[214:217], v[34:37]
	v_mfma_f32_16x16x32_bf16 v[2:5], v[190:193], v[244:247], v[2:5]
	s_setprio 0
	v_mfma_f32_16x16x32_bf16 v[22:25], v[166:169], v[240:243], v[22:25]
	v_mfma_f32_16x16x32_bf16 v[18:21], v[198:201], v[240:243], v[18:21]
	v_mfma_f32_16x16x32_bf16 v[2:5], v[198:201], v[248:251], v[2:5]
	v_mfma_f32_16x16x32_bf16 v[6:9], v[166:169], v[248:251], v[6:9]
	s_barrier
	s_add_i32 s88, s88, 2
	s_add_u32 s10, s10, 0x100
	s_addc_u32 s11, s11, 0
	s_add_u32 s86, s86, 0x100
	s_addc_u32 s87, s87, 0
	s_cmp_gt_u32 s88, 29
	s_cbranch_scc0 .LBB0_592
	s_and_b64 vcc, exec, s[26:27]
	s_cbranch_vccz .LBB0_595
	s_barrier

; #define PG8_STAGE(bufoff, gbase, voff) do { _Pragma("unroll") for (int _i = 0; _i < 2; ++_i) \
;         __builtin_amdgcn_global_load_lds((const unsigned*)((const char*)(gbase) + (voff)[_i]), (PG8_LAS unsigned*)(lds + (bufoff) + ldsw + _i * 8192), 16, 0, 0); } while (0)
; #define PG8_WAIT_V(n) asm volatile("s_waitcnt vmcnt(" #n ")" ::: "memory")
; #define PG8_WAIT_L(n) asm volatile("s_waitcnt lgkmcnt(" #n ")" ::: "memory")
; #define PG8_BAR __builtin_amdgcn_s_barrier()
; #define PG8_SCHED __builtin_amdgcn_sched_barrier(0)
; template <class Epi, class Sched, bool ALIGN_EPI, bool F8 = false>
; __device__ __forceinline__ void gemm_phase(PG8_LAS unsigned char* lds, const Gemm g, const Sched& S, const Epi& E, int tid) {
;     ...
;             PG8_LDB(B0, 0, 0); PG8_LDB(B1, 0, 1); PG8_SCHED; PG8_LDA(At, 0, 0); PG8_STAGE(PG8_SA(1, 1), a1 + hstepA, voffA);
;             PG8_WAIT_V(8); PG8_WAIT_L(0); PG8_BAR; PG8_MMA(0, 0, At, B0); PG8_MMA(0, 1, At, B1); PG8_BAR; PG8_SCHED;
;             PG8_LDA(At, 0, 1); PG8_STAGE(PG8_SB(0, 0), b2, voffB); PG8_STAGE(PG8_SB(0, 1), b2 + hstepB, voffB); PG8_STAGE(PG8_SA(0, 0), a2, voffA);
;             PG8_WAIT_V(8); PG8_WAIT_L(0); PG8_BAR; PG8_MMA(1, 0, At, B0); PG8_MMA(1, 1, At, B1); PG8_BAR; PG8_SCHED;
.LBB0_739:
	s_add_u32 s14, s50, 0xfff80080
	s_addc_u32 s15, s51, -1
	s_add_i32 s84, 0, 0x10000
	s_cmp_eq_u32 s83, 28
	s_cselect_b32 s69, s5, s15
	s_cselect_b32 s68, s7, s14
	v_add_u32_e32 v0, s84, v173
	s_cselect_b32 s15, s23, s82
	s_cselect_b32 s14, s25, s45
	s_add_i32 vcc_lo, 0, 0x14000
	ds_read_b128 v[54:57], v0
	ds_read_b128 v[62:65], v0 offset:1024
	ds_read_b128 v[66:69], v0 offset:2048
	ds_read_b128 v[70:73], v0 offset:3072
	v_add_u32_e32 v0, vcc_lo, v173
	ds_read_b128 v[162:165], v0
	ds_read_b128 v[166:169], v0 offset:1024
	ds_read_b128 v[190:193], v0 offset:2048
	ds_read_b128 v[198:201], v0 offset:3072
	v_lshl_add_u64 v[170:171], s[50:51], 0, v[158:159]
	s_add_i32 m0, s1, 0xc000
	ds_read_b128 v[202:205], v175
	ds_read_b128 v[206:209], v175 offset:1024
	ds_read_b128 v[210:213], v175 offset:2048
	ds_read_b128 v[214:217], v175 offset:3072
	ds_read_b128 v[236:239], v175 offset:4096
	ds_read_b128 v[240:243], v175 offset:5120
	ds_read_b128 v[244:247], v175 offset:6144
	ds_read_b128 v[248:251], v175 offset:7168
	global_load_lds_dwordx4 v[170:171], off
	v_lshl_add_u64 v[170:171], s[50:51], 0, v[160:161]
	s_add_i32 m0, s1, 0xe000
	s_nop 0
	global_load_lds_dwordx4 v[170:171], off
	s_waitcnt vmcnt(8)
	s_waitcnt lgkmcnt(0)
	s_barrier
	s_setprio 1
	s_waitcnt lgkmcnt(0)
	v_mfma_f32_16x16x32_bf16 v[142:145], v[54:57], v[202:205], v[142:145]
	v_mfma_f32_16x16x32_bf16 v[138:141], v[66:69], v[202:205], v[138:141]
	v_mfma_f32_16x16x32_bf16 v[122:125], v[66:69], v[210:213], v[122:125]
	v_mfma_f32_16x16x32_bf16 v[126:129], v[54:57], v[210:213], v[126:129]
	v_mfma_f32_16x16x32_bf16 v[110:113], v[54:57], v[236:239], v[110:113]
	v_mfma_f32_16x16x32_bf16 v[106:109], v[66:69], v[236:239], v[106:109]
	v_mfma_f32_16x16x32_bf16 v[90:93], v[66:69], v[244:247], v[90:93]
	v_mfma_f32_16x16x32_bf16 v[94:97], v[54:57], v[244:247], v[94:97]
	v_mfma_f32_16x16x32_bf16 v[142:145], v[62:65], v[206:209], v[142:145]
	v_mfma_f32_16x16x32_bf16 v[138:141], v[70:73], v[206:209], v[138:141]
	v_mfma_f32_16x16x32_bf16 v[122:125], v[70:73], v[214:217], v[122:125]
	v_mfma_f32_16x16x32_bf16 v[126:129], v[62:65], v[214:217], v[126:129]
	v_mfma_f32_16x16x32_bf16 v[110:113], v[62:65], v[240:243], v[110:113]
	v_mfma_f32_16x16x32_bf16 v[106:109], v[70:73], v[240:243], v[106:109]
	v_mfma_f32_16x16x32_bf16 v[90:93], v[70:73], v[248:251], v[90:93]
	v_mfma_f32_16x16x32_bf16 v[94:97], v[62:65], v[248:251], v[94:97]
	s_setprio 0
	s_setprio 1
	v_mfma_f32_16x16x32_bf16 v[134:137], v[162:165], v[202:205], v[134:137]
	v_mfma_f32_16x16x32_bf16 v[130:133], v[190:193], v[202:205], v[130:133]
	v_mfma_f32_16x16x32_bf16 v[114:117], v[190:193], v[210:213], v[114:117]
	v_mfma_f32_16x16x32_bf16 v[118:121], v[162:165], v[210:213], v[118:121]
	v_mfma_f32_16x16x32_bf16 v[102:105], v[162:165], v[236:239], v[102:105]
	v_mfma_f32_16x16x32_bf16 v[98:101], v[190:193], v[236:239], v[98:101]
	v_mfma_f32_16x16x32_bf16 v[82:85], v[190:193], v[244:247], v[82:85]
	v_mfma_f32_16x16x32_bf16 v[86:89], v[162:165], v[244:247], v[86:89]
	v_mfma_f32_16x16x32_bf16 v[134:137], v[166:169], v[206:209], v[134:137]
	v_mfma_f32_16x16x32_bf16 v[130:133], v[198:201], v[206:209], v[130:133]
	v_mfma_f32_16x16x32_bf16 v[114:117], v[198:201], v[214:217], v[114:117]
	v_mfma_f32_16x16x32_bf16 v[118:121], v[166:169], v[214:217], v[118:121]
	s_setprio 0
	v_mfma_f32_16x16x32_bf16 v[102:105], v[166:169], v[240:243], v[102:105]
	v_mfma_f32_16x16x32_bf16 v[98:101], v[198:201], v[240:243], v[98:101]
	v_mfma_f32_16x16x32_bf16 v[82:85], v[198:201], v[248:251], v[82:85]
	v_mfma_f32_16x16x32_bf16 v[86:89], v[166:169], v[248:251], v[86:89]
	s_barrier
	s_add_i32 s84, s84, s0
	v_lshl_add_u64 v[170:171], s[14:15], 0, v[148:149]
	s_mov_b32 m0, s84
	ds_read_b128 v[202:205], v175 offset:16384
	ds_read_b128 v[206:209], v175 offset:17408
	ds_read_b128 v[210:213], v175 offset:18432
	ds_read_b128 v[214:217], v175 offset:19456
	ds_read_b128 v[236:239], v175 offset:20480
	ds_read_b128 v[240:243], v175 offset:21504
	ds_read_b128 v[244:247], v175 offset:22528
	ds_read_b128 v[248:251], v175 offset:23552
	global_load_lds_dwordx4 v[170:171], off
	s_add_i32 m0, s84, 0x2000
	s_add_u32 s84, s14, 0x80000
	v_lshl_add_u64 v[176:177], s[14:15], 0, v[152:153]
	s_addc_u32 s85, s15, 0
	s_add_i32 vcc_lo, vcc_lo, s0
	global_load_lds_dwordx4 v[176:177], off
	v_lshl_add_u64 v[178:179], s[84:85], 0, v[148:149]
	s_mov_b32 m0, vcc_lo
	v_lshl_add_u64 v[180:181], s[68:69], 0, v[150:151]
	global_load_lds_dwordx4 v[178:179], off
	v_lshl_add_u64 v[178:179], s[84:85], 0, v[152:153]
	s_add_i32 m0, vcc_lo, 0x2000
	s_nop 0
	global_load_lds_dwordx4 v[178:179], off
	v_lshl_add_u64 v[178:179], s[68:69], 0, v[146:147]
	s_mov_b32 m0, s1
	s_nop 0
	global_load_lds_dwordx4 v[178:179], off
	s_mov_b32 m0, s44
	s_nop 0
	global_load_lds_dwordx4 v[180:181], off
	s_waitcnt vmcnt(8)
	s_waitcnt lgkmcnt(0)
	s_barrier
; #define PG8_STAGE(bufoff, gbase, voff) do { _Pragma("unroll") for (int _i = 0; _i < 2; ++_i) \
;         __builtin_amdgcn_global_load_lds((const unsigned*)((const char*)(gbase) + (voff)[_i]), (PG8_LAS unsigned*)(lds + (bufoff) + ldsw + _i * 8192), 16, 0, 0); } while (0)
; #define PG8_WAIT_V(n) asm volatile("s_waitcnt vmcnt(" #n ")" ::: "memory")
; #define PG8_WAIT_L(n) asm volatile("s_waitcnt lgkmcnt(" #n ")" ::: "memory")
; #define PG8_BAR __builtin_amdgcn_s_barrier()
; #define PG8_SCHED __builtin_amdgcn_sched_barrier(0)
; template <class Epi, class Sched, bool ALIGN_EPI, bool F8 = false>
; __device__ __forceinline__ void gemm_phase(PG8_LAS unsigned char* lds, const Gemm g, const Sched& S, const Epi& E, int tid) {
;     ...
;             PG8_LDB(B0, 0, 0); PG8_LDB(B1, 0, 1); PG8_SCHED; PG8_LDA(At, 0, 0); PG8_STAGE(PG8_SA(1, 1), a1 + hstepA, voffA);
;             PG8_WAIT_V(8); PG8_WAIT_L(0); PG8_BAR; PG8_MMA(0, 0, At, B0); PG8_MMA(0, 1, At, B1); PG8_BAR; PG8_SCHED;
;             PG8_LDA(At, 0, 1); PG8_STAGE(PG8_SB(0, 0), b2, voffB); PG8_STAGE(PG8_SB(0, 1), b2 + hstepB, voffB); PG8_STAGE(PG8_SA(0, 0), a2, voffA);
;             PG8_WAIT_V(8); PG8_WAIT_L(0); PG8_BAR; PG8_MMA(1, 0, At, B0); PG8_MMA(1, 1, At, B1); PG8_BAR; PG8_SCHED;
;             PG8_LDB(B0, 1, 0); PG8_LDB(B1, 1, 1); PG8_SCHED; PG8_LDA(At, 1, 0); PG8_STAGE(PG8_SA(0, 1), a2 + hstepA, voffA);
;             PG8_WAIT_V(8); PG8_WAIT_L(0); PG8_BAR; PG8_MMA(0, 0, At, B0); PG8_MMA(0, 1, At, B1); PG8_BAR; PG8_SCHED;
;             PG8_LDA(At, 1, 1); PG8_STAGE(PG8_SB(1, 0), b3, voffB); PG8_STAGE(PG8_SB(1, 1), b3 + hstepB, voffB); PG8_STAGE(PG8_SA(1, 0), a3, voffA);
;             PG8_WAIT_V(8); PG8_WAIT_L(0); PG8_BAR; PG8_MMA(1, 0, At, B0); PG8_MMA(1, 1, At, B1); PG8_BAR; PG8_SCHED;
	s_setprio 1
	s_waitcnt lgkmcnt(0)
	v_mfma_f32_16x16x32_bf16 v[78:81], v[54:57], v[202:205], v[78:81]
	v_mfma_f32_16x16x32_bf16 v[74:77], v[66:69], v[202:205], v[74:77]
	v_mfma_f32_16x16x32_bf16 v[42:45], v[66:69], v[210:213], v[42:45]
	v_mfma_f32_16x16x32_bf16 v[46:49], v[54:57], v[210:213], v[46:49]
	v_mfma_f32_16x16x32_bf16 v[30:33], v[54:57], v[236:239], v[30:33]
	v_mfma_f32_16x16x32_bf16 v[26:29], v[66:69], v[236:239], v[26:29]
	v_mfma_f32_16x16x32_bf16 v[10:13], v[66:69], v[244:247], v[10:13]
	v_mfma_f32_16x16x32_bf16 v[14:17], v[54:57], v[244:247], v[14:17]
	v_mfma_f32_16x16x32_bf16 v[78:81], v[62:65], v[206:209], v[78:81]
	v_mfma_f32_16x16x32_bf16 v[74:77], v[70:73], v[206:209], v[74:77]
	v_mfma_f32_16x16x32_bf16 v[42:45], v[70:73], v[214:217], v[42:45]
	v_mfma_f32_16x16x32_bf16 v[46:49], v[62:65], v[214:217], v[46:49]
	v_mfma_f32_16x16x32_bf16 v[30:33], v[62:65], v[240:243], v[30:33]
	v_mfma_f32_16x16x32_bf16 v[26:29], v[70:73], v[240:243], v[26:29]
	v_mfma_f32_16x16x32_bf16 v[10:13], v[70:73], v[248:251], v[10:13]
	v_mfma_f32_16x16x32_bf16 v[14:17], v[62:65], v[248:251], v[14:17]
	s_setprio 0
	s_setprio 1
	v_mfma_f32_16x16x32_bf16 v[50:53], v[190:193], v[202:205], v[50:53]
	v_mfma_f32_16x16x32_bf16 v[38:41], v[162:165], v[210:213], v[38:41]
	v_mfma_f32_16x16x32_bf16 v[22:25], v[162:165], v[236:239], v[22:25]
	v_mfma_f32_16x16x32_bf16 v[34:37], v[190:193], v[210:213], v[34:37]
	v_mfma_f32_16x16x32_bf16 v[18:21], v[190:193], v[236:239], v[18:21]
	v_mfma_f32_16x16x32_bf16 v[6:9], v[162:165], v[244:247], v[6:9]
	v_mfma_f32_16x16x32_bf16 v[54:57], v[162:165], v[202:205], v[58:61]
	v_mfma_f32_16x16x32_bf16 v[2:5], v[190:193], v[244:247], v[2:5]
	v_mfma_f32_16x16x32_bf16 v[50:53], v[198:201], v[206:209], v[50:53]
	v_mfma_f32_16x16x32_bf16 v[38:41], v[166:169], v[214:217], v[38:41]
	v_mfma_f32_16x16x32_bf16 v[22:25], v[166:169], v[240:243], v[22:25]
	v_mfma_f32_16x16x32_bf16 v[34:37], v[198:201], v[214:217], v[34:37]
	s_setprio 0
	v_mfma_f32_16x16x32_bf16 v[18:21], v[198:201], v[240:243], v[18:21]
	v_mfma_f32_16x16x32_bf16 v[6:9], v[166:169], v[248:251], v[6:9]
	v_mfma_f32_16x16x32_bf16 v[54:57], v[166:169], v[206:209], v[54:57]
	v_mfma_f32_16x16x32_bf16 v[2:5], v[198:201], v[248:251], v[2:5]
	s_barrier
	s_add_i32 s84, 0, 0x18000
	v_add_u32_e32 v0, s84, v173
	s_add_i32 s85, 0, 0x1c000
	ds_read_b128 v[58:61], v0
	ds_read_b128 v[62:65], v0 offset:1024
	ds_read_b128 v[66:69], v0 offset:2048
	ds_read_b128 v[70:73], v0 offset:3072
	v_add_u32_e32 v0, s85, v173
	ds_read_b128 v[162:165], v0
	ds_read_b128 v[166:169], v0 offset:1024
	ds_read_b128 v[190:193], v0 offset:2048
	ds_read_b128 v[198:201], v0 offset:3072
	s_add_u32 s68, s68, 0x80000
	s_addc_u32 s69, s69, 0
	s_mov_b32 m0, s86
	v_lshl_add_u64 v[182:183], s[68:69], 0, v[146:147]
	ds_read_b128 v[202:205], v175 offset:32768
	ds_read_b128 v[206:209], v175 offset:33792
	ds_read_b128 v[210:213], v175 offset:34816
	ds_read_b128 v[214:217], v175 offset:35840
	ds_read_b128 v[236:239], v175 offset:36864
	ds_read_b128 v[240:243], v175 offset:37888
	ds_read_b128 v[244:247], v175 offset:38912
	ds_read_b128 v[248:251], v175 offset:39936
	global_load_lds_dwordx4 v[182:183], off
	v_lshl_add_u64 v[182:183], s[68:69], 0, v[150:151]
	s_mov_b32 m0, s87
	s_nop 0
	global_load_lds_dwordx4 v[182:183], off
	s_waitcnt vmcnt(8)
	s_waitcnt lgkmcnt(0)
	s_barrier
	s_setprio 1
	s_waitcnt lgkmcnt(0)
	v_mfma_f32_16x16x32_bf16 v[142:145], v[58:61], v[202:205], v[142:145]
	v_mfma_f32_16x16x32_bf16 v[138:141], v[66:69], v[202:205], v[138:141]
	v_mfma_f32_16x16x32_bf16 v[122:125], v[66:69], v[210:213], v[122:125]
	v_mfma_f32_16x16x32_bf16 v[126:129], v[58:61], v[210:213], v[126:129]
	v_mfma_f32_16x16x32_bf16 v[110:113], v[58:61], v[236:239], v[110:113]
	v_mfma_f32_16x16x32_bf16 v[106:109], v[66:69], v[236:239], v[106:109]
	v_mfma_f32_16x16x32_bf16 v[90:93], v[66:69], v[244:247], v[90:93]
	v_mfma_f32_16x16x32_bf16 v[94:97], v[58:61], v[244:247], v[94:97]
	v_mfma_f32_16x16x32_bf16 v[142:145], v[62:65], v[206:209], v[142:145]
	v_mfma_f32_16x16x32_bf16 v[138:141], v[70:73], v[206:209], v[138:141]
	v_mfma_f32_16x16x32_bf16 v[122:125], v[70:73], v[214:217], v[122:125]
	v_mfma_f32_16x16x32_bf16 v[126:129], v[62:65], v[214:217], v[126:129]
	v_mfma_f32_16x16x32_bf16 v[110:113], v[62:65], v[240:243], v[110:113]
	v_mfma_f32_16x16x32_bf16 v[106:109], v[70:73], v[240:243], v[106:109]
	v_mfma_f32_16x16x32_bf16 v[90:93], v[70:73], v[248:251], v[90:93]
	v_mfma_f32_16x16x32_bf16 v[94:97], v[62:65], v[248:251], v[94:97]
	s_setprio 0
	s_setprio 1
	v_mfma_f32_16x16x32_bf16 v[134:137], v[162:165], v[202:205], v[134:137]
	v_mfma_f32_16x16x32_bf16 v[130:133], v[190:193], v[202:205], v[130:133]
	v_mfma_f32_16x16x32_bf16 v[114:117], v[190:193], v[210:213], v[114:117]
	v_mfma_f32_16x16x32_bf16 v[118:121], v[162:165], v[210:213], v[118:121]
	v_mfma_f32_16x16x32_bf16 v[102:105], v[162:165], v[236:239], v[102:105]
	v_mfma_f32_16x16x32_bf16 v[98:101], v[190:193], v[236:239], v[98:101]
	v_mfma_f32_16x16x32_bf16 v[82:85], v[190:193], v[244:247], v[82:85]
	v_mfma_f32_16x16x32_bf16 v[86:89], v[162:165], v[244:247], v[86:89]
	v_mfma_f32_16x16x32_bf16 v[134:137], v[166:169], v[206:209], v[134:137]
	v_mfma_f32_16x16x32_bf16 v[130:133], v[198:201], v[206:209], v[130:133]
	v_mfma_f32_16x16x32_bf16 v[114:117], v[198:201], v[214:217], v[114:117]
	v_mfma_f32_16x16x32_bf16 v[118:121], v[166:169], v[214:217], v[118:121]
	s_setprio 0
	v_mfma_f32_16x16x32_bf16 v[102:105], v[166:169], v[240:243], v[102:105]
	v_mfma_f32_16x16x32_bf16 v[98:101], v[198:201], v[240:243], v[98:101]
	v_mfma_f32_16x16x32_bf16 v[82:85], v[198:201], v[248:251], v[82:85]
	v_mfma_f32_16x16x32_bf16 v[86:89], v[166:169], v[248:251], v[86:89]
	s_barrier
; #define PG8_STAGE(bufoff, gbase, voff) do { _Pragma("unroll") for (int _i = 0; _i < 2; ++_i) \
;         __builtin_amdgcn_global_load_lds((const unsigned*)((const char*)(gbase) + (voff)[_i]), (PG8_LAS unsigned*)(lds + (bufoff) + ldsw + _i * 8192), 16, 0, 0); } while (0)
; #define PG8_WAIT_V(n) asm volatile("s_waitcnt vmcnt(" #n ")" ::: "memory")
; #define PG8_WAIT_L(n) asm volatile("s_waitcnt lgkmcnt(" #n ")" ::: "memory")
; #define PG8_BAR __builtin_amdgcn_s_barrier()
; #define PG8_SCHED __builtin_amdgcn_sched_barrier(0)
; template <class Epi, class Sched, bool ALIGN_EPI, bool F8 = false>
; __device__ __forceinline__ void gemm_phase(PG8_LAS unsigned char* lds, const Gemm g, const Sched& S, const Epi& E, int tid) {
;     ...
;             PG8_LDA(At, 1, 1); PG8_STAGE(PG8_SB(1, 0), b3, voffB); PG8_STAGE(PG8_SB(1, 1), b3 + hstepB, voffB); PG8_STAGE(PG8_SA(1, 0), a3, voffA);
;             PG8_WAIT_V(8); PG8_WAIT_L(0); PG8_BAR; PG8_MMA(1, 0, At, B0); PG8_MMA(1, 1, At, B1); PG8_BAR; PG8_SCHED;
;         }
;         if constexpr (ALIGN_EPI) { if (wr == 0) PG8_BAR; }
	s_add_i32 s68, s84, s0
	v_lshl_add_u64 v[170:171], v[170:171], 0, s[60:61]
	s_mov_b32 m0, s68
	ds_read_b128 v[202:205], v175 offset:49152
	ds_read_b128 v[206:209], v175 offset:50176
	ds_read_b128 v[210:213], v175 offset:51200
	ds_read_b128 v[214:217], v175 offset:52224
	ds_read_b128 v[236:239], v175 offset:53248
	ds_read_b128 v[240:243], v175 offset:54272
	ds_read_b128 v[244:247], v175 offset:55296
	ds_read_b128 v[248:251], v175 offset:56320
	global_load_lds_dwordx4 v[170:171], off
	s_add_i32 m0, s68, 0x2000
	s_add_u32 s14, s14, 0x80080
	v_lshl_add_u64 v[170:171], v[176:177], 0, s[60:61]
	s_addc_u32 s15, s15, 0
	s_add_i32 s68, s85, s0
	global_load_lds_dwordx4 v[170:171], off
	v_lshl_add_u64 v[170:171], s[14:15], 0, v[148:149]
	s_mov_b32 m0, s68
	s_nop 0
	global_load_lds_dwordx4 v[170:171], off
	v_lshl_add_u64 v[170:171], s[14:15], 0, v[152:153]
	s_add_i32 m0, s68, 0x2000
	s_nop 0
	global_load_lds_dwordx4 v[170:171], off
	v_lshl_add_u64 v[170:171], v[178:179], 0, s[60:61]
	s_mov_b32 m0, s88
	s_nop 0
	global_load_lds_dwordx4 v[170:171], off
	v_lshl_add_u64 v[170:171], v[180:181], 0, s[60:61]
	s_mov_b32 m0, s89
	s_nop 0
	global_load_lds_dwordx4 v[170:171], off
	s_waitcnt vmcnt(8)
	s_waitcnt lgkmcnt(0)
	s_barrier
	s_setprio 1
	s_waitcnt lgkmcnt(0)
	v_mfma_f32_16x16x32_bf16 v[78:81], v[58:61], v[202:205], v[78:81]
	v_mfma_f32_16x16x32_bf16 v[74:77], v[66:69], v[202:205], v[74:77]
	v_mfma_f32_16x16x32_bf16 v[42:45], v[66:69], v[210:213], v[42:45]
	v_mfma_f32_16x16x32_bf16 v[46:49], v[58:61], v[210:213], v[46:49]
	v_mfma_f32_16x16x32_bf16 v[30:33], v[58:61], v[236:239], v[30:33]
	v_mfma_f32_16x16x32_bf16 v[26:29], v[66:69], v[236:239], v[26:29]
	v_mfma_f32_16x16x32_bf16 v[10:13], v[66:69], v[244:247], v[10:13]
	v_mfma_f32_16x16x32_bf16 v[14:17], v[58:61], v[244:247], v[14:17]
	v_mfma_f32_16x16x32_bf16 v[78:81], v[62:65], v[206:209], v[78:81]
	v_mfma_f32_16x16x32_bf16 v[74:77], v[70:73], v[206:209], v[74:77]
	v_mfma_f32_16x16x32_bf16 v[42:45], v[70:73], v[214:217], v[42:45]
	v_mfma_f32_16x16x32_bf16 v[46:49], v[62:65], v[214:217], v[46:49]
	v_mfma_f32_16x16x32_bf16 v[30:33], v[62:65], v[240:243], v[30:33]
	v_mfma_f32_16x16x32_bf16 v[26:29], v[70:73], v[240:243], v[26:29]
	v_mfma_f32_16x16x32_bf16 v[10:13], v[70:73], v[248:251], v[10:13]
	v_mfma_f32_16x16x32_bf16 v[14:17], v[62:65], v[248:251], v[14:17]
	s_setprio 0
	s_setprio 1
	v_mfma_f32_16x16x32_bf16 v[54:57], v[162:165], v[202:205], v[54:57]
	v_mfma_f32_16x16x32_bf16 v[50:53], v[190:193], v[202:205], v[50:53]
	v_mfma_f32_16x16x32_bf16 v[34:37], v[190:193], v[210:213], v[34:37]
	v_mfma_f32_16x16x32_bf16 v[38:41], v[162:165], v[210:213], v[38:41]
	v_mfma_f32_16x16x32_bf16 v[22:25], v[162:165], v[236:239], v[22:25]
	v_mfma_f32_16x16x32_bf16 v[18:21], v[190:193], v[236:239], v[18:21]
	v_mfma_f32_16x16x32_bf16 v[2:5], v[190:193], v[244:247], v[2:5]
	v_mfma_f32_16x16x32_bf16 v[6:9], v[162:165], v[244:247], v[6:9]
	v_mfma_f32_16x16x32_bf16 v[58:61], v[166:169], v[206:209], v[54:57]
	v_mfma_f32_16x16x32_bf16 v[50:53], v[198:201], v[206:209], v[50:53]
	v_mfma_f32_16x16x32_bf16 v[34:37], v[198:201], v[214:217], v[34:37]
	v_mfma_f32_16x16x32_bf16 v[38:41], v[166:169], v[214:217], v[38:41]
	s_setprio 0
	v_mfma_f32_16x16x32_bf16 v[22:25], v[166:169], v[240:243], v[22:25]
	v_mfma_f32_16x16x32_bf16 v[18:21], v[198:201], v[240:243], v[18:21]
	v_mfma_f32_16x16x32_bf16 v[2:5], v[198:201], v[248:251], v[2:5]
	v_mfma_f32_16x16x32_bf16 v[6:9], v[166:169], v[248:251], v[6:9]
	s_barrier
	s_add_i32 s83, s83, 2
	s_add_u32 s50, s50, 0x100
	s_addc_u32 s51, s51, 0
	s_add_u32 s45, s45, 0x100
	s_addc_u32 s82, s82, 0
	s_cmp_gt_u32 s83, 29
	s_cbranch_scc0 .LBB0_739
	s_and_b64 vcc, exec, s[20:21]
	s_cbranch_vccz .LBB0_742
	s_barrier

; #define PG8_STAGE(bufoff, gbase, voff) do { _Pragma("unroll") for (int _i = 0; _i < 2; ++_i) \
;         __builtin_amdgcn_global_load_lds((const unsigned*)((const char*)(gbase) + (voff)[_i]), (PG8_LAS unsigned*)(lds + (bufoff) + ldsw + _i * 8192), 16, 0, 0); } while (0)
; #define PG8_WAIT_V(n) asm volatile("s_waitcnt vmcnt(" #n ")" ::: "memory")
; #define PG8_WAIT_L(n) asm volatile("s_waitcnt lgkmcnt(" #n ")" ::: "memory")
; #define PG8_BAR __builtin_amdgcn_s_barrier()
; #define PG8_SCHED __builtin_amdgcn_sched_barrier(0)
; template <class Epi, class Sched, bool ALIGN_EPI, bool F8 = false>
; __device__ __forceinline__ void gemm_phase(PG8_LAS unsigned char* lds, const Gemm g, const Sched& S, const Epi& E, int tid) {
;     ...
;             const bool last = (t == nt - 2);
;             const char* a1 = cA + (size_t)(t + 1) * kstep;
;             const char* a2 = last ? nA : cA + (size_t)(t + 2) * kstep; const char* b2 = last ? nB : cB + (size_t)(t + 2) * kstep;
;             const char* a3 = a2 + kstep; const char* b3 = b2 + kstep;
;             if (last && has_next) S.a_ready(nxt);
;             PG8_LDB(B0, 0, 0); PG8_LDB(B1, 0, 1); PG8_SCHED; PG8_LDA(At, 0, 0); PG8_STAGE(PG8_SA(1, 1), a1 + hstepA, voffA);
;             PG8_WAIT_V(8); PG8_WAIT_L(0); PG8_BAR; PG8_MMA(0, 0, At, B0); PG8_MMA(0, 1, At, B1); PG8_BAR; PG8_SCHED;
;             PG8_LDA(At, 0, 1); PG8_STAGE(PG8_SB(0, 0), b2, voffB); PG8_STAGE(PG8_SB(0, 1), b2 + hstepB, voffB); PG8_STAGE(PG8_SA(0, 0), a2, voffA);
.LBB0_1057:
	s_add_u32 s24, s22, 0x100
	s_addc_u32 s25, s23, 0
	s_add_i32 s50, 0, 0x10000
	s_cmp_eq_u32 vcc_hi, 4
	s_cselect_b32 s29, s19, s25
	s_cselect_b32 s28, s18, s24
	v_add_u32_e32 v140, s50, v144
	s_cselect_b32 s27, s13, vcc_lo
	s_cselect_b32 s26, s84, s85
	s_add_i32 s51, 0, 0x14000
	ds_read_b128 v[148:151], v140
	ds_read_b128 v[152:155], v140 offset:1024
	ds_read_b128 v[156:159], v140 offset:2048
	ds_read_b128 v[160:163], v140 offset:3072
	v_add_u32_e32 v140, s51, v144
	ds_read_b128 v[164:167], v140
	ds_read_b128 v[168:171], v140 offset:1024
	ds_read_b128 v[172:175], v140 offset:2048
	ds_read_b128 v[190:193], v140 offset:3072
	v_lshl_add_u64 v[142:143], s[22:23], 0, v[136:137]
	s_add_i32 m0, s17, 0xc000
	ds_read_b128 v[194:197], v146
	ds_read_b128 v[198:201], v146 offset:1024
	ds_read_b128 v[202:205], v146 offset:2048
	ds_read_b128 v[206:209], v146 offset:3072
	ds_read_b128 v[210:213], v146 offset:4096
	ds_read_b128 v[214:217], v146 offset:5120
	ds_read_b128 v[236:239], v146 offset:6144
	ds_read_b128 v[240:243], v146 offset:7168
	global_load_lds_dwordx4 v[142:143], off
	v_lshl_add_u64 v[142:143], s[22:23], 0, v[138:139]
	s_add_i32 m0, s17, 0xe000
	s_nop 0
	global_load_lds_dwordx4 v[142:143], off
	s_waitcnt vmcnt(8)
	s_waitcnt lgkmcnt(0)
	s_barrier
	s_setprio 1
	s_waitcnt lgkmcnt(0)
	v_mfma_f32_16x16x32_bf16 v[126:129], v[148:151], v[194:197], v[126:129]
	v_mfma_f32_16x16x32_bf16 v[122:125], v[156:159], v[194:197], v[122:125]
	v_mfma_f32_16x16x32_bf16 v[106:109], v[156:159], v[202:205], v[106:109]
	v_mfma_f32_16x16x32_bf16 v[114:117], v[148:151], v[202:205], v[114:117]
	v_mfma_f32_16x16x32_bf16 v[98:101], v[148:151], v[210:213], v[98:101]
	v_mfma_f32_16x16x32_bf16 v[90:93], v[156:159], v[210:213], v[90:93]
	v_mfma_f32_16x16x32_bf16 v[74:77], v[156:159], v[236:239], v[74:77]
	v_mfma_f32_16x16x32_bf16 v[82:85], v[148:151], v[236:239], v[82:85]
	v_mfma_f32_16x16x32_bf16 v[126:129], v[152:155], v[198:201], v[126:129]
	v_mfma_f32_16x16x32_bf16 v[122:125], v[160:163], v[198:201], v[122:125]
	v_mfma_f32_16x16x32_bf16 v[106:109], v[160:163], v[206:209], v[106:109]
	v_mfma_f32_16x16x32_bf16 v[114:117], v[152:155], v[206:209], v[114:117]
	v_mfma_f32_16x16x32_bf16 v[98:101], v[152:155], v[214:217], v[98:101]
	v_mfma_f32_16x16x32_bf16 v[90:93], v[160:163], v[214:217], v[90:93]
	v_mfma_f32_16x16x32_bf16 v[74:77], v[160:163], v[240:243], v[74:77]
	v_mfma_f32_16x16x32_bf16 v[82:85], v[152:155], v[240:243], v[82:85]
	s_setprio 0
	s_setprio 1
	v_mfma_f32_16x16x32_bf16 v[118:121], v[164:167], v[194:197], v[118:121]
	v_mfma_f32_16x16x32_bf16 v[110:113], v[172:175], v[194:197], v[110:113]
	v_mfma_f32_16x16x32_bf16 v[94:97], v[172:175], v[202:205], v[94:97]
	v_mfma_f32_16x16x32_bf16 v[102:105], v[164:167], v[202:205], v[102:105]
	v_mfma_f32_16x16x32_bf16 v[86:89], v[164:167], v[210:213], v[86:89]
	v_mfma_f32_16x16x32_bf16 v[78:81], v[172:175], v[210:213], v[78:81]
	v_mfma_f32_16x16x32_bf16 v[66:69], v[172:175], v[236:239], v[66:69]
	v_mfma_f32_16x16x32_bf16 v[70:73], v[164:167], v[236:239], v[70:73]
	v_mfma_f32_16x16x32_bf16 v[118:121], v[168:171], v[198:201], v[118:121]
	v_mfma_f32_16x16x32_bf16 v[110:113], v[190:193], v[198:201], v[110:113]
	v_mfma_f32_16x16x32_bf16 v[94:97], v[190:193], v[206:209], v[94:97]
	v_mfma_f32_16x16x32_bf16 v[102:105], v[168:171], v[206:209], v[102:105]
	s_setprio 0
	v_mfma_f32_16x16x32_bf16 v[86:89], v[168:171], v[214:217], v[86:89]
	v_mfma_f32_16x16x32_bf16 v[78:81], v[190:193], v[214:217], v[78:81]
	v_mfma_f32_16x16x32_bf16 v[66:69], v[190:193], v[240:243], v[66:69]
	v_mfma_f32_16x16x32_bf16 v[70:73], v[168:171], v[240:243], v[70:73]
	s_barrier
	s_add_i32 s22, s50, s34
	v_lshl_add_u64 v[142:143], s[26:27], 0, v[0:1]
	s_mov_b32 m0, s22
	ds_read_b128 v[194:197], v146 offset:16384
	ds_read_b128 v[198:201], v146 offset:17408
	ds_read_b128 v[202:205], v146 offset:18432
	ds_read_b128 v[206:209], v146 offset:19456
	ds_read_b128 v[210:213], v146 offset:20480
	ds_read_b128 v[214:217], v146 offset:21504
	ds_read_b128 v[236:239], v146 offset:22528
	ds_read_b128 v[240:243], v146 offset:23552
	global_load_lds_dwordx4 v[142:143], off
	s_add_i32 m0, s22, 0x2000
	s_add_u32 s22, s26, 0x20000
	v_lshl_add_u64 v[176:177], s[26:27], 0, v[134:135]
	s_addc_u32 s23, s27, 0
	s_add_i32 s50, s51, s34
	global_load_lds_dwordx4 v[176:177], off
	v_lshl_add_u64 v[178:179], s[22:23], 0, v[0:1]
	s_mov_b32 m0, s50
	v_lshl_add_u64 v[180:181], s[28:29], 0, v[132:133]
	global_load_lds_dwordx4 v[178:179], off
	v_lshl_add_u64 v[178:179], s[22:23], 0, v[134:135]
	s_add_i32 m0, s50, 0x2000
	s_nop 0
	global_load_lds_dwordx4 v[178:179], off
	v_lshl_add_u64 v[178:179], s[28:29], 0, v[130:131]
	s_mov_b32 m0, s17
	s_nop 0
	global_load_lds_dwordx4 v[178:179], off
	s_mov_b32 m0, s35
	s_nop 0
	global_load_lds_dwordx4 v[180:181], off
	s_waitcnt vmcnt(8)
	s_waitcnt lgkmcnt(0)
	s_barrier
; #define PG8_STAGE(bufoff, gbase, voff) do { _Pragma("unroll") for (int _i = 0; _i < 2; ++_i) \
;         __builtin_amdgcn_global_load_lds((const unsigned*)((const char*)(gbase) + (voff)[_i]), (PG8_LAS unsigned*)(lds + (bufoff) + ldsw + _i * 8192), 16, 0, 0); } while (0)
; #define PG8_WAIT_V(n) asm volatile("s_waitcnt vmcnt(" #n ")" ::: "memory")
; #define PG8_WAIT_L(n) asm volatile("s_waitcnt lgkmcnt(" #n ")" ::: "memory")
; #define PG8_BAR __builtin_amdgcn_s_barrier()
; #define PG8_SCHED __builtin_amdgcn_sched_barrier(0)
; template <class Epi, class Sched, bool ALIGN_EPI, bool F8 = false>
; __device__ __forceinline__ void gemm_phase(PG8_LAS unsigned char* lds, const Gemm g, const Sched& S, const Epi& E, int tid) {
;     ...
;             PG8_WAIT_V(8); PG8_WAIT_L(0); PG8_BAR; PG8_MMA(1, 0, At, B0); PG8_MMA(1, 1, At, B1); PG8_BAR; PG8_SCHED;
;             PG8_LDB(B0, 1, 0); PG8_LDB(B1, 1, 1); PG8_SCHED; PG8_LDA(At, 1, 0); PG8_STAGE(PG8_SA(0, 1), a2 + hstepA, voffA);
;             PG8_WAIT_V(8); PG8_WAIT_L(0); PG8_BAR; PG8_MMA(0, 0, At, B0); PG8_MMA(0, 1, At, B1); PG8_BAR; PG8_SCHED;
	s_setprio 1
	s_waitcnt lgkmcnt(0)
	v_mfma_f32_16x16x32_bf16 v[62:65], v[148:151], v[194:197], v[62:65]
	v_mfma_f32_16x16x32_bf16 v[58:61], v[156:159], v[194:197], v[58:61]
	v_mfma_f32_16x16x32_bf16 v[42:45], v[156:159], v[202:205], v[42:45]
	v_mfma_f32_16x16x32_bf16 v[50:53], v[148:151], v[202:205], v[50:53]
	v_mfma_f32_16x16x32_bf16 v[34:37], v[148:151], v[210:213], v[34:37]
	v_mfma_f32_16x16x32_bf16 v[26:29], v[156:159], v[210:213], v[26:29]
	v_mfma_f32_16x16x32_bf16 v[10:13], v[156:159], v[236:239], v[10:13]
	v_mfma_f32_16x16x32_bf16 v[18:21], v[148:151], v[236:239], v[18:21]
	v_mfma_f32_16x16x32_bf16 v[62:65], v[152:155], v[198:201], v[62:65]
	v_mfma_f32_16x16x32_bf16 v[58:61], v[160:163], v[198:201], v[58:61]
	v_mfma_f32_16x16x32_bf16 v[42:45], v[160:163], v[206:209], v[42:45]
	v_mfma_f32_16x16x32_bf16 v[50:53], v[152:155], v[206:209], v[50:53]
	v_mfma_f32_16x16x32_bf16 v[34:37], v[152:155], v[214:217], v[34:37]
	v_mfma_f32_16x16x32_bf16 v[26:29], v[160:163], v[214:217], v[26:29]
	v_mfma_f32_16x16x32_bf16 v[10:13], v[160:163], v[240:243], v[10:13]
	v_mfma_f32_16x16x32_bf16 v[18:21], v[152:155], v[240:243], v[18:21]
	s_setprio 0
	s_setprio 1
	v_mfma_f32_16x16x32_bf16 v[54:57], v[164:167], v[194:197], v[54:57]
	v_mfma_f32_16x16x32_bf16 v[46:49], v[172:175], v[194:197], v[46:49]
	v_mfma_f32_16x16x32_bf16 v[30:33], v[172:175], v[202:205], v[30:33]
	v_mfma_f32_16x16x32_bf16 v[38:41], v[164:167], v[202:205], v[38:41]
	v_mfma_f32_16x16x32_bf16 v[22:25], v[164:167], v[210:213], v[22:25]
	v_mfma_f32_16x16x32_bf16 v[14:17], v[172:175], v[210:213], v[14:17]
	v_mfma_f32_16x16x32_bf16 v[2:5], v[172:175], v[236:239], v[2:5]
	v_mfma_f32_16x16x32_bf16 v[6:9], v[164:167], v[236:239], v[6:9]
	v_mfma_f32_16x16x32_bf16 v[54:57], v[168:171], v[198:201], v[54:57]
	v_mfma_f32_16x16x32_bf16 v[46:49], v[190:193], v[198:201], v[46:49]
	v_mfma_f32_16x16x32_bf16 v[30:33], v[190:193], v[206:209], v[30:33]
	v_mfma_f32_16x16x32_bf16 v[38:41], v[168:171], v[206:209], v[38:41]
	s_setprio 0
	v_mfma_f32_16x16x32_bf16 v[22:25], v[168:171], v[214:217], v[22:25]
	v_mfma_f32_16x16x32_bf16 v[14:17], v[190:193], v[214:217], v[14:17]
	v_mfma_f32_16x16x32_bf16 v[2:5], v[190:193], v[240:243], v[2:5]
	v_mfma_f32_16x16x32_bf16 v[6:9], v[168:171], v[240:243], v[6:9]
	s_barrier
	s_add_i32 s50, 0, 0x18000
	v_add_u32_e32 v140, s50, v144
	s_add_i32 s51, 0, 0x1c000
	ds_read_b128 v[148:151], v140
	ds_read_b128 v[152:155], v140 offset:1024
	ds_read_b128 v[156:159], v140 offset:2048
	ds_read_b128 v[160:163], v140 offset:3072
	v_add_u32_e32 v140, s51, v144
	ds_read_b128 v[164:167], v140
	ds_read_b128 v[168:171], v140 offset:1024
	ds_read_b128 v[172:175], v140 offset:2048
	ds_read_b128 v[190:193], v140 offset:3072
	s_add_u32 s22, s28, 0x110000
	s_addc_u32 s23, s29, 0
	s_mov_b32 m0, s38
	v_lshl_add_u64 v[182:183], s[22:23], 0, v[130:131]
	ds_read_b128 v[194:197], v146 offset:32768
	ds_read_b128 v[198:201], v146 offset:33792
	ds_read_b128 v[202:205], v146 offset:34816
	ds_read_b128 v[206:209], v146 offset:35840
	ds_read_b128 v[210:213], v146 offset:36864
	ds_read_b128 v[214:217], v146 offset:37888
	ds_read_b128 v[236:239], v146 offset:38912
	ds_read_b128 v[240:243], v146 offset:39936
	global_load_lds_dwordx4 v[182:183], off
	v_lshl_add_u64 v[182:183], s[22:23], 0, v[132:133]
	s_mov_b32 m0, s39
	s_nop 0
	global_load_lds_dwordx4 v[182:183], off
	s_waitcnt vmcnt(8)
	s_waitcnt lgkmcnt(0)
	s_barrier
	s_setprio 1
	s_waitcnt lgkmcnt(0)
	v_mfma_f32_16x16x32_bf16 v[126:129], v[148:151], v[194:197], v[126:129]
	v_mfma_f32_16x16x32_bf16 v[122:125], v[156:159], v[194:197], v[122:125]
	v_mfma_f32_16x16x32_bf16 v[106:109], v[156:159], v[202:205], v[106:109]
	v_mfma_f32_16x16x32_bf16 v[114:117], v[148:151], v[202:205], v[114:117]
	v_mfma_f32_16x16x32_bf16 v[98:101], v[148:151], v[210:213], v[98:101]
	v_mfma_f32_16x16x32_bf16 v[90:93], v[156:159], v[210:213], v[90:93]
	v_mfma_f32_16x16x32_bf16 v[74:77], v[156:159], v[236:239], v[74:77]
	v_mfma_f32_16x16x32_bf16 v[82:85], v[148:151], v[236:239], v[82:85]
	v_mfma_f32_16x16x32_bf16 v[126:129], v[152:155], v[198:201], v[126:129]
	v_mfma_f32_16x16x32_bf16 v[122:125], v[160:163], v[198:201], v[122:125]
	v_mfma_f32_16x16x32_bf16 v[106:109], v[160:163], v[206:209], v[106:109]
	v_mfma_f32_16x16x32_bf16 v[114:117], v[152:155], v[206:209], v[114:117]
	v_mfma_f32_16x16x32_bf16 v[98:101], v[152:155], v[214:217], v[98:101]
	v_mfma_f32_16x16x32_bf16 v[90:93], v[160:163], v[214:217], v[90:93]
	v_mfma_f32_16x16x32_bf16 v[74:77], v[160:163], v[240:243], v[74:77]
	v_mfma_f32_16x16x32_bf16 v[82:85], v[152:155], v[240:243], v[82:85]
	s_setprio 0
	s_setprio 1
	v_mfma_f32_16x16x32_bf16 v[118:121], v[164:167], v[194:197], v[118:121]
	v_mfma_f32_16x16x32_bf16 v[110:113], v[172:175], v[194:197], v[110:113]
	v_mfma_f32_16x16x32_bf16 v[94:97], v[172:175], v[202:205], v[94:97]
	v_mfma_f32_16x16x32_bf16 v[102:105], v[164:167], v[202:205], v[102:105]
	v_mfma_f32_16x16x32_bf16 v[86:89], v[164:167], v[210:213], v[86:89]
	v_mfma_f32_16x16x32_bf16 v[78:81], v[172:175], v[210:213], v[78:81]
	v_mfma_f32_16x16x32_bf16 v[66:69], v[172:175], v[236:239], v[66:69]
	v_mfma_f32_16x16x32_bf16 v[70:73], v[164:167], v[236:239], v[70:73]
	v_mfma_f32_16x16x32_bf16 v[118:121], v[168:171], v[198:201], v[118:121]
	v_mfma_f32_16x16x32_bf16 v[110:113], v[190:193], v[198:201], v[110:113]
	v_mfma_f32_16x16x32_bf16 v[94:97], v[190:193], v[206:209], v[94:97]
	v_mfma_f32_16x16x32_bf16 v[102:105], v[168:171], v[206:209], v[102:105]
	s_setprio 0
	v_mfma_f32_16x16x32_bf16 v[86:89], v[168:171], v[214:217], v[86:89]
	v_mfma_f32_16x16x32_bf16 v[78:81], v[190:193], v[214:217], v[78:81]
	v_mfma_f32_16x16x32_bf16 v[66:69], v[190:193], v[240:243], v[66:69]
	v_mfma_f32_16x16x32_bf16 v[70:73], v[168:171], v[240:243], v[70:73]
	s_barrier
; #define PG8_STAGE(bufoff, gbase, voff) do { _Pragma("unroll") for (int _i = 0; _i < 2; ++_i) \
;         __builtin_amdgcn_global_load_lds((const unsigned*)((const char*)(gbase) + (voff)[_i]), (PG8_LAS unsigned*)(lds + (bufoff) + ldsw + _i * 8192), 16, 0, 0); } while (0)
; #define PG8_WAIT_V(n) asm volatile("s_waitcnt vmcnt(" #n ")" ::: "memory")
; #define PG8_WAIT_L(n) asm volatile("s_waitcnt lgkmcnt(" #n ")" ::: "memory")
; #define PG8_BAR __builtin_amdgcn_s_barrier()
; #define PG8_SCHED __builtin_amdgcn_sched_barrier(0)
; template <class Epi, class Sched, bool ALIGN_EPI, bool F8 = false>
; __device__ __forceinline__ void gemm_phase(PG8_LAS unsigned char* lds, const Gemm g, const Sched& S, const Epi& E, int tid) {
;     ...
;             PG8_LDA(At, 1, 1); PG8_STAGE(PG8_SB(1, 0), b3, voffB); PG8_STAGE(PG8_SB(1, 1), b3 + hstepB, voffB); PG8_STAGE(PG8_SA(1, 0), a3, voffA);
;             PG8_WAIT_V(8); PG8_WAIT_L(0); PG8_BAR; PG8_MMA(1, 0, At, B0); PG8_MMA(1, 1, At, B1); PG8_BAR; PG8_SCHED;
;         }
;         if constexpr (ALIGN_EPI) { if (wr == 0) PG8_BAR; }
	s_add_i32 s22, s50, s34
	v_lshl_add_u64 v[142:143], v[142:143], 0, s[60:61]
	s_mov_b32 m0, s22
	ds_read_b128 v[194:197], v146 offset:49152
	ds_read_b128 v[198:201], v146 offset:50176
	ds_read_b128 v[202:205], v146 offset:51200
	ds_read_b128 v[206:209], v146 offset:52224
	ds_read_b128 v[210:213], v146 offset:53248
	ds_read_b128 v[214:217], v146 offset:54272
	ds_read_b128 v[236:239], v146 offset:55296
	ds_read_b128 v[240:243], v146 offset:56320
	global_load_lds_dwordx4 v[142:143], off
	s_add_i32 m0, s22, 0x2000
	s_add_u32 s22, s26, 0x20080
	v_lshl_add_u64 v[142:143], v[176:177], 0, s[60:61]
	s_addc_u32 s23, s27, 0
	s_add_i32 s26, s51, s34
	global_load_lds_dwordx4 v[142:143], off
	v_lshl_add_u64 v[142:143], s[22:23], 0, v[0:1]
	s_mov_b32 m0, s26
	s_nop 0
	global_load_lds_dwordx4 v[142:143], off
	v_lshl_add_u64 v[142:143], s[22:23], 0, v[134:135]
	s_add_i32 m0, s26, 0x2000
	s_nop 0
	global_load_lds_dwordx4 v[142:143], off
	v_lshl_add_u64 v[142:143], v[178:179], 0, s[60:61]
	s_mov_b32 m0, s82
	s_nop 0
	global_load_lds_dwordx4 v[142:143], off
	v_lshl_add_u64 v[142:143], v[180:181], 0, s[60:61]
	s_mov_b32 m0, s83
	s_nop 0
	global_load_lds_dwordx4 v[142:143], off
	s_waitcnt vmcnt(8)
	s_waitcnt lgkmcnt(0)
	s_barrier
	s_setprio 1
	s_waitcnt lgkmcnt(0)
	v_mfma_f32_16x16x32_bf16 v[62:65], v[148:151], v[194:197], v[62:65]
	v_mfma_f32_16x16x32_bf16 v[58:61], v[156:159], v[194:197], v[58:61]
	v_mfma_f32_16x16x32_bf16 v[42:45], v[156:159], v[202:205], v[42:45]
	v_mfma_f32_16x16x32_bf16 v[50:53], v[148:151], v[202:205], v[50:53]
	v_mfma_f32_16x16x32_bf16 v[34:37], v[148:151], v[210:213], v[34:37]
	v_mfma_f32_16x16x32_bf16 v[26:29], v[156:159], v[210:213], v[26:29]
	v_mfma_f32_16x16x32_bf16 v[10:13], v[156:159], v[236:239], v[10:13]
	v_mfma_f32_16x16x32_bf16 v[18:21], v[148:151], v[236:239], v[18:21]
	v_mfma_f32_16x16x32_bf16 v[62:65], v[152:155], v[198:201], v[62:65]
	v_mfma_f32_16x16x32_bf16 v[58:61], v[160:163], v[198:201], v[58:61]
	v_mfma_f32_16x16x32_bf16 v[42:45], v[160:163], v[206:209], v[42:45]
	v_mfma_f32_16x16x32_bf16 v[50:53], v[152:155], v[206:209], v[50:53]
	v_mfma_f32_16x16x32_bf16 v[34:37], v[152:155], v[214:217], v[34:37]
	v_mfma_f32_16x16x32_bf16 v[26:29], v[160:163], v[214:217], v[26:29]
	v_mfma_f32_16x16x32_bf16 v[10:13], v[160:163], v[240:243], v[10:13]
	v_mfma_f32_16x16x32_bf16 v[18:21], v[152:155], v[240:243], v[18:21]
	s_setprio 0
	s_setprio 1
	v_mfma_f32_16x16x32_bf16 v[54:57], v[164:167], v[194:197], v[54:57]
	v_mfma_f32_16x16x32_bf16 v[46:49], v[172:175], v[194:197], v[46:49]
	v_mfma_f32_16x16x32_bf16 v[30:33], v[172:175], v[202:205], v[30:33]
	v_mfma_f32_16x16x32_bf16 v[38:41], v[164:167], v[202:205], v[38:41]
	v_mfma_f32_16x16x32_bf16 v[22:25], v[164:167], v[210:213], v[22:25]
	v_mfma_f32_16x16x32_bf16 v[14:17], v[172:175], v[210:213], v[14:17]
	v_mfma_f32_16x16x32_bf16 v[2:5], v[172:175], v[236:239], v[2:5]
	v_mfma_f32_16x16x32_bf16 v[6:9], v[164:167], v[236:239], v[6:9]
	v_mfma_f32_16x16x32_bf16 v[54:57], v[168:171], v[198:201], v[54:57]
	v_mfma_f32_16x16x32_bf16 v[46:49], v[190:193], v[198:201], v[46:49]
	v_mfma_f32_16x16x32_bf16 v[30:33], v[190:193], v[206:209], v[30:33]
	v_mfma_f32_16x16x32_bf16 v[38:41], v[168:171], v[206:209], v[38:41]
	s_setprio 0
	v_mfma_f32_16x16x32_bf16 v[22:25], v[168:171], v[214:217], v[22:25]
	v_mfma_f32_16x16x32_bf16 v[14:17], v[190:193], v[214:217], v[14:17]
	v_mfma_f32_16x16x32_bf16 v[2:5], v[190:193], v[240:243], v[2:5]
	v_mfma_f32_16x16x32_bf16 v[6:9], v[168:171], v[240:243], v[6:9]
	s_barrier
	s_add_i32 vcc_hi, vcc_hi, 2
	s_add_u32 s85, s85, 0x100
	s_addc_u32 vcc_lo, vcc_lo, 0
	s_cmp_gt_u32 vcc_hi, 5
	s_mov_b64 s[22:23], s[24:25]
	s_cbranch_scc0 .LBB0_1057
	s_and_b64 vcc, exec, s[8:9]
	s_cbranch_vccz .LBB0_1060
	s_barrier

; #define PG8_STAGE(bufoff, gbase, voff) do { _Pragma("unroll") for (int _i = 0; _i < 2; ++_i) \
;         __builtin_amdgcn_global_load_lds((const unsigned*)((const char*)(gbase) + (voff)[_i]), (PG8_LAS unsigned*)(lds + (bufoff) + ldsw + _i * 8192), 16, 0, 0); } while (0)
; #define PG8_WAIT_V(n) asm volatile("s_waitcnt vmcnt(" #n ")" ::: "memory")
; #define PG8_WAIT_L(n) asm volatile("s_waitcnt lgkmcnt(" #n ")" ::: "memory")
; #define PG8_BAR __builtin_amdgcn_s_barrier()
; #define PG8_SCHED __builtin_amdgcn_sched_barrier(0)
; template <class Epi, class Sched, bool ALIGN_EPI, bool F8 = false>
; __device__ __forceinline__ void gemm_phase(PG8_LAS unsigned char* lds, const Gemm g, const Sched& S, const Epi& E, int tid) {
;     ...
;             const bool last = (t == nt - 2);
;             const char* a1 = cA + (size_t)(t + 1) * kstep;
;             const char* a2 = last ? nA : cA + (size_t)(t + 2) * kstep; const char* b2 = last ? nB : cB + (size_t)(t + 2) * kstep;
;             const char* a3 = a2 + kstep; const char* b3 = b2 + kstep;
;             if (last && has_next) S.a_ready(nxt);
;             PG8_LDB(B0, 0, 0); PG8_LDB(B1, 0, 1); PG8_SCHED; PG8_LDA(At, 0, 0); PG8_STAGE(PG8_SA(1, 1), a1 + hstepA, voffA);
;             PG8_WAIT_V(8); PG8_WAIT_L(0); PG8_BAR; PG8_MMA(0, 0, At, B0); PG8_MMA(0, 1, At, B1); PG8_BAR; PG8_SCHED;
;             PG8_LDA(At, 0, 1); PG8_STAGE(PG8_SB(0, 0), b2, voffB); PG8_STAGE(PG8_SB(0, 1), b2 + hstepB, voffB); PG8_STAGE(PG8_SA(0, 0), a2, voffA);
.LBB0_1147:
	s_add_u32 s24, s22, 0xfff00080
	s_addc_u32 s25, s23, -1
	s_add_i32 s88, 0, 0x10000
	s_cmp_eq_u32 s87, 4
	s_cselect_b32 s27, s83, s25
	s_cselect_b32 s26, s84, s24
	v_add_u32_e32 v144, s88, v145
	s_cselect_b32 s25, s11, s86
	s_cselect_b32 s24, s13, s85
	s_add_i32 s94, 0, 0x14000
	ds_read_b128 v[150:153], v144
	ds_read_b128 v[154:157], v144 offset:1024
	ds_read_b128 v[158:161], v144 offset:2048
	ds_read_b128 v[162:165], v144 offset:3072
	v_add_u32_e32 v144, s94, v145
	ds_read_b128 v[166:169], v144
	ds_read_b128 v[170:173], v144 offset:1024
	ds_read_b128 v[174:177], v144 offset:2048
	ds_read_b128 v[178:181], v144 offset:3072
	v_lshl_add_u64 v[146:147], s[22:23], 0, v[140:141]
	s_add_i32 m0, s31, 0xc000
	ds_read_b128 v[182:185], v148
	ds_read_b128 v[186:189], v148 offset:1024
	ds_read_b128 v[190:193], v148 offset:2048
	ds_read_b128 v[194:197], v148 offset:3072
	ds_read_b128 v[198:201], v148 offset:4096
	ds_read_b128 v[202:205], v148 offset:5120
	ds_read_b128 v[206:209], v148 offset:6144
	ds_read_b128 v[210:213], v148 offset:7168
	global_load_lds_dwordx4 v[146:147], off
	v_lshl_add_u64 v[146:147], s[22:23], 0, v[142:143]
	s_add_i32 m0, s31, 0xe000
	s_nop 0
	global_load_lds_dwordx4 v[146:147], off
	s_waitcnt vmcnt(8)
	s_waitcnt lgkmcnt(0)
	s_barrier
	s_setprio 1
	s_waitcnt lgkmcnt(0)
	v_mfma_f32_16x16x32_bf16 v[126:129], v[150:153], v[182:185], v[126:129]
	v_mfma_f32_16x16x32_bf16 v[122:125], v[158:161], v[182:185], v[122:125]
	v_mfma_f32_16x16x32_bf16 v[106:109], v[158:161], v[190:193], v[106:109]
	v_mfma_f32_16x16x32_bf16 v[114:117], v[150:153], v[190:193], v[114:117]
	v_mfma_f32_16x16x32_bf16 v[98:101], v[150:153], v[198:201], v[98:101]
	v_mfma_f32_16x16x32_bf16 v[90:93], v[158:161], v[198:201], v[90:93]
	v_mfma_f32_16x16x32_bf16 v[74:77], v[158:161], v[206:209], v[74:77]
	v_mfma_f32_16x16x32_bf16 v[82:85], v[150:153], v[206:209], v[82:85]
	v_mfma_f32_16x16x32_bf16 v[126:129], v[154:157], v[186:189], v[126:129]
	v_mfma_f32_16x16x32_bf16 v[122:125], v[162:165], v[186:189], v[122:125]
	v_mfma_f32_16x16x32_bf16 v[106:109], v[162:165], v[194:197], v[106:109]
	v_mfma_f32_16x16x32_bf16 v[114:117], v[154:157], v[194:197], v[114:117]
	v_mfma_f32_16x16x32_bf16 v[98:101], v[154:157], v[202:205], v[98:101]
	v_mfma_f32_16x16x32_bf16 v[90:93], v[162:165], v[202:205], v[90:93]
	v_mfma_f32_16x16x32_bf16 v[74:77], v[162:165], v[210:213], v[74:77]
	v_mfma_f32_16x16x32_bf16 v[82:85], v[154:157], v[210:213], v[82:85]
	s_setprio 0
	s_setprio 1
	v_mfma_f32_16x16x32_bf16 v[118:121], v[166:169], v[182:185], v[118:121]
	v_mfma_f32_16x16x32_bf16 v[110:113], v[174:177], v[182:185], v[110:113]
	v_mfma_f32_16x16x32_bf16 v[94:97], v[174:177], v[190:193], v[94:97]
	v_mfma_f32_16x16x32_bf16 v[102:105], v[166:169], v[190:193], v[102:105]
	v_mfma_f32_16x16x32_bf16 v[86:89], v[166:169], v[198:201], v[86:89]
	v_mfma_f32_16x16x32_bf16 v[78:81], v[174:177], v[198:201], v[78:81]
	v_mfma_f32_16x16x32_bf16 v[66:69], v[174:177], v[206:209], v[66:69]
	v_mfma_f32_16x16x32_bf16 v[70:73], v[166:169], v[206:209], v[70:73]
	v_mfma_f32_16x16x32_bf16 v[118:121], v[170:173], v[186:189], v[118:121]
	v_mfma_f32_16x16x32_bf16 v[110:113], v[178:181], v[186:189], v[110:113]
	v_mfma_f32_16x16x32_bf16 v[94:97], v[178:181], v[194:197], v[94:97]
	v_mfma_f32_16x16x32_bf16 v[102:105], v[170:173], v[194:197], v[102:105]
	s_setprio 0
	v_mfma_f32_16x16x32_bf16 v[86:89], v[170:173], v[202:205], v[86:89]
	v_mfma_f32_16x16x32_bf16 v[78:81], v[178:181], v[202:205], v[78:81]
	v_mfma_f32_16x16x32_bf16 v[66:69], v[178:181], v[210:213], v[66:69]
	v_mfma_f32_16x16x32_bf16 v[70:73], v[170:173], v[210:213], v[70:73]
	s_barrier
	s_add_i32 s88, s88, s30
	v_lshl_add_u64 v[146:147], s[24:25], 0, v[134:135]
	s_mov_b32 m0, s88
	ds_read_b128 v[182:185], v148 offset:16384
	ds_read_b128 v[186:189], v148 offset:17408
	ds_read_b128 v[190:193], v148 offset:18432
	ds_read_b128 v[194:197], v148 offset:19456
	ds_read_b128 v[198:201], v148 offset:20480
	ds_read_b128 v[202:205], v148 offset:21504
	ds_read_b128 v[206:209], v148 offset:22528
	ds_read_b128 v[210:213], v148 offset:23552
	global_load_lds_dwordx4 v[146:147], off
	s_add_i32 m0, s88, 0x2000
	s_add_u32 s88, s24, 0x80000
	v_lshl_add_u64 v[214:215], s[24:25], 0, v[130:131]
	s_addc_u32 s89, s25, 0
	s_add_i32 s94, s94, s30
	global_load_lds_dwordx4 v[214:215], off
	v_lshl_add_u64 v[216:217], s[88:89], 0, v[134:135]
	s_mov_b32 m0, s94
	v_lshl_add_u64 v[218:219], s[26:27], 0, v[132:133]
	global_load_lds_dwordx4 v[216:217], off
	v_lshl_add_u64 v[216:217], s[88:89], 0, v[130:131]
	s_add_i32 m0, s94, 0x2000
	s_nop 0
	global_load_lds_dwordx4 v[216:217], off
	v_lshl_add_u64 v[216:217], s[26:27], 0, v[136:137]
	s_mov_b32 m0, s31
	s_nop 0
	global_load_lds_dwordx4 v[216:217], off
	s_mov_b32 m0, s34
	s_nop 0
	global_load_lds_dwordx4 v[218:219], off
	s_waitcnt vmcnt(8)
	s_waitcnt lgkmcnt(0)
	s_barrier
; #define PG8_STAGE(bufoff, gbase, voff) do { _Pragma("unroll") for (int _i = 0; _i < 2; ++_i) \
;         __builtin_amdgcn_global_load_lds((const unsigned*)((const char*)(gbase) + (voff)[_i]), (PG8_LAS unsigned*)(lds + (bufoff) + ldsw + _i * 8192), 16, 0, 0); } while (0)
; #define PG8_WAIT_V(n) asm volatile("s_waitcnt vmcnt(" #n ")" ::: "memory")
; #define PG8_WAIT_L(n) asm volatile("s_waitcnt lgkmcnt(" #n ")" ::: "memory")
; #define PG8_BAR __builtin_amdgcn_s_barrier()
; #define PG8_SCHED __builtin_amdgcn_sched_barrier(0)
; template <class Epi, class Sched, bool ALIGN_EPI, bool F8 = false>
; __device__ __forceinline__ void gemm_phase(PG8_LAS unsigned char* lds, const Gemm g, const Sched& S, const Epi& E, int tid) {
;     ...
;             PG8_WAIT_V(8); PG8_WAIT_L(0); PG8_BAR; PG8_MMA(1, 0, At, B0); PG8_MMA(1, 1, At, B1); PG8_BAR; PG8_SCHED;
;             PG8_LDB(B0, 1, 0); PG8_LDB(B1, 1, 1); PG8_SCHED; PG8_LDA(At, 1, 0); PG8_STAGE(PG8_SA(0, 1), a2 + hstepA, voffA);
;             PG8_WAIT_V(8); PG8_WAIT_L(0); PG8_BAR; PG8_MMA(0, 0, At, B0); PG8_MMA(0, 1, At, B1); PG8_BAR; PG8_SCHED;
	s_setprio 1
	s_waitcnt lgkmcnt(0)
	v_mfma_f32_16x16x32_bf16 v[62:65], v[150:153], v[182:185], v[62:65]
	v_mfma_f32_16x16x32_bf16 v[58:61], v[158:161], v[182:185], v[58:61]
	v_mfma_f32_16x16x32_bf16 v[42:45], v[158:161], v[190:193], v[42:45]
	v_mfma_f32_16x16x32_bf16 v[50:53], v[150:153], v[190:193], v[50:53]
	v_mfma_f32_16x16x32_bf16 v[34:37], v[150:153], v[198:201], v[34:37]
	v_mfma_f32_16x16x32_bf16 v[26:29], v[158:161], v[198:201], v[26:29]
	v_mfma_f32_16x16x32_bf16 v[10:13], v[158:161], v[206:209], v[10:13]
	v_mfma_f32_16x16x32_bf16 v[18:21], v[150:153], v[206:209], v[18:21]
	v_mfma_f32_16x16x32_bf16 v[62:65], v[154:157], v[186:189], v[62:65]
	v_mfma_f32_16x16x32_bf16 v[58:61], v[162:165], v[186:189], v[58:61]
	v_mfma_f32_16x16x32_bf16 v[42:45], v[162:165], v[194:197], v[42:45]
	v_mfma_f32_16x16x32_bf16 v[50:53], v[154:157], v[194:197], v[50:53]
	v_mfma_f32_16x16x32_bf16 v[34:37], v[154:157], v[202:205], v[34:37]
	v_mfma_f32_16x16x32_bf16 v[26:29], v[162:165], v[202:205], v[26:29]
	v_mfma_f32_16x16x32_bf16 v[10:13], v[162:165], v[210:213], v[10:13]
	v_mfma_f32_16x16x32_bf16 v[18:21], v[154:157], v[210:213], v[18:21]
	s_setprio 0
	s_setprio 1
	v_mfma_f32_16x16x32_bf16 v[54:57], v[166:169], v[182:185], v[54:57]
	v_mfma_f32_16x16x32_bf16 v[46:49], v[174:177], v[182:185], v[46:49]
	v_mfma_f32_16x16x32_bf16 v[30:33], v[174:177], v[190:193], v[30:33]
	v_mfma_f32_16x16x32_bf16 v[38:41], v[166:169], v[190:193], v[38:41]
	v_mfma_f32_16x16x32_bf16 v[22:25], v[166:169], v[198:201], v[22:25]
	v_mfma_f32_16x16x32_bf16 v[14:17], v[174:177], v[198:201], v[14:17]
	v_mfma_f32_16x16x32_bf16 v[2:5], v[174:177], v[206:209], v[2:5]
	v_mfma_f32_16x16x32_bf16 v[6:9], v[166:169], v[206:209], v[6:9]
	v_mfma_f32_16x16x32_bf16 v[54:57], v[170:173], v[186:189], v[54:57]
	v_mfma_f32_16x16x32_bf16 v[46:49], v[178:181], v[186:189], v[46:49]
	v_mfma_f32_16x16x32_bf16 v[30:33], v[178:181], v[194:197], v[30:33]
	v_mfma_f32_16x16x32_bf16 v[38:41], v[170:173], v[194:197], v[38:41]
	s_setprio 0
	v_mfma_f32_16x16x32_bf16 v[22:25], v[170:173], v[202:205], v[22:25]
	v_mfma_f32_16x16x32_bf16 v[14:17], v[178:181], v[202:205], v[14:17]
	v_mfma_f32_16x16x32_bf16 v[2:5], v[178:181], v[210:213], v[2:5]
	v_mfma_f32_16x16x32_bf16 v[6:9], v[170:173], v[210:213], v[6:9]
	s_barrier
	s_add_i32 s88, 0, 0x18000
	v_add_u32_e32 v144, s88, v145
	s_add_i32 s89, 0, 0x1c000
	ds_read_b128 v[150:153], v144
	ds_read_b128 v[154:157], v144 offset:1024
	ds_read_b128 v[158:161], v144 offset:2048
	ds_read_b128 v[162:165], v144 offset:3072
	v_add_u32_e32 v144, s89, v145
	ds_read_b128 v[166:169], v144
	ds_read_b128 v[170:173], v144 offset:1024
	ds_read_b128 v[174:177], v144 offset:2048
	ds_read_b128 v[178:181], v144 offset:3072
	s_add_u32 s26, s26, 0x100000
	s_addc_u32 s27, s27, 0
	s_mov_b32 m0, s35
	v_lshl_add_u64 v[220:221], s[26:27], 0, v[136:137]
	ds_read_b128 v[182:185], v148 offset:32768
	ds_read_b128 v[186:189], v148 offset:33792
	ds_read_b128 v[190:193], v148 offset:34816
	ds_read_b128 v[194:197], v148 offset:35840
	ds_read_b128 v[198:201], v148 offset:36864
	ds_read_b128 v[202:205], v148 offset:37888
	ds_read_b128 v[206:209], v148 offset:38912
	ds_read_b128 v[210:213], v148 offset:39936
	global_load_lds_dwordx4 v[220:221], off
	v_lshl_add_u64 v[220:221], s[26:27], 0, v[132:133]
	s_mov_b32 m0, s38
	s_nop 0
	global_load_lds_dwordx4 v[220:221], off
	s_waitcnt vmcnt(8)
	s_waitcnt lgkmcnt(0)
	s_barrier
	s_setprio 1
	s_waitcnt lgkmcnt(0)
	v_mfma_f32_16x16x32_bf16 v[126:129], v[150:153], v[182:185], v[126:129]
	v_mfma_f32_16x16x32_bf16 v[122:125], v[158:161], v[182:185], v[122:125]
	v_mfma_f32_16x16x32_bf16 v[106:109], v[158:161], v[190:193], v[106:109]
	v_mfma_f32_16x16x32_bf16 v[114:117], v[150:153], v[190:193], v[114:117]
	v_mfma_f32_16x16x32_bf16 v[98:101], v[150:153], v[198:201], v[98:101]
	v_mfma_f32_16x16x32_bf16 v[90:93], v[158:161], v[198:201], v[90:93]
	v_mfma_f32_16x16x32_bf16 v[74:77], v[158:161], v[206:209], v[74:77]
	v_mfma_f32_16x16x32_bf16 v[82:85], v[150:153], v[206:209], v[82:85]
	v_mfma_f32_16x16x32_bf16 v[126:129], v[154:157], v[186:189], v[126:129]
	v_mfma_f32_16x16x32_bf16 v[122:125], v[162:165], v[186:189], v[122:125]
	v_mfma_f32_16x16x32_bf16 v[106:109], v[162:165], v[194:197], v[106:109]
	v_mfma_f32_16x16x32_bf16 v[114:117], v[154:157], v[194:197], v[114:117]
	v_mfma_f32_16x16x32_bf16 v[98:101], v[154:157], v[202:205], v[98:101]
	v_mfma_f32_16x16x32_bf16 v[90:93], v[162:165], v[202:205], v[90:93]
	v_mfma_f32_16x16x32_bf16 v[74:77], v[162:165], v[210:213], v[74:77]
	v_mfma_f32_16x16x32_bf16 v[82:85], v[154:157], v[210:213], v[82:85]
	s_setprio 0
	s_setprio 1
	v_mfma_f32_16x16x32_bf16 v[118:121], v[166:169], v[182:185], v[118:121]
	v_mfma_f32_16x16x32_bf16 v[110:113], v[174:177], v[182:185], v[110:113]
	v_mfma_f32_16x16x32_bf16 v[94:97], v[174:177], v[190:193], v[94:97]
	v_mfma_f32_16x16x32_bf16 v[102:105], v[166:169], v[190:193], v[102:105]
	v_mfma_f32_16x16x32_bf16 v[86:89], v[166:169], v[198:201], v[86:89]
	v_mfma_f32_16x16x32_bf16 v[78:81], v[174:177], v[198:201], v[78:81]
	v_mfma_f32_16x16x32_bf16 v[66:69], v[174:177], v[206:209], v[66:69]
	v_mfma_f32_16x16x32_bf16 v[70:73], v[166:169], v[206:209], v[70:73]
	v_mfma_f32_16x16x32_bf16 v[118:121], v[170:173], v[186:189], v[118:121]
	v_mfma_f32_16x16x32_bf16 v[110:113], v[178:181], v[186:189], v[110:113]
	v_mfma_f32_16x16x32_bf16 v[94:97], v[178:181], v[194:197], v[94:97]
	v_mfma_f32_16x16x32_bf16 v[102:105], v[170:173], v[194:197], v[102:105]
	s_setprio 0
	v_mfma_f32_16x16x32_bf16 v[86:89], v[170:173], v[202:205], v[86:89]
	v_mfma_f32_16x16x32_bf16 v[78:81], v[178:181], v[202:205], v[78:81]
	v_mfma_f32_16x16x32_bf16 v[66:69], v[178:181], v[210:213], v[66:69]
	v_mfma_f32_16x16x32_bf16 v[70:73], v[170:173], v[210:213], v[70:73]
	s_barrier
; #define PG8_STAGE(bufoff, gbase, voff) do { _Pragma("unroll") for (int _i = 0; _i < 2; ++_i) \
;         __builtin_amdgcn_global_load_lds((const unsigned*)((const char*)(gbase) + (voff)[_i]), (PG8_LAS unsigned*)(lds + (bufoff) + ldsw + _i * 8192), 16, 0, 0); } while (0)
; #define PG8_WAIT_V(n) asm volatile("s_waitcnt vmcnt(" #n ")" ::: "memory")
; #define PG8_WAIT_L(n) asm volatile("s_waitcnt lgkmcnt(" #n ")" ::: "memory")
; #define PG8_BAR __builtin_amdgcn_s_barrier()
; #define PG8_SCHED __builtin_amdgcn_sched_barrier(0)
; template <class Epi, class Sched, bool ALIGN_EPI, bool F8 = false>
; __device__ __forceinline__ void gemm_phase(PG8_LAS unsigned char* lds, const Gemm g, const Sched& S, const Epi& E, int tid) {
;     ...
;             PG8_LDA(At, 1, 1); PG8_STAGE(PG8_SB(1, 0), b3, voffB); PG8_STAGE(PG8_SB(1, 1), b3 + hstepB, voffB); PG8_STAGE(PG8_SA(1, 0), a3, voffA);
;             PG8_WAIT_V(8); PG8_WAIT_L(0); PG8_BAR; PG8_MMA(1, 0, At, B0); PG8_MMA(1, 1, At, B1); PG8_BAR; PG8_SCHED;
;         }
;         if constexpr (ALIGN_EPI) { if (wr == 0) PG8_BAR; }
	s_add_i32 s26, s88, s30
	v_lshl_add_u64 v[146:147], v[146:147], 0, s[60:61]
	s_mov_b32 m0, s26
	ds_read_b128 v[182:185], v148 offset:49152
	ds_read_b128 v[186:189], v148 offset:50176
	ds_read_b128 v[190:193], v148 offset:51200
	ds_read_b128 v[194:197], v148 offset:52224
	ds_read_b128 v[198:201], v148 offset:53248
	ds_read_b128 v[202:205], v148 offset:54272
	ds_read_b128 v[206:209], v148 offset:55296
	ds_read_b128 v[210:213], v148 offset:56320
	global_load_lds_dwordx4 v[146:147], off
	s_add_i32 m0, s26, 0x2000
	s_add_u32 s24, s24, 0x80080
	v_lshl_add_u64 v[146:147], v[214:215], 0, s[60:61]
	s_addc_u32 s25, s25, 0
	s_add_i32 s26, s89, s30
	global_load_lds_dwordx4 v[146:147], off
	v_lshl_add_u64 v[146:147], s[24:25], 0, v[134:135]
	s_mov_b32 m0, s26
	s_nop 0
	global_load_lds_dwordx4 v[146:147], off
	v_lshl_add_u64 v[146:147], s[24:25], 0, v[130:131]
	s_add_i32 m0, s26, 0x2000
	s_nop 0
	global_load_lds_dwordx4 v[146:147], off
	v_lshl_add_u64 v[146:147], v[216:217], 0, s[60:61]
	s_mov_b32 m0, s45
	s_nop 0
	global_load_lds_dwordx4 v[146:147], off
	v_lshl_add_u64 v[146:147], v[218:219], 0, s[60:61]
	s_mov_b32 m0, s50
	s_nop 0
	global_load_lds_dwordx4 v[146:147], off
	s_waitcnt vmcnt(8)
	s_waitcnt lgkmcnt(0)
	s_barrier
	s_setprio 1
	s_waitcnt lgkmcnt(0)
	v_mfma_f32_16x16x32_bf16 v[62:65], v[150:153], v[182:185], v[62:65]
	v_mfma_f32_16x16x32_bf16 v[58:61], v[158:161], v[182:185], v[58:61]
	v_mfma_f32_16x16x32_bf16 v[42:45], v[158:161], v[190:193], v[42:45]
	v_mfma_f32_16x16x32_bf16 v[50:53], v[150:153], v[190:193], v[50:53]
	v_mfma_f32_16x16x32_bf16 v[34:37], v[150:153], v[198:201], v[34:37]
	v_mfma_f32_16x16x32_bf16 v[26:29], v[158:161], v[198:201], v[26:29]
	v_mfma_f32_16x16x32_bf16 v[10:13], v[158:161], v[206:209], v[10:13]
	v_mfma_f32_16x16x32_bf16 v[18:21], v[150:153], v[206:209], v[18:21]
	v_mfma_f32_16x16x32_bf16 v[62:65], v[154:157], v[186:189], v[62:65]
	v_mfma_f32_16x16x32_bf16 v[58:61], v[162:165], v[186:189], v[58:61]
	v_mfma_f32_16x16x32_bf16 v[42:45], v[162:165], v[194:197], v[42:45]
	v_mfma_f32_16x16x32_bf16 v[50:53], v[154:157], v[194:197], v[50:53]
	v_mfma_f32_16x16x32_bf16 v[34:37], v[154:157], v[202:205], v[34:37]
	v_mfma_f32_16x16x32_bf16 v[26:29], v[162:165], v[202:205], v[26:29]
	v_mfma_f32_16x16x32_bf16 v[10:13], v[162:165], v[210:213], v[10:13]
	v_mfma_f32_16x16x32_bf16 v[18:21], v[154:157], v[210:213], v[18:21]
	s_setprio 0
	s_setprio 1
	v_mfma_f32_16x16x32_bf16 v[54:57], v[166:169], v[182:185], v[54:57]
	v_mfma_f32_16x16x32_bf16 v[46:49], v[174:177], v[182:185], v[46:49]
	v_mfma_f32_16x16x32_bf16 v[30:33], v[174:177], v[190:193], v[30:33]
	v_mfma_f32_16x16x32_bf16 v[38:41], v[166:169], v[190:193], v[38:41]
	v_mfma_f32_16x16x32_bf16 v[22:25], v[166:169], v[198:201], v[22:25]
	v_mfma_f32_16x16x32_bf16 v[14:17], v[174:177], v[198:201], v[14:17]
	v_mfma_f32_16x16x32_bf16 v[2:5], v[174:177], v[206:209], v[2:5]
	v_mfma_f32_16x16x32_bf16 v[6:9], v[166:169], v[206:209], v[6:9]
	v_mfma_f32_16x16x32_bf16 v[54:57], v[170:173], v[186:189], v[54:57]
	v_mfma_f32_16x16x32_bf16 v[46:49], v[178:181], v[186:189], v[46:49]
	v_mfma_f32_16x16x32_bf16 v[30:33], v[178:181], v[194:197], v[30:33]
	v_mfma_f32_16x16x32_bf16 v[38:41], v[170:173], v[194:197], v[38:41]
	s_setprio 0
	v_mfma_f32_16x16x32_bf16 v[22:25], v[170:173], v[202:205], v[22:25]
	v_mfma_f32_16x16x32_bf16 v[14:17], v[178:181], v[202:205], v[14:17]
	v_mfma_f32_16x16x32_bf16 v[2:5], v[178:181], v[210:213], v[2:5]
	v_mfma_f32_16x16x32_bf16 v[6:9], v[170:173], v[210:213], v[6:9]
	s_barrier
	s_add_i32 s87, s87, 2
	s_add_u32 s22, s22, 0x100
	s_addc_u32 s23, s23, 0
	s_add_u32 s85, s85, 0x100
	s_addc_u32 s86, s86, 0
	s_cmp_gt_u32 s87, 5
	s_cbranch_scc0 .LBB0_1147
	s_and_b64 vcc, exec, s[6:7]
	s_cbranch_vccz .LBB0_1150
	s_barrier

; #define PG8_STAGE(bufoff, gbase, voff) do { _Pragma("unroll") for (int _i = 0; _i < 2; ++_i) \
;         __builtin_amdgcn_global_load_lds((const unsigned*)((const char*)(gbase) + (voff)[_i]), (PG8_LAS unsigned*)(lds + (bufoff) + ldsw + _i * 8192), 16, 0, 0); } while (0)
; #define PG8_WAIT_V(n) asm volatile("s_waitcnt vmcnt(" #n ")" ::: "memory")
; #define PG8_WAIT_L(n) asm volatile("s_waitcnt lgkmcnt(" #n ")" ::: "memory")
; #define PG8_BAR __builtin_amdgcn_s_barrier()
; #define PG8_SCHED __builtin_amdgcn_sched_barrier(0)
; template <class Epi, class Sched, bool ALIGN_EPI, bool F8 = false>
; __device__ __forceinline__ void gemm_phase(PG8_LAS unsigned char* lds, const Gemm g, const Sched& S, const Epi& E, int tid) {
;     ...
;             const bool last = (t == nt - 2);
;             const char* a1 = cA + (size_t)(t + 1) * kstep;
;             const char* a2 = last ? nA : cA + (size_t)(t + 2) * kstep; const char* b2 = last ? nB : cB + (size_t)(t + 2) * kstep;
;             const char* a3 = a2 + kstep; const char* b3 = b2 + kstep;
;             if (last && has_next) S.a_ready(nxt);
;             PG8_LDB(B0, 0, 0); PG8_LDB(B1, 0, 1); PG8_SCHED; PG8_LDA(At, 0, 0); PG8_STAGE(PG8_SA(1, 1), a1 + hstepA, voffA);
;             PG8_WAIT_V(8); PG8_WAIT_L(0); PG8_BAR; PG8_MMA(0, 0, At, B0); PG8_MMA(0, 1, At, B1); PG8_BAR; PG8_SCHED;
;             PG8_LDA(At, 0, 1); PG8_STAGE(PG8_SB(0, 0), b2, voffB); PG8_STAGE(PG8_SB(0, 1), b2 + hstepB, voffB); PG8_STAGE(PG8_SA(0, 0), a2, voffA);
.LBB0_1163:
	s_add_u32 s24, s22, 0xfff80080
	s_addc_u32 s25, s23, -1
	s_add_i32 s87, 0, 0x10000
	s_cmp_eq_u32 s86, 4
	s_cselect_b32 s27, s9, s25
	s_cselect_b32 s26, s11, s24
	v_add_u32_e32 v144, s87, v145
	s_cselect_b32 s25, s13, s85
	s_cselect_b32 s24, s83, s84
	s_add_i32 s94, 0, 0x14000
	ds_read_b128 v[150:153], v144
	ds_read_b128 v[154:157], v144 offset:1024
	ds_read_b128 v[158:161], v144 offset:2048
	ds_read_b128 v[162:165], v144 offset:3072
	v_add_u32_e32 v144, s94, v145
	ds_read_b128 v[166:169], v144
	ds_read_b128 v[170:173], v144 offset:1024
	ds_read_b128 v[174:177], v144 offset:2048
	ds_read_b128 v[178:181], v144 offset:3072
	v_lshl_add_u64 v[146:147], s[22:23], 0, v[140:141]
	s_add_i32 m0, s31, 0xc000
	ds_read_b128 v[182:185], v148
	ds_read_b128 v[186:189], v148 offset:1024
	ds_read_b128 v[190:193], v148 offset:2048
	ds_read_b128 v[194:197], v148 offset:3072
	ds_read_b128 v[198:201], v148 offset:4096
	ds_read_b128 v[202:205], v148 offset:5120
	ds_read_b128 v[206:209], v148 offset:6144
	ds_read_b128 v[210:213], v148 offset:7168
	global_load_lds_dwordx4 v[146:147], off
	v_lshl_add_u64 v[146:147], s[22:23], 0, v[142:143]
	s_add_i32 m0, s31, 0xe000
	s_nop 0
	global_load_lds_dwordx4 v[146:147], off
	s_waitcnt vmcnt(8)
	s_waitcnt lgkmcnt(0)
	s_barrier
	s_setprio 1
	s_waitcnt lgkmcnt(0)
	v_mfma_f32_16x16x32_bf16 v[126:129], v[150:153], v[182:185], v[126:129]
	v_mfma_f32_16x16x32_bf16 v[122:125], v[158:161], v[182:185], v[122:125]
	v_mfma_f32_16x16x32_bf16 v[106:109], v[158:161], v[190:193], v[106:109]
	v_mfma_f32_16x16x32_bf16 v[114:117], v[150:153], v[190:193], v[114:117]
	v_mfma_f32_16x16x32_bf16 v[98:101], v[150:153], v[198:201], v[98:101]
	v_mfma_f32_16x16x32_bf16 v[90:93], v[158:161], v[198:201], v[90:93]
	v_mfma_f32_16x16x32_bf16 v[74:77], v[158:161], v[206:209], v[74:77]
	v_mfma_f32_16x16x32_bf16 v[82:85], v[150:153], v[206:209], v[82:85]
	v_mfma_f32_16x16x32_bf16 v[126:129], v[154:157], v[186:189], v[126:129]
	v_mfma_f32_16x16x32_bf16 v[122:125], v[162:165], v[186:189], v[122:125]
	v_mfma_f32_16x16x32_bf16 v[106:109], v[162:165], v[194:197], v[106:109]
	v_mfma_f32_16x16x32_bf16 v[114:117], v[154:157], v[194:197], v[114:117]
	v_mfma_f32_16x16x32_bf16 v[98:101], v[154:157], v[202:205], v[98:101]
	v_mfma_f32_16x16x32_bf16 v[90:93], v[162:165], v[202:205], v[90:93]
	v_mfma_f32_16x16x32_bf16 v[74:77], v[162:165], v[210:213], v[74:77]
	v_mfma_f32_16x16x32_bf16 v[82:85], v[154:157], v[210:213], v[82:85]
	s_setprio 0
	s_setprio 1
	v_mfma_f32_16x16x32_bf16 v[118:121], v[166:169], v[182:185], v[118:121]
	v_mfma_f32_16x16x32_bf16 v[110:113], v[174:177], v[182:185], v[110:113]
	v_mfma_f32_16x16x32_bf16 v[94:97], v[174:177], v[190:193], v[94:97]
	v_mfma_f32_16x16x32_bf16 v[102:105], v[166:169], v[190:193], v[102:105]
	v_mfma_f32_16x16x32_bf16 v[86:89], v[166:169], v[198:201], v[86:89]
	v_mfma_f32_16x16x32_bf16 v[78:81], v[174:177], v[198:201], v[78:81]
	v_mfma_f32_16x16x32_bf16 v[66:69], v[174:177], v[206:209], v[66:69]
	v_mfma_f32_16x16x32_bf16 v[70:73], v[166:169], v[206:209], v[70:73]
	v_mfma_f32_16x16x32_bf16 v[118:121], v[170:173], v[186:189], v[118:121]
	v_mfma_f32_16x16x32_bf16 v[110:113], v[178:181], v[186:189], v[110:113]
	v_mfma_f32_16x16x32_bf16 v[94:97], v[178:181], v[194:197], v[94:97]
	v_mfma_f32_16x16x32_bf16 v[102:105], v[170:173], v[194:197], v[102:105]
	s_setprio 0
	v_mfma_f32_16x16x32_bf16 v[86:89], v[170:173], v[202:205], v[86:89]
	v_mfma_f32_16x16x32_bf16 v[78:81], v[178:181], v[202:205], v[78:81]
	v_mfma_f32_16x16x32_bf16 v[66:69], v[178:181], v[210:213], v[66:69]
	v_mfma_f32_16x16x32_bf16 v[70:73], v[170:173], v[210:213], v[70:73]
	s_barrier
	s_add_i32 s87, s87, s30
	v_lshl_add_u64 v[146:147], s[24:25], 0, v[134:135]
	s_mov_b32 m0, s87
	ds_read_b128 v[182:185], v148 offset:16384
	ds_read_b128 v[186:189], v148 offset:17408
	ds_read_b128 v[190:193], v148 offset:18432
	ds_read_b128 v[194:197], v148 offset:19456
	ds_read_b128 v[198:201], v148 offset:20480
	ds_read_b128 v[202:205], v148 offset:21504
	ds_read_b128 v[206:209], v148 offset:22528
	ds_read_b128 v[210:213], v148 offset:23552
	global_load_lds_dwordx4 v[146:147], off
	s_add_i32 m0, s87, 0x2000
	s_add_u32 s88, s24, 0x100000
	v_lshl_add_u64 v[214:215], s[24:25], 0, v[130:131]
	s_addc_u32 s89, s25, 0
	s_add_i32 s87, s94, s30
	global_load_lds_dwordx4 v[214:215], off
	v_lshl_add_u64 v[216:217], s[88:89], 0, v[134:135]
	s_mov_b32 m0, s87
	v_lshl_add_u64 v[218:219], s[26:27], 0, v[132:133]
	global_load_lds_dwordx4 v[216:217], off
	v_lshl_add_u64 v[216:217], s[88:89], 0, v[130:131]
	s_add_i32 m0, s87, 0x2000
	s_nop 0
	global_load_lds_dwordx4 v[216:217], off
	v_lshl_add_u64 v[216:217], s[26:27], 0, v[136:137]
	s_mov_b32 m0, s31
	s_nop 0
	global_load_lds_dwordx4 v[216:217], off
	s_mov_b32 m0, s34
	s_nop 0
	global_load_lds_dwordx4 v[218:219], off
	s_waitcnt vmcnt(8)
	s_waitcnt lgkmcnt(0)
	s_barrier
; #define PG8_STAGE(bufoff, gbase, voff) do { _Pragma("unroll") for (int _i = 0; _i < 2; ++_i) \
;         __builtin_amdgcn_global_load_lds((const unsigned*)((const char*)(gbase) + (voff)[_i]), (PG8_LAS unsigned*)(lds + (bufoff) + ldsw + _i * 8192), 16, 0, 0); } while (0)
; #define PG8_WAIT_V(n) asm volatile("s_waitcnt vmcnt(" #n ")" ::: "memory")
; #define PG8_WAIT_L(n) asm volatile("s_waitcnt lgkmcnt(" #n ")" ::: "memory")
; #define PG8_BAR __builtin_amdgcn_s_barrier()
; #define PG8_SCHED __builtin_amdgcn_sched_barrier(0)
; template <class Epi, class Sched, bool ALIGN_EPI, bool F8 = false>
; __device__ __forceinline__ void gemm_phase(PG8_LAS unsigned char* lds, const Gemm g, const Sched& S, const Epi& E, int tid) {
;     ...
;             PG8_WAIT_V(8); PG8_WAIT_L(0); PG8_BAR; PG8_MMA(1, 0, At, B0); PG8_MMA(1, 1, At, B1); PG8_BAR; PG8_SCHED;
;             PG8_LDB(B0, 1, 0); PG8_LDB(B1, 1, 1); PG8_SCHED; PG8_LDA(At, 1, 0); PG8_STAGE(PG8_SA(0, 1), a2 + hstepA, voffA);
;             PG8_WAIT_V(8); PG8_WAIT_L(0); PG8_BAR; PG8_MMA(0, 0, At, B0); PG8_MMA(0, 1, At, B1); PG8_BAR; PG8_SCHED;
	s_setprio 1
	s_waitcnt lgkmcnt(0)
	v_mfma_f32_16x16x32_bf16 v[62:65], v[150:153], v[182:185], v[62:65]
	v_mfma_f32_16x16x32_bf16 v[58:61], v[158:161], v[182:185], v[58:61]
	v_mfma_f32_16x16x32_bf16 v[42:45], v[158:161], v[190:193], v[42:45]
	v_mfma_f32_16x16x32_bf16 v[50:53], v[150:153], v[190:193], v[50:53]
	v_mfma_f32_16x16x32_bf16 v[34:37], v[150:153], v[198:201], v[34:37]
	v_mfma_f32_16x16x32_bf16 v[26:29], v[158:161], v[198:201], v[26:29]
	v_mfma_f32_16x16x32_bf16 v[10:13], v[158:161], v[206:209], v[10:13]
	v_mfma_f32_16x16x32_bf16 v[18:21], v[150:153], v[206:209], v[18:21]
	v_mfma_f32_16x16x32_bf16 v[62:65], v[154:157], v[186:189], v[62:65]
	v_mfma_f32_16x16x32_bf16 v[58:61], v[162:165], v[186:189], v[58:61]
	v_mfma_f32_16x16x32_bf16 v[42:45], v[162:165], v[194:197], v[42:45]
	v_mfma_f32_16x16x32_bf16 v[50:53], v[154:157], v[194:197], v[50:53]
	v_mfma_f32_16x16x32_bf16 v[34:37], v[154:157], v[202:205], v[34:37]
	v_mfma_f32_16x16x32_bf16 v[26:29], v[162:165], v[202:205], v[26:29]
	v_mfma_f32_16x16x32_bf16 v[10:13], v[162:165], v[210:213], v[10:13]
	v_mfma_f32_16x16x32_bf16 v[18:21], v[154:157], v[210:213], v[18:21]
	s_setprio 0
	s_setprio 1
	v_mfma_f32_16x16x32_bf16 v[54:57], v[166:169], v[182:185], v[54:57]
	v_mfma_f32_16x16x32_bf16 v[46:49], v[174:177], v[182:185], v[46:49]
	v_mfma_f32_16x16x32_bf16 v[30:33], v[174:177], v[190:193], v[30:33]
	v_mfma_f32_16x16x32_bf16 v[38:41], v[166:169], v[190:193], v[38:41]
	v_mfma_f32_16x16x32_bf16 v[22:25], v[166:169], v[198:201], v[22:25]
	v_mfma_f32_16x16x32_bf16 v[14:17], v[174:177], v[198:201], v[14:17]
	v_mfma_f32_16x16x32_bf16 v[2:5], v[174:177], v[206:209], v[2:5]
	v_mfma_f32_16x16x32_bf16 v[6:9], v[166:169], v[206:209], v[6:9]
	v_mfma_f32_16x16x32_bf16 v[54:57], v[170:173], v[186:189], v[54:57]
	v_mfma_f32_16x16x32_bf16 v[46:49], v[178:181], v[186:189], v[46:49]
	v_mfma_f32_16x16x32_bf16 v[30:33], v[178:181], v[194:197], v[30:33]
	v_mfma_f32_16x16x32_bf16 v[38:41], v[170:173], v[194:197], v[38:41]
	s_setprio 0
	v_mfma_f32_16x16x32_bf16 v[22:25], v[170:173], v[202:205], v[22:25]
	v_mfma_f32_16x16x32_bf16 v[14:17], v[178:181], v[202:205], v[14:17]
	v_mfma_f32_16x16x32_bf16 v[2:5], v[178:181], v[210:213], v[2:5]
	v_mfma_f32_16x16x32_bf16 v[6:9], v[170:173], v[210:213], v[6:9]
	s_barrier
	s_add_i32 s87, 0, 0x18000
	v_add_u32_e32 v144, s87, v145
	s_add_i32 s88, 0, 0x1c000
	ds_read_b128 v[150:153], v144
	ds_read_b128 v[154:157], v144 offset:1024
	ds_read_b128 v[158:161], v144 offset:2048
	ds_read_b128 v[162:165], v144 offset:3072
	v_add_u32_e32 v144, s88, v145
	ds_read_b128 v[166:169], v144
	ds_read_b128 v[170:173], v144 offset:1024
	ds_read_b128 v[174:177], v144 offset:2048
	ds_read_b128 v[178:181], v144 offset:3072
	s_add_u32 s26, s26, 0x80000
	s_addc_u32 s27, s27, 0
	s_mov_b32 m0, s35
	v_lshl_add_u64 v[220:221], s[26:27], 0, v[136:137]
	ds_read_b128 v[182:185], v148 offset:32768
	ds_read_b128 v[186:189], v148 offset:33792
	ds_read_b128 v[190:193], v148 offset:34816
	ds_read_b128 v[194:197], v148 offset:35840
	ds_read_b128 v[198:201], v148 offset:36864
	ds_read_b128 v[202:205], v148 offset:37888
	ds_read_b128 v[206:209], v148 offset:38912
	ds_read_b128 v[210:213], v148 offset:39936
	global_load_lds_dwordx4 v[220:221], off
	v_lshl_add_u64 v[220:221], s[26:27], 0, v[132:133]
	s_mov_b32 m0, s38
	s_nop 0
	global_load_lds_dwordx4 v[220:221], off
	s_waitcnt vmcnt(8)
	s_waitcnt lgkmcnt(0)
	s_barrier
	s_setprio 1
	s_waitcnt lgkmcnt(0)
	v_mfma_f32_16x16x32_bf16 v[126:129], v[150:153], v[182:185], v[126:129]
	v_mfma_f32_16x16x32_bf16 v[122:125], v[158:161], v[182:185], v[122:125]
	v_mfma_f32_16x16x32_bf16 v[106:109], v[158:161], v[190:193], v[106:109]
	v_mfma_f32_16x16x32_bf16 v[114:117], v[150:153], v[190:193], v[114:117]
	v_mfma_f32_16x16x32_bf16 v[98:101], v[150:153], v[198:201], v[98:101]
	v_mfma_f32_16x16x32_bf16 v[90:93], v[158:161], v[198:201], v[90:93]
	v_mfma_f32_16x16x32_bf16 v[74:77], v[158:161], v[206:209], v[74:77]
	v_mfma_f32_16x16x32_bf16 v[82:85], v[150:153], v[206:209], v[82:85]
	v_mfma_f32_16x16x32_bf16 v[126:129], v[154:157], v[186:189], v[126:129]
	v_mfma_f32_16x16x32_bf16 v[122:125], v[162:165], v[186:189], v[122:125]
	v_mfma_f32_16x16x32_bf16 v[106:109], v[162:165], v[194:197], v[106:109]
	v_mfma_f32_16x16x32_bf16 v[114:117], v[154:157], v[194:197], v[114:117]
	v_mfma_f32_16x16x32_bf16 v[98:101], v[154:157], v[202:205], v[98:101]
	v_mfma_f32_16x16x32_bf16 v[90:93], v[162:165], v[202:205], v[90:93]
	v_mfma_f32_16x16x32_bf16 v[74:77], v[162:165], v[210:213], v[74:77]
	v_mfma_f32_16x16x32_bf16 v[82:85], v[154:157], v[210:213], v[82:85]
	s_setprio 0
	s_setprio 1
	v_mfma_f32_16x16x32_bf16 v[118:121], v[166:169], v[182:185], v[118:121]
	v_mfma_f32_16x16x32_bf16 v[110:113], v[174:177], v[182:185], v[110:113]
	v_mfma_f32_16x16x32_bf16 v[94:97], v[174:177], v[190:193], v[94:97]
	v_mfma_f32_16x16x32_bf16 v[102:105], v[166:169], v[190:193], v[102:105]
	v_mfma_f32_16x16x32_bf16 v[86:89], v[166:169], v[198:201], v[86:89]
	v_mfma_f32_16x16x32_bf16 v[78:81], v[174:177], v[198:201], v[78:81]
	v_mfma_f32_16x16x32_bf16 v[66:69], v[174:177], v[206:209], v[66:69]
	v_mfma_f32_16x16x32_bf16 v[70:73], v[166:169], v[206:209], v[70:73]
	v_mfma_f32_16x16x32_bf16 v[118:121], v[170:173], v[186:189], v[118:121]
	v_mfma_f32_16x16x32_bf16 v[110:113], v[178:181], v[186:189], v[110:113]
	v_mfma_f32_16x16x32_bf16 v[94:97], v[178:181], v[194:197], v[94:97]
	v_mfma_f32_16x16x32_bf16 v[102:105], v[170:173], v[194:197], v[102:105]
	s_setprio 0
	v_mfma_f32_16x16x32_bf16 v[86:89], v[170:173], v[202:205], v[86:89]
	v_mfma_f32_16x16x32_bf16 v[78:81], v[178:181], v[202:205], v[78:81]
	v_mfma_f32_16x16x32_bf16 v[66:69], v[178:181], v[210:213], v[66:69]
	v_mfma_f32_16x16x32_bf16 v[70:73], v[170:173], v[210:213], v[70:73]
	s_barrier
; #define PG8_STAGE(bufoff, gbase, voff) do { _Pragma("unroll") for (int _i = 0; _i < 2; ++_i) \
;         __builtin_amdgcn_global_load_lds((const unsigned*)((const char*)(gbase) + (voff)[_i]), (PG8_LAS unsigned*)(lds + (bufoff) + ldsw + _i * 8192), 16, 0, 0); } while (0)
; #define PG8_WAIT_V(n) asm volatile("s_waitcnt vmcnt(" #n ")" ::: "memory")
; #define PG8_WAIT_L(n) asm volatile("s_waitcnt lgkmcnt(" #n ")" ::: "memory")
; #define PG8_BAR __builtin_amdgcn_s_barrier()
; #define PG8_SCHED __builtin_amdgcn_sched_barrier(0)
; template <class Epi, class Sched, bool ALIGN_EPI, bool F8 = false>
; __device__ __forceinline__ void gemm_phase(PG8_LAS unsigned char* lds, const Gemm g, const Sched& S, const Epi& E, int tid) {
;     ...
;             PG8_LDA(At, 1, 1); PG8_STAGE(PG8_SB(1, 0), b3, voffB); PG8_STAGE(PG8_SB(1, 1), b3 + hstepB, voffB); PG8_STAGE(PG8_SA(1, 0), a3, voffA);
;             PG8_WAIT_V(8); PG8_WAIT_L(0); PG8_BAR; PG8_MMA(1, 0, At, B0); PG8_MMA(1, 1, At, B1); PG8_BAR; PG8_SCHED;
;         }
;         if constexpr (ALIGN_EPI) { if (wr == 0) PG8_BAR; }
	s_add_i32 s26, s87, s30
	v_lshl_add_u64 v[146:147], v[146:147], 0, s[60:61]
	s_mov_b32 m0, s26
	ds_read_b128 v[182:185], v148 offset:49152
	ds_read_b128 v[186:189], v148 offset:50176
	ds_read_b128 v[190:193], v148 offset:51200
	ds_read_b128 v[194:197], v148 offset:52224
	ds_read_b128 v[198:201], v148 offset:53248
	ds_read_b128 v[202:205], v148 offset:54272
	ds_read_b128 v[206:209], v148 offset:55296
	ds_read_b128 v[210:213], v148 offset:56320
	global_load_lds_dwordx4 v[146:147], off
	s_add_i32 m0, s26, 0x2000
	s_add_u32 s24, s24, 0x100080
	v_lshl_add_u64 v[146:147], v[214:215], 0, s[60:61]
	s_addc_u32 s25, s25, 0
	s_add_i32 s26, s88, s30
	global_load_lds_dwordx4 v[146:147], off
	v_lshl_add_u64 v[146:147], s[24:25], 0, v[134:135]
	s_mov_b32 m0, s26
	s_nop 0
	global_load_lds_dwordx4 v[146:147], off
	v_lshl_add_u64 v[146:147], s[24:25], 0, v[130:131]
	s_add_i32 m0, s26, 0x2000
	s_nop 0
	global_load_lds_dwordx4 v[146:147], off
	v_lshl_add_u64 v[146:147], v[216:217], 0, s[60:61]
	s_mov_b32 m0, s45
	s_nop 0
	global_load_lds_dwordx4 v[146:147], off
	v_lshl_add_u64 v[146:147], v[218:219], 0, s[60:61]
	s_mov_b32 m0, s50
	s_nop 0
	global_load_lds_dwordx4 v[146:147], off
	s_waitcnt vmcnt(8)
	s_waitcnt lgkmcnt(0)
	s_barrier
	s_setprio 1
	s_waitcnt lgkmcnt(0)
	v_mfma_f32_16x16x32_bf16 v[62:65], v[150:153], v[182:185], v[62:65]
	v_mfma_f32_16x16x32_bf16 v[58:61], v[158:161], v[182:185], v[58:61]
	v_mfma_f32_16x16x32_bf16 v[42:45], v[158:161], v[190:193], v[42:45]
	v_mfma_f32_16x16x32_bf16 v[50:53], v[150:153], v[190:193], v[50:53]
	v_mfma_f32_16x16x32_bf16 v[34:37], v[150:153], v[198:201], v[34:37]
	v_mfma_f32_16x16x32_bf16 v[26:29], v[158:161], v[198:201], v[26:29]
	v_mfma_f32_16x16x32_bf16 v[10:13], v[158:161], v[206:209], v[10:13]
	v_mfma_f32_16x16x32_bf16 v[18:21], v[150:153], v[206:209], v[18:21]
	v_mfma_f32_16x16x32_bf16 v[62:65], v[154:157], v[186:189], v[62:65]
	v_mfma_f32_16x16x32_bf16 v[58:61], v[162:165], v[186:189], v[58:61]
	v_mfma_f32_16x16x32_bf16 v[42:45], v[162:165], v[194:197], v[42:45]
	v_mfma_f32_16x16x32_bf16 v[50:53], v[154:157], v[194:197], v[50:53]
	v_mfma_f32_16x16x32_bf16 v[34:37], v[154:157], v[202:205], v[34:37]
	v_mfma_f32_16x16x32_bf16 v[26:29], v[162:165], v[202:205], v[26:29]
	v_mfma_f32_16x16x32_bf16 v[10:13], v[162:165], v[210:213], v[10:13]
	v_mfma_f32_16x16x32_bf16 v[18:21], v[154:157], v[210:213], v[18:21]
	s_setprio 0
	s_setprio 1
	v_mfma_f32_16x16x32_bf16 v[54:57], v[166:169], v[182:185], v[54:57]
	v_mfma_f32_16x16x32_bf16 v[46:49], v[174:177], v[182:185], v[46:49]
	v_mfma_f32_16x16x32_bf16 v[30:33], v[174:177], v[190:193], v[30:33]
	v_mfma_f32_16x16x32_bf16 v[38:41], v[166:169], v[190:193], v[38:41]
	v_mfma_f32_16x16x32_bf16 v[22:25], v[166:169], v[198:201], v[22:25]
	v_mfma_f32_16x16x32_bf16 v[14:17], v[174:177], v[198:201], v[14:17]
	v_mfma_f32_16x16x32_bf16 v[2:5], v[174:177], v[206:209], v[2:5]
	v_mfma_f32_16x16x32_bf16 v[6:9], v[166:169], v[206:209], v[6:9]
	v_mfma_f32_16x16x32_bf16 v[54:57], v[170:173], v[186:189], v[54:57]
	v_mfma_f32_16x16x32_bf16 v[46:49], v[178:181], v[186:189], v[46:49]
	v_mfma_f32_16x16x32_bf16 v[30:33], v[178:181], v[194:197], v[30:33]
	v_mfma_f32_16x16x32_bf16 v[38:41], v[170:173], v[194:197], v[38:41]
	s_setprio 0
	v_mfma_f32_16x16x32_bf16 v[22:25], v[170:173], v[202:205], v[22:25]
	v_mfma_f32_16x16x32_bf16 v[14:17], v[178:181], v[202:205], v[14:17]
	v_mfma_f32_16x16x32_bf16 v[2:5], v[178:181], v[210:213], v[2:5]
	v_mfma_f32_16x16x32_bf16 v[6:9], v[170:173], v[210:213], v[6:9]
	s_barrier
	s_add_i32 s86, s86, 2
	s_add_u32 s22, s22, 0x100
	s_addc_u32 s23, s23, 0
	s_add_u32 s84, s84, 0x100
	s_addc_u32 s85, s85, 0
	s_cmp_gt_u32 s86, 5
	s_cbranch_scc0 .LBB0_1163
	s_and_b64 vcc, exec, s[6:7]
	s_cbranch_vccz .LBB0_1166
	s_barrier

; #define PG8_STAGE(bufoff, gbase, voff) do { _Pragma("unroll") for (int _i = 0; _i < 2; ++_i) \
;         __builtin_amdgcn_global_load_lds((const unsigned*)((const char*)(gbase) + (voff)[_i]), (PG8_LAS unsigned*)(lds + (bufoff) + ldsw + _i * 8192), 16, 0, 0); } while (0)
; #define PG8_WAIT_V(n) asm volatile("s_waitcnt vmcnt(" #n ")" ::: "memory")
; #define PG8_WAIT_L(n) asm volatile("s_waitcnt lgkmcnt(" #n ")" ::: "memory")
; #define PG8_BAR __builtin_amdgcn_s_barrier()
; #define PG8_SCHED __builtin_amdgcn_sched_barrier(0)
; template <class Epi, class Sched, bool ALIGN_EPI, bool F8 = false>
; __device__ __forceinline__ void gemm_phase(PG8_LAS unsigned char* lds, const Gemm g, const Sched& S, const Epi& E, int tid) {
;     ...
;             const bool last = (t == nt - 2);
;             const char* a1 = cA + (size_t)(t + 1) * kstep;
;             const char* a2 = last ? nA : cA + (size_t)(t + 2) * kstep; const char* b2 = last ? nB : cB + (size_t)(t + 2) * kstep;
;             const char* a3 = a2 + kstep; const char* b3 = b2 + kstep;
;             if (last && has_next) S.a_ready(nxt);
;             PG8_LDB(B0, 0, 0); PG8_LDB(B1, 0, 1); PG8_SCHED; PG8_LDA(At, 0, 0); PG8_STAGE(PG8_SA(1, 1), a1 + hstepA, voffA);
;             PG8_WAIT_V(8); PG8_WAIT_L(0); PG8_BAR; PG8_MMA(0, 0, At, B0); PG8_MMA(0, 1, At, B1); PG8_BAR; PG8_SCHED;
;             PG8_LDA(At, 0, 1); PG8_STAGE(PG8_SB(0, 0), b2, voffB); PG8_STAGE(PG8_SB(0, 1), b2 + hstepB, voffB); PG8_STAGE(PG8_SA(0, 0), a2, voffA);
.LBB0_1239:
	s_add_u32 s10, s12, 0x100
	s_addc_u32 s11, s13, 0
	s_add_i32 s88, 0, 0x10000
	s_cmp_eq_u32 s25, 12
	s_cselect_b32 s31, s27, s11
	s_cselect_b32 s30, s26, s10
	s_cselect_b32 s15, s29, s7
	s_cselect_b32 s14, s28, s6
	s_add_i32 s89, 0, 0x14000
	v_add_u32_e32 v152, s88, v236
	v_add_u32_e32 v168, s89, v236
	ds_read_b128 v[140:143], v152
	ds_read_b128 v[144:147], v152 offset:1024
	ds_read_b128 v[148:151], v152 offset:2048
	ds_read_b128 v[152:155], v152 offset:3072
	ds_read_b128 v[156:159], v168
	ds_read_b128 v[160:163], v168 offset:1024
	ds_read_b128 v[164:167], v168 offset:2048
	ds_read_b128 v[168:171], v168 offset:3072
	v_lshl_add_u64 v[204:205], s[12:13], 0, v[136:137]
	s_add_i32 m0, s45, 0xc000
	ds_read_b128 v[172:175], v238
	ds_read_b128 v[176:179], v238 offset:1024
	ds_read_b128 v[180:183], v238 offset:2048
	ds_read_b128 v[184:187], v238 offset:3072
	ds_read_b128 v[188:191], v238 offset:4096
	ds_read_b128 v[192:195], v238 offset:5120
	ds_read_b128 v[196:199], v238 offset:6144
	ds_read_b128 v[200:203], v238 offset:7168
	global_load_lds_dwordx4 v[204:205], off
	v_lshl_add_u64 v[204:205], s[12:13], 0, v[138:139]
	s_add_i32 m0, s45, 0xe000
	s_nop 0
	global_load_lds_dwordx4 v[204:205], off
	s_waitcnt vmcnt(8)
	s_waitcnt lgkmcnt(0)
	s_barrier
	s_setprio 1
	s_waitcnt lgkmcnt(0)
	v_mfma_f32_16x16x32_bf16 v[126:129], v[140:143], v[172:175], v[126:129]
	v_mfma_f32_16x16x32_bf16 v[122:125], v[148:151], v[172:175], v[122:125]
	v_mfma_f32_16x16x32_bf16 v[114:117], v[148:151], v[180:183], v[114:117]
	v_mfma_f32_16x16x32_bf16 v[118:121], v[140:143], v[180:183], v[118:121]
	v_mfma_f32_16x16x32_bf16 v[110:113], v[140:143], v[188:191], v[110:113]
	v_mfma_f32_16x16x32_bf16 v[106:109], v[148:151], v[188:191], v[106:109]
	v_mfma_f32_16x16x32_bf16 v[98:101], v[148:151], v[196:199], v[98:101]
	v_mfma_f32_16x16x32_bf16 v[102:105], v[140:143], v[196:199], v[102:105]
	v_mfma_f32_16x16x32_bf16 v[126:129], v[144:147], v[176:179], v[126:129]
	v_mfma_f32_16x16x32_bf16 v[122:125], v[152:155], v[176:179], v[122:125]
	v_mfma_f32_16x16x32_bf16 v[114:117], v[152:155], v[184:187], v[114:117]
	v_mfma_f32_16x16x32_bf16 v[118:121], v[144:147], v[184:187], v[118:121]
	v_mfma_f32_16x16x32_bf16 v[110:113], v[144:147], v[192:195], v[110:113]
	v_mfma_f32_16x16x32_bf16 v[106:109], v[152:155], v[192:195], v[106:109]
	v_mfma_f32_16x16x32_bf16 v[98:101], v[152:155], v[200:203], v[98:101]
	v_mfma_f32_16x16x32_bf16 v[102:105], v[144:147], v[200:203], v[102:105]
	s_setprio 0
	s_setprio 1
	v_mfma_f32_16x16x32_bf16 v[94:97], v[156:159], v[172:175], v[94:97]
	v_mfma_f32_16x16x32_bf16 v[90:93], v[164:167], v[172:175], v[90:93]
	v_mfma_f32_16x16x32_bf16 v[82:85], v[164:167], v[180:183], v[82:85]
	v_mfma_f32_16x16x32_bf16 v[86:89], v[156:159], v[180:183], v[86:89]
	v_mfma_f32_16x16x32_bf16 v[78:81], v[156:159], v[188:191], v[78:81]
	v_mfma_f32_16x16x32_bf16 v[74:77], v[164:167], v[188:191], v[74:77]
	v_mfma_f32_16x16x32_bf16 v[66:69], v[164:167], v[196:199], v[66:69]
	v_mfma_f32_16x16x32_bf16 v[70:73], v[156:159], v[196:199], v[70:73]
	v_mfma_f32_16x16x32_bf16 v[94:97], v[160:163], v[176:179], v[94:97]
	v_mfma_f32_16x16x32_bf16 v[90:93], v[168:171], v[176:179], v[90:93]
	v_mfma_f32_16x16x32_bf16 v[82:85], v[168:171], v[184:187], v[82:85]
	v_mfma_f32_16x16x32_bf16 v[86:89], v[160:163], v[184:187], v[86:89]
	s_setprio 0
	v_mfma_f32_16x16x32_bf16 v[78:81], v[160:163], v[192:195], v[78:81]
	v_mfma_f32_16x16x32_bf16 v[74:77], v[168:171], v[192:195], v[74:77]
	v_mfma_f32_16x16x32_bf16 v[66:69], v[168:171], v[200:203], v[66:69]
	v_mfma_f32_16x16x32_bf16 v[70:73], v[160:163], v[200:203], v[70:73]
	s_barrier
	s_add_i32 s12, s88, s44
	v_lshl_add_u64 v[204:205], s[14:15], 0, v[0:1]
	s_mov_b32 m0, s12
	ds_read_b128 v[172:175], v238 offset:16384
	ds_read_b128 v[176:179], v238 offset:17408
	ds_read_b128 v[180:183], v238 offset:18432
	ds_read_b128 v[184:187], v238 offset:19456
	ds_read_b128 v[188:191], v238 offset:20480
	ds_read_b128 v[192:195], v238 offset:21504
	ds_read_b128 v[196:199], v238 offset:22528
	ds_read_b128 v[200:203], v238 offset:23552
	global_load_lds_dwordx4 v[204:205], off
	s_add_i32 m0, s12, 0x2000
	s_add_u32 s12, s14, 0xc0000
	v_lshl_add_u64 v[206:207], s[14:15], 0, v[130:131]
	s_addc_u32 s13, s15, 0
	s_add_i32 s88, s89, s44
	global_load_lds_dwordx4 v[206:207], off
	v_lshl_add_u64 v[208:209], s[12:13], 0, v[0:1]
	s_mov_b32 m0, s88
	v_lshl_add_u64 v[210:211], s[30:31], 0, v[132:133]
	global_load_lds_dwordx4 v[208:209], off
	v_lshl_add_u64 v[208:209], s[12:13], 0, v[130:131]
	s_add_i32 m0, s88, 0x2000
	s_nop 0
	global_load_lds_dwordx4 v[208:209], off
	v_lshl_add_u64 v[208:209], s[30:31], 0, v[134:135]
	s_mov_b32 m0, s45
	s_nop 0
	global_load_lds_dwordx4 v[208:209], off
	s_mov_b32 m0, s50
	s_nop 0
	global_load_lds_dwordx4 v[210:211], off
	s_waitcnt vmcnt(8)
	s_waitcnt lgkmcnt(0)
	s_barrier
; #define PG8_STAGE(bufoff, gbase, voff) do { _Pragma("unroll") for (int _i = 0; _i < 2; ++_i) \
;         __builtin_amdgcn_global_load_lds((const unsigned*)((const char*)(gbase) + (voff)[_i]), (PG8_LAS unsigned*)(lds + (bufoff) + ldsw + _i * 8192), 16, 0, 0); } while (0)
; #define PG8_WAIT_V(n) asm volatile("s_waitcnt vmcnt(" #n ")" ::: "memory")
; #define PG8_WAIT_L(n) asm volatile("s_waitcnt lgkmcnt(" #n ")" ::: "memory")
; #define PG8_BAR __builtin_amdgcn_s_barrier()
; #define PG8_SCHED __builtin_amdgcn_sched_barrier(0)
; template <class Epi, class Sched, bool ALIGN_EPI, bool F8 = false>
; __device__ __forceinline__ void gemm_phase(PG8_LAS unsigned char* lds, const Gemm g, const Sched& S, const Epi& E, int tid) {
;     ...
;             PG8_WAIT_V(8); PG8_WAIT_L(0); PG8_BAR; PG8_MMA(1, 0, At, B0); PG8_MMA(1, 1, At, B1); PG8_BAR; PG8_SCHED;
;             PG8_LDB(B0, 1, 0); PG8_LDB(B1, 1, 1); PG8_SCHED; PG8_LDA(At, 1, 0); PG8_STAGE(PG8_SA(0, 1), a2 + hstepA, voffA);
;             PG8_WAIT_V(8); PG8_WAIT_L(0); PG8_BAR; PG8_MMA(0, 0, At, B0); PG8_MMA(0, 1, At, B1); PG8_BAR; PG8_SCHED;
	s_setprio 1
	s_waitcnt lgkmcnt(0)
	v_mfma_f32_16x16x32_bf16 v[62:65], v[140:143], v[172:175], v[62:65]
	v_mfma_f32_16x16x32_bf16 v[58:61], v[148:151], v[172:175], v[58:61]
	v_mfma_f32_16x16x32_bf16 v[50:53], v[148:151], v[180:183], v[50:53]
	v_mfma_f32_16x16x32_bf16 v[54:57], v[140:143], v[180:183], v[54:57]
	v_mfma_f32_16x16x32_bf16 v[46:49], v[140:143], v[188:191], v[46:49]
	v_mfma_f32_16x16x32_bf16 v[42:45], v[148:151], v[188:191], v[42:45]
	v_mfma_f32_16x16x32_bf16 v[34:37], v[148:151], v[196:199], v[34:37]
	v_mfma_f32_16x16x32_bf16 v[38:41], v[140:143], v[196:199], v[38:41]
	v_mfma_f32_16x16x32_bf16 v[62:65], v[144:147], v[176:179], v[62:65]
	v_mfma_f32_16x16x32_bf16 v[58:61], v[152:155], v[176:179], v[58:61]
	v_mfma_f32_16x16x32_bf16 v[50:53], v[152:155], v[184:187], v[50:53]
	v_mfma_f32_16x16x32_bf16 v[54:57], v[144:147], v[184:187], v[54:57]
	v_mfma_f32_16x16x32_bf16 v[46:49], v[144:147], v[192:195], v[46:49]
	v_mfma_f32_16x16x32_bf16 v[42:45], v[152:155], v[192:195], v[42:45]
	v_mfma_f32_16x16x32_bf16 v[34:37], v[152:155], v[200:203], v[34:37]
	v_mfma_f32_16x16x32_bf16 v[38:41], v[144:147], v[200:203], v[38:41]
	s_setprio 0
	s_setprio 1
	v_mfma_f32_16x16x32_bf16 v[30:33], v[156:159], v[172:175], v[30:33]
	v_mfma_f32_16x16x32_bf16 v[26:29], v[164:167], v[172:175], v[26:29]
	v_mfma_f32_16x16x32_bf16 v[18:21], v[164:167], v[180:183], v[18:21]
	v_mfma_f32_16x16x32_bf16 v[22:25], v[156:159], v[180:183], v[22:25]
	v_mfma_f32_16x16x32_bf16 v[14:17], v[156:159], v[188:191], v[14:17]
	v_mfma_f32_16x16x32_bf16 v[10:13], v[164:167], v[188:191], v[10:13]
	v_mfma_f32_16x16x32_bf16 v[2:5], v[164:167], v[196:199], v[2:5]
	v_mfma_f32_16x16x32_bf16 v[6:9], v[156:159], v[196:199], v[6:9]
	v_mfma_f32_16x16x32_bf16 v[30:33], v[160:163], v[176:179], v[30:33]
	v_mfma_f32_16x16x32_bf16 v[26:29], v[168:171], v[176:179], v[26:29]
	v_mfma_f32_16x16x32_bf16 v[18:21], v[168:171], v[184:187], v[18:21]
	v_mfma_f32_16x16x32_bf16 v[22:25], v[160:163], v[184:187], v[22:25]
	s_setprio 0
	v_mfma_f32_16x16x32_bf16 v[14:17], v[160:163], v[192:195], v[14:17]
	v_mfma_f32_16x16x32_bf16 v[10:13], v[168:171], v[192:195], v[10:13]
	v_mfma_f32_16x16x32_bf16 v[2:5], v[168:171], v[200:203], v[2:5]
	v_mfma_f32_16x16x32_bf16 v[6:9], v[160:163], v[200:203], v[6:9]
	s_barrier
	s_add_i32 s88, 0, 0x18000
	s_add_i32 s89, 0, 0x1c000
	v_add_u32_e32 v152, s88, v236
	v_add_u32_e32 v168, s89, v236
	ds_read_b128 v[140:143], v152
	ds_read_b128 v[144:147], v152 offset:1024
	ds_read_b128 v[148:151], v152 offset:2048
	ds_read_b128 v[152:155], v152 offset:3072
	ds_read_b128 v[156:159], v168
	ds_read_b128 v[160:163], v168 offset:1024
	ds_read_b128 v[164:167], v168 offset:2048
	ds_read_b128 v[168:171], v168 offset:3072
	s_add_u32 s12, s30, 0xc0000
	s_addc_u32 s13, s31, 0
	s_mov_b32 m0, s51
	v_lshl_add_u64 v[212:213], s[12:13], 0, v[134:135]
	ds_read_b128 v[172:175], v238 offset:32768
	ds_read_b128 v[176:179], v238 offset:33792
	ds_read_b128 v[180:183], v238 offset:34816
	ds_read_b128 v[184:187], v238 offset:35840
	ds_read_b128 v[188:191], v238 offset:36864
	ds_read_b128 v[192:195], v238 offset:37888
	ds_read_b128 v[196:199], v238 offset:38912
	ds_read_b128 v[200:203], v238 offset:39936
	global_load_lds_dwordx4 v[212:213], off
	v_lshl_add_u64 v[212:213], s[12:13], 0, v[132:133]
	s_mov_b32 m0, s68
	s_nop 0
	global_load_lds_dwordx4 v[212:213], off
	s_waitcnt vmcnt(8)
	s_waitcnt lgkmcnt(0)
	s_barrier
	s_setprio 1
	s_waitcnt lgkmcnt(0)
	v_mfma_f32_16x16x32_bf16 v[126:129], v[140:143], v[172:175], v[126:129]
	v_mfma_f32_16x16x32_bf16 v[122:125], v[148:151], v[172:175], v[122:125]
	v_mfma_f32_16x16x32_bf16 v[114:117], v[148:151], v[180:183], v[114:117]
	v_mfma_f32_16x16x32_bf16 v[118:121], v[140:143], v[180:183], v[118:121]
	v_mfma_f32_16x16x32_bf16 v[110:113], v[140:143], v[188:191], v[110:113]
	v_mfma_f32_16x16x32_bf16 v[106:109], v[148:151], v[188:191], v[106:109]
	v_mfma_f32_16x16x32_bf16 v[98:101], v[148:151], v[196:199], v[98:101]
	v_mfma_f32_16x16x32_bf16 v[102:105], v[140:143], v[196:199], v[102:105]
	v_mfma_f32_16x16x32_bf16 v[126:129], v[144:147], v[176:179], v[126:129]
	v_mfma_f32_16x16x32_bf16 v[122:125], v[152:155], v[176:179], v[122:125]
	v_mfma_f32_16x16x32_bf16 v[114:117], v[152:155], v[184:187], v[114:117]
	v_mfma_f32_16x16x32_bf16 v[118:121], v[144:147], v[184:187], v[118:121]
	v_mfma_f32_16x16x32_bf16 v[110:113], v[144:147], v[192:195], v[110:113]
	v_mfma_f32_16x16x32_bf16 v[106:109], v[152:155], v[192:195], v[106:109]
	v_mfma_f32_16x16x32_bf16 v[98:101], v[152:155], v[200:203], v[98:101]
	v_mfma_f32_16x16x32_bf16 v[102:105], v[144:147], v[200:203], v[102:105]
	s_setprio 0
	s_setprio 1
	v_mfma_f32_16x16x32_bf16 v[94:97], v[156:159], v[172:175], v[94:97]
	v_mfma_f32_16x16x32_bf16 v[90:93], v[164:167], v[172:175], v[90:93]
	v_mfma_f32_16x16x32_bf16 v[82:85], v[164:167], v[180:183], v[82:85]
	v_mfma_f32_16x16x32_bf16 v[86:89], v[156:159], v[180:183], v[86:89]
	v_mfma_f32_16x16x32_bf16 v[78:81], v[156:159], v[188:191], v[78:81]
	v_mfma_f32_16x16x32_bf16 v[74:77], v[164:167], v[188:191], v[74:77]
	v_mfma_f32_16x16x32_bf16 v[66:69], v[164:167], v[196:199], v[66:69]
	v_mfma_f32_16x16x32_bf16 v[70:73], v[156:159], v[196:199], v[70:73]
	v_mfma_f32_16x16x32_bf16 v[94:97], v[160:163], v[176:179], v[94:97]
	v_mfma_f32_16x16x32_bf16 v[90:93], v[168:171], v[176:179], v[90:93]
	v_mfma_f32_16x16x32_bf16 v[82:85], v[168:171], v[184:187], v[82:85]
	v_mfma_f32_16x16x32_bf16 v[86:89], v[160:163], v[184:187], v[86:89]
	s_setprio 0
	v_mfma_f32_16x16x32_bf16 v[78:81], v[160:163], v[192:195], v[78:81]
	v_mfma_f32_16x16x32_bf16 v[74:77], v[168:171], v[192:195], v[74:77]
	v_mfma_f32_16x16x32_bf16 v[66:69], v[168:171], v[200:203], v[66:69]
	v_mfma_f32_16x16x32_bf16 v[70:73], v[160:163], v[200:203], v[70:73]
	s_barrier
; #define PG8_STAGE(bufoff, gbase, voff) do { _Pragma("unroll") for (int _i = 0; _i < 2; ++_i) \
;         __builtin_amdgcn_global_load_lds((const unsigned*)((const char*)(gbase) + (voff)[_i]), (PG8_LAS unsigned*)(lds + (bufoff) + ldsw + _i * 8192), 16, 0, 0); } while (0)
; #define PG8_WAIT_V(n) asm volatile("s_waitcnt vmcnt(" #n ")" ::: "memory")
; #define PG8_WAIT_L(n) asm volatile("s_waitcnt lgkmcnt(" #n ")" ::: "memory")
; #define PG8_BAR __builtin_amdgcn_s_barrier()
; #define PG8_SCHED __builtin_amdgcn_sched_barrier(0)
; template <class Epi, class Sched, bool ALIGN_EPI, bool F8 = false>
; __device__ __forceinline__ void gemm_phase(PG8_LAS unsigned char* lds, const Gemm g, const Sched& S, const Epi& E, int tid) {
;     ...
;             PG8_LDA(At, 1, 1); PG8_STAGE(PG8_SB(1, 0), b3, voffB); PG8_STAGE(PG8_SB(1, 1), b3 + hstepB, voffB); PG8_STAGE(PG8_SA(1, 0), a3, voffA);
;             PG8_WAIT_V(8); PG8_WAIT_L(0); PG8_BAR; PG8_MMA(1, 0, At, B0); PG8_MMA(1, 1, At, B1); PG8_BAR; PG8_SCHED;
;         }
;         if constexpr (ALIGN_EPI) { if (wr == 0) PG8_BAR; }
	s_add_i32 s12, s88, s44
	v_lshl_add_u64 v[204:205], v[204:205], 0, s[60:61]
	s_mov_b32 m0, s12
	ds_read_b128 v[172:175], v238 offset:49152
	ds_read_b128 v[176:179], v238 offset:50176
	ds_read_b128 v[180:183], v238 offset:51200
	ds_read_b128 v[184:187], v238 offset:52224
	ds_read_b128 v[188:191], v238 offset:53248
	ds_read_b128 v[192:195], v238 offset:54272
	ds_read_b128 v[196:199], v238 offset:55296
	ds_read_b128 v[200:203], v238 offset:56320
	global_load_lds_dwordx4 v[204:205], off
	s_add_i32 m0, s12, 0x2000
	s_add_u32 s12, s14, 0xc0080
	v_lshl_add_u64 v[204:205], v[206:207], 0, s[60:61]
	s_addc_u32 s13, s15, 0
	s_add_i32 s14, s89, s44
	global_load_lds_dwordx4 v[204:205], off
	v_lshl_add_u64 v[204:205], s[12:13], 0, v[0:1]
	s_mov_b32 m0, s14
	s_nop 0
	global_load_lds_dwordx4 v[204:205], off
	v_lshl_add_u64 v[204:205], s[12:13], 0, v[130:131]
	s_add_i32 m0, s14, 0x2000
	s_nop 0
	global_load_lds_dwordx4 v[204:205], off
	v_lshl_add_u64 v[204:205], v[208:209], 0, s[60:61]
	s_mov_b32 m0, s69
	s_nop 0
	global_load_lds_dwordx4 v[204:205], off
	v_lshl_add_u64 v[204:205], v[210:211], 0, s[60:61]
	s_mov_b32 m0, s82
	s_nop 0
	global_load_lds_dwordx4 v[204:205], off
	s_waitcnt vmcnt(8)
	s_waitcnt lgkmcnt(0)
	s_barrier
	s_setprio 1
	s_waitcnt lgkmcnt(0)
	v_mfma_f32_16x16x32_bf16 v[62:65], v[140:143], v[172:175], v[62:65]
	v_mfma_f32_16x16x32_bf16 v[58:61], v[148:151], v[172:175], v[58:61]
	v_mfma_f32_16x16x32_bf16 v[50:53], v[148:151], v[180:183], v[50:53]
	v_mfma_f32_16x16x32_bf16 v[54:57], v[140:143], v[180:183], v[54:57]
	v_mfma_f32_16x16x32_bf16 v[46:49], v[140:143], v[188:191], v[46:49]
	v_mfma_f32_16x16x32_bf16 v[42:45], v[148:151], v[188:191], v[42:45]
	v_mfma_f32_16x16x32_bf16 v[34:37], v[148:151], v[196:199], v[34:37]
	v_mfma_f32_16x16x32_bf16 v[38:41], v[140:143], v[196:199], v[38:41]
	v_mfma_f32_16x16x32_bf16 v[62:65], v[144:147], v[176:179], v[62:65]
	v_mfma_f32_16x16x32_bf16 v[58:61], v[152:155], v[176:179], v[58:61]
	v_mfma_f32_16x16x32_bf16 v[50:53], v[152:155], v[184:187], v[50:53]
	v_mfma_f32_16x16x32_bf16 v[54:57], v[144:147], v[184:187], v[54:57]
	v_mfma_f32_16x16x32_bf16 v[46:49], v[144:147], v[192:195], v[46:49]
	v_mfma_f32_16x16x32_bf16 v[42:45], v[152:155], v[192:195], v[42:45]
	v_mfma_f32_16x16x32_bf16 v[34:37], v[152:155], v[200:203], v[34:37]
	v_mfma_f32_16x16x32_bf16 v[38:41], v[144:147], v[200:203], v[38:41]
	s_setprio 0
	s_setprio 1
	v_mfma_f32_16x16x32_bf16 v[30:33], v[156:159], v[172:175], v[30:33]
	v_mfma_f32_16x16x32_bf16 v[26:29], v[164:167], v[172:175], v[26:29]
	v_mfma_f32_16x16x32_bf16 v[18:21], v[164:167], v[180:183], v[18:21]
	v_mfma_f32_16x16x32_bf16 v[22:25], v[156:159], v[180:183], v[22:25]
	v_mfma_f32_16x16x32_bf16 v[14:17], v[156:159], v[188:191], v[14:17]
	v_mfma_f32_16x16x32_bf16 v[10:13], v[164:167], v[188:191], v[10:13]
	v_mfma_f32_16x16x32_bf16 v[2:5], v[164:167], v[196:199], v[2:5]
	v_mfma_f32_16x16x32_bf16 v[6:9], v[156:159], v[196:199], v[6:9]
	v_mfma_f32_16x16x32_bf16 v[30:33], v[160:163], v[176:179], v[30:33]
	v_mfma_f32_16x16x32_bf16 v[26:29], v[168:171], v[176:179], v[26:29]
	v_mfma_f32_16x16x32_bf16 v[18:21], v[168:171], v[184:187], v[18:21]
	v_mfma_f32_16x16x32_bf16 v[22:25], v[160:163], v[184:187], v[22:25]
	s_setprio 0
	v_mfma_f32_16x16x32_bf16 v[14:17], v[160:163], v[192:195], v[14:17]
	v_mfma_f32_16x16x32_bf16 v[10:13], v[168:171], v[192:195], v[10:13]
	v_mfma_f32_16x16x32_bf16 v[2:5], v[168:171], v[200:203], v[2:5]
	v_mfma_f32_16x16x32_bf16 v[6:9], v[160:163], v[200:203], v[6:9]
	s_barrier
	s_add_i32 s25, s25, 2
	s_add_u32 s6, s6, 0x100
	s_addc_u32 s7, s7, 0
	s_cmp_gt_u32 s25, 13
	s_mov_b64 s[12:13], s[10:11]
	s_cbranch_scc0 .LBB0_1239
	s_and_b64 vcc, exec, s[22:23]
	s_cbranch_vccz .LBB0_1242
	s_barrier

; #define PG8_STAGE(bufoff, gbase, voff) do { _Pragma("unroll") for (int _i = 0; _i < 2; ++_i) \
;         __builtin_amdgcn_global_load_lds((const unsigned*)((const char*)(gbase) + (voff)[_i]), (PG8_LAS unsigned*)(lds + (bufoff) + ldsw + _i * 8192), 16, 0, 0); } while (0)
; #define PG8_WAIT_V(n) asm volatile("s_waitcnt vmcnt(" #n ")" ::: "memory")
; #define PG8_WAIT_L(n) asm volatile("s_waitcnt lgkmcnt(" #n ")" ::: "memory")
; #define PG8_BAR __builtin_amdgcn_s_barrier()
; #define PG8_SCHED __builtin_amdgcn_sched_barrier(0)
; template <class Epi, class Sched, bool ALIGN_EPI, bool F8 = false>
; __device__ __forceinline__ void gemm_phase(PG8_LAS unsigned char* lds, const Gemm g, const Sched& S, const Epi& E, int tid) {
;     ...
;             const bool last = (t == nt - 2);
;             const char* a1 = cA + (size_t)(t + 1) * kstep;
;             const char* a2 = last ? nA : cA + (size_t)(t + 2) * kstep; const char* b2 = last ? nB : cB + (size_t)(t + 2) * kstep;
;             const char* a3 = a2 + kstep; const char* b3 = b2 + kstep;
;             if (last && has_next) S.a_ready(nxt);
;             PG8_LDB(B0, 0, 0); PG8_LDB(B1, 0, 1); PG8_SCHED; PG8_LDA(At, 0, 0); PG8_STAGE(PG8_SA(1, 1), a1 + hstepA, voffA);
;             PG8_WAIT_V(8); PG8_WAIT_L(0); PG8_BAR; PG8_MMA(0, 0, At, B0); PG8_MMA(0, 1, At, B1); PG8_BAR; PG8_SCHED;
;             PG8_LDA(At, 0, 1); PG8_STAGE(PG8_SB(0, 0), b2, voffB); PG8_STAGE(PG8_SB(0, 1), b2 + hstepB, voffB); PG8_STAGE(PG8_SA(0, 0), a2, voffA);
.LBB0_1397:
	s_add_u32 s7, s24, 0xfff80080
	s_addc_u32 s26, s25, -1
	s_add_i32 s50, 0, 0x10000
	s_cmp_eq_u32 s6, 28
	s_cselect_b32 s29, s21, s26
	s_cselect_b32 s28, s20, s7
	s_cselect_b32 s27, s23, s19
	s_cselect_b32 s26, s22, s17
	s_add_i32 s7, 0, 0x14000
	v_add_u32_e32 v142, s50, v201
	v_add_u32_e32 v168, s7, v201
	ds_read_b128 v[130:133], v142
	ds_read_b128 v[134:137], v142 offset:1024
	ds_read_b128 v[138:141], v142 offset:2048
	ds_read_b128 v[142:145], v142 offset:3072
	ds_read_b128 v[146:149], v168
	ds_read_b128 v[150:153], v168 offset:1024
	ds_read_b128 v[154:157], v168 offset:2048
	ds_read_b128 v[168:171], v168 offset:3072
	v_lshl_add_u64 v[208:209], s[24:25], 0, v[164:165]
	s_add_i32 m0, s38, 0xc000
	ds_read_b128 v[172:175], v203
	ds_read_b128 v[176:179], v203 offset:1024
	ds_read_b128 v[180:183], v203 offset:2048
	ds_read_b128 v[184:187], v203 offset:3072
	ds_read_b128 v[188:191], v203 offset:4096
	ds_read_b128 v[192:195], v203 offset:5120
	ds_read_b128 v[196:199], v203 offset:6144
	ds_read_b128 v[204:207], v203 offset:7168
	global_load_lds_dwordx4 v[208:209], off
	v_lshl_add_u64 v[208:209], s[24:25], 0, v[166:167]
	s_add_i32 m0, s38, 0xe000
	s_nop 0
	global_load_lds_dwordx4 v[208:209], off
	s_waitcnt vmcnt(8)
	s_waitcnt lgkmcnt(0)
	s_barrier
	s_setprio 1
	s_waitcnt lgkmcnt(0)
	v_mfma_f32_16x16x32_bf16 v[126:129], v[130:133], v[172:175], v[126:129]
	v_mfma_f32_16x16x32_bf16 v[122:125], v[138:141], v[172:175], v[122:125]
	v_mfma_f32_16x16x32_bf16 v[106:109], v[138:141], v[180:183], v[106:109]
	v_mfma_f32_16x16x32_bf16 v[110:113], v[130:133], v[180:183], v[110:113]
	v_mfma_f32_16x16x32_bf16 v[94:97], v[130:133], v[188:191], v[94:97]
	v_mfma_f32_16x16x32_bf16 v[90:93], v[138:141], v[188:191], v[90:93]
	v_mfma_f32_16x16x32_bf16 v[74:77], v[138:141], v[196:199], v[74:77]
	v_mfma_f32_16x16x32_bf16 v[78:81], v[130:133], v[196:199], v[78:81]
	v_mfma_f32_16x16x32_bf16 v[126:129], v[134:137], v[176:179], v[126:129]
	v_mfma_f32_16x16x32_bf16 v[122:125], v[142:145], v[176:179], v[122:125]
	v_mfma_f32_16x16x32_bf16 v[106:109], v[142:145], v[184:187], v[106:109]
	v_mfma_f32_16x16x32_bf16 v[110:113], v[134:137], v[184:187], v[110:113]
	v_mfma_f32_16x16x32_bf16 v[94:97], v[134:137], v[192:195], v[94:97]
	v_mfma_f32_16x16x32_bf16 v[90:93], v[142:145], v[192:195], v[90:93]
	v_mfma_f32_16x16x32_bf16 v[74:77], v[142:145], v[204:207], v[74:77]
	v_mfma_f32_16x16x32_bf16 v[78:81], v[134:137], v[204:207], v[78:81]
	s_setprio 0
	s_setprio 1
	v_mfma_f32_16x16x32_bf16 v[118:121], v[146:149], v[172:175], v[118:121]
	v_mfma_f32_16x16x32_bf16 v[114:117], v[154:157], v[172:175], v[114:117]
	v_mfma_f32_16x16x32_bf16 v[98:101], v[154:157], v[180:183], v[98:101]
	v_mfma_f32_16x16x32_bf16 v[102:105], v[146:149], v[180:183], v[102:105]
	v_mfma_f32_16x16x32_bf16 v[86:89], v[146:149], v[188:191], v[86:89]
	v_mfma_f32_16x16x32_bf16 v[82:85], v[154:157], v[188:191], v[82:85]
	v_mfma_f32_16x16x32_bf16 v[66:69], v[154:157], v[196:199], v[66:69]
	v_mfma_f32_16x16x32_bf16 v[70:73], v[146:149], v[196:199], v[70:73]
	v_mfma_f32_16x16x32_bf16 v[118:121], v[150:153], v[176:179], v[118:121]
	v_mfma_f32_16x16x32_bf16 v[114:117], v[168:171], v[176:179], v[114:117]
	v_mfma_f32_16x16x32_bf16 v[98:101], v[168:171], v[184:187], v[98:101]
	v_mfma_f32_16x16x32_bf16 v[102:105], v[150:153], v[184:187], v[102:105]
	s_setprio 0
	v_mfma_f32_16x16x32_bf16 v[86:89], v[150:153], v[192:195], v[86:89]
	v_mfma_f32_16x16x32_bf16 v[82:85], v[168:171], v[192:195], v[82:85]
	v_mfma_f32_16x16x32_bf16 v[66:69], v[168:171], v[204:207], v[66:69]
	v_mfma_f32_16x16x32_bf16 v[70:73], v[150:153], v[204:207], v[70:73]
	s_barrier
	s_add_i32 s50, s50, s35
	v_lshl_add_u64 v[208:209], s[26:27], 0, v[0:1]
	s_mov_b32 m0, s50
	ds_read_b128 v[172:175], v203 offset:16384
	ds_read_b128 v[176:179], v203 offset:17408
	ds_read_b128 v[180:183], v203 offset:18432
	ds_read_b128 v[184:187], v203 offset:19456
	ds_read_b128 v[188:191], v203 offset:20480
	ds_read_b128 v[192:195], v203 offset:21504
	ds_read_b128 v[196:199], v203 offset:22528
	ds_read_b128 v[204:207], v203 offset:23552
	global_load_lds_dwordx4 v[208:209], off
	s_add_i32 m0, s50, 0x2000
	s_add_u32 s86, s26, 0x80000
	v_lshl_add_u64 v[210:211], s[26:27], 0, v[158:159]
	s_addc_u32 s87, s27, 0
	s_add_i32 s7, s7, s35
	global_load_lds_dwordx4 v[210:211], off
	v_lshl_add_u64 v[212:213], s[86:87], 0, v[0:1]
	s_mov_b32 m0, s7
	v_lshl_add_u64 v[214:215], s[28:29], 0, v[160:161]
	global_load_lds_dwordx4 v[212:213], off
	v_lshl_add_u64 v[212:213], s[86:87], 0, v[158:159]
	s_add_i32 m0, s7, 0x2000
	s_nop 0
	global_load_lds_dwordx4 v[212:213], off
	v_lshl_add_u64 v[212:213], s[28:29], 0, v[162:163]
	s_mov_b32 m0, s38
	s_nop 0
	global_load_lds_dwordx4 v[212:213], off
	s_mov_b32 m0, s39
	s_nop 0
	global_load_lds_dwordx4 v[214:215], off
	s_waitcnt vmcnt(8)
	s_waitcnt lgkmcnt(0)
	s_barrier
; #define PG8_STAGE(bufoff, gbase, voff) do { _Pragma("unroll") for (int _i = 0; _i < 2; ++_i) \
;         __builtin_amdgcn_global_load_lds((const unsigned*)((const char*)(gbase) + (voff)[_i]), (PG8_LAS unsigned*)(lds + (bufoff) + ldsw + _i * 8192), 16, 0, 0); } while (0)
; #define PG8_WAIT_V(n) asm volatile("s_waitcnt vmcnt(" #n ")" ::: "memory")
; #define PG8_WAIT_L(n) asm volatile("s_waitcnt lgkmcnt(" #n ")" ::: "memory")
; #define PG8_BAR __builtin_amdgcn_s_barrier()
; #define PG8_SCHED __builtin_amdgcn_sched_barrier(0)
; template <class Epi, class Sched, bool ALIGN_EPI, bool F8 = false>
; __device__ __forceinline__ void gemm_phase(PG8_LAS unsigned char* lds, const Gemm g, const Sched& S, const Epi& E, int tid) {
;     ...
;             PG8_WAIT_V(8); PG8_WAIT_L(0); PG8_BAR; PG8_MMA(1, 0, At, B0); PG8_MMA(1, 1, At, B1); PG8_BAR; PG8_SCHED;
;             PG8_LDB(B0, 1, 0); PG8_LDB(B1, 1, 1); PG8_SCHED; PG8_LDA(At, 1, 0); PG8_STAGE(PG8_SA(0, 1), a2 + hstepA, voffA);
;             PG8_WAIT_V(8); PG8_WAIT_L(0); PG8_BAR; PG8_MMA(0, 0, At, B0); PG8_MMA(0, 1, At, B1); PG8_BAR; PG8_SCHED;
	s_setprio 1
	s_waitcnt lgkmcnt(0)
	v_mfma_f32_16x16x32_bf16 v[62:65], v[130:133], v[172:175], v[62:65]
	v_mfma_f32_16x16x32_bf16 v[58:61], v[138:141], v[172:175], v[58:61]
	v_mfma_f32_16x16x32_bf16 v[42:45], v[138:141], v[180:183], v[42:45]
	v_mfma_f32_16x16x32_bf16 v[46:49], v[130:133], v[180:183], v[46:49]
	v_mfma_f32_16x16x32_bf16 v[30:33], v[130:133], v[188:191], v[30:33]
	v_mfma_f32_16x16x32_bf16 v[26:29], v[138:141], v[188:191], v[26:29]
	v_mfma_f32_16x16x32_bf16 v[10:13], v[138:141], v[196:199], v[10:13]
	v_mfma_f32_16x16x32_bf16 v[14:17], v[130:133], v[196:199], v[14:17]
	v_mfma_f32_16x16x32_bf16 v[62:65], v[134:137], v[176:179], v[62:65]
	v_mfma_f32_16x16x32_bf16 v[58:61], v[142:145], v[176:179], v[58:61]
	v_mfma_f32_16x16x32_bf16 v[42:45], v[142:145], v[184:187], v[42:45]
	v_mfma_f32_16x16x32_bf16 v[46:49], v[134:137], v[184:187], v[46:49]
	v_mfma_f32_16x16x32_bf16 v[30:33], v[134:137], v[192:195], v[30:33]
	v_mfma_f32_16x16x32_bf16 v[26:29], v[142:145], v[192:195], v[26:29]
	v_mfma_f32_16x16x32_bf16 v[10:13], v[142:145], v[204:207], v[10:13]
	v_mfma_f32_16x16x32_bf16 v[14:17], v[134:137], v[204:207], v[14:17]
	s_setprio 0
	s_setprio 1
	v_mfma_f32_16x16x32_bf16 v[54:57], v[146:149], v[172:175], v[54:57]
	v_mfma_f32_16x16x32_bf16 v[50:53], v[154:157], v[172:175], v[50:53]
	v_mfma_f32_16x16x32_bf16 v[34:37], v[154:157], v[180:183], v[34:37]
	v_mfma_f32_16x16x32_bf16 v[38:41], v[146:149], v[180:183], v[38:41]
	v_mfma_f32_16x16x32_bf16 v[22:25], v[146:149], v[188:191], v[22:25]
	v_mfma_f32_16x16x32_bf16 v[18:21], v[154:157], v[188:191], v[18:21]
	v_mfma_f32_16x16x32_bf16 v[2:5], v[154:157], v[196:199], v[2:5]
	v_mfma_f32_16x16x32_bf16 v[6:9], v[146:149], v[196:199], v[6:9]
	v_mfma_f32_16x16x32_bf16 v[54:57], v[150:153], v[176:179], v[54:57]
	v_mfma_f32_16x16x32_bf16 v[50:53], v[168:171], v[176:179], v[50:53]
	v_mfma_f32_16x16x32_bf16 v[34:37], v[168:171], v[184:187], v[34:37]
	v_mfma_f32_16x16x32_bf16 v[38:41], v[150:153], v[184:187], v[38:41]
	s_setprio 0
	v_mfma_f32_16x16x32_bf16 v[22:25], v[150:153], v[192:195], v[22:25]
	v_mfma_f32_16x16x32_bf16 v[18:21], v[168:171], v[192:195], v[18:21]
	v_mfma_f32_16x16x32_bf16 v[2:5], v[168:171], v[204:207], v[2:5]
	v_mfma_f32_16x16x32_bf16 v[6:9], v[150:153], v[204:207], v[6:9]
	s_barrier
	s_add_i32 s7, 0, 0x18000
	s_add_i32 s50, 0, 0x1c000
	v_add_u32_e32 v142, s7, v201
	v_add_u32_e32 v168, s50, v201
	ds_read_b128 v[130:133], v142
	ds_read_b128 v[134:137], v142 offset:1024
	ds_read_b128 v[138:141], v142 offset:2048
	ds_read_b128 v[142:145], v142 offset:3072
	ds_read_b128 v[146:149], v168
	ds_read_b128 v[150:153], v168 offset:1024
	ds_read_b128 v[154:157], v168 offset:2048
	ds_read_b128 v[168:171], v168 offset:3072
	s_add_u32 s28, s28, 0x80000
	s_addc_u32 s29, s29, 0
	s_mov_b32 m0, s44
	v_lshl_add_u64 v[216:217], s[28:29], 0, v[162:163]
	ds_read_b128 v[172:175], v203 offset:32768
	ds_read_b128 v[176:179], v203 offset:33792
	ds_read_b128 v[180:183], v203 offset:34816
	ds_read_b128 v[184:187], v203 offset:35840
	ds_read_b128 v[188:191], v203 offset:36864
	ds_read_b128 v[192:195], v203 offset:37888
	ds_read_b128 v[196:199], v203 offset:38912
	ds_read_b128 v[204:207], v203 offset:39936
	global_load_lds_dwordx4 v[216:217], off
	v_lshl_add_u64 v[216:217], s[28:29], 0, v[160:161]
	s_mov_b32 m0, s45
	s_nop 0
	global_load_lds_dwordx4 v[216:217], off
	s_waitcnt vmcnt(8)
	s_waitcnt lgkmcnt(0)
	s_barrier
	s_setprio 1
	s_waitcnt lgkmcnt(0)
	v_mfma_f32_16x16x32_bf16 v[126:129], v[130:133], v[172:175], v[126:129]
	v_mfma_f32_16x16x32_bf16 v[122:125], v[138:141], v[172:175], v[122:125]
	v_mfma_f32_16x16x32_bf16 v[106:109], v[138:141], v[180:183], v[106:109]
	v_mfma_f32_16x16x32_bf16 v[110:113], v[130:133], v[180:183], v[110:113]
	v_mfma_f32_16x16x32_bf16 v[94:97], v[130:133], v[188:191], v[94:97]
	v_mfma_f32_16x16x32_bf16 v[90:93], v[138:141], v[188:191], v[90:93]
	v_mfma_f32_16x16x32_bf16 v[74:77], v[138:141], v[196:199], v[74:77]
	v_mfma_f32_16x16x32_bf16 v[78:81], v[130:133], v[196:199], v[78:81]
	v_mfma_f32_16x16x32_bf16 v[126:129], v[134:137], v[176:179], v[126:129]
	v_mfma_f32_16x16x32_bf16 v[122:125], v[142:145], v[176:179], v[122:125]
	v_mfma_f32_16x16x32_bf16 v[106:109], v[142:145], v[184:187], v[106:109]
	v_mfma_f32_16x16x32_bf16 v[110:113], v[134:137], v[184:187], v[110:113]
	v_mfma_f32_16x16x32_bf16 v[94:97], v[134:137], v[192:195], v[94:97]
	v_mfma_f32_16x16x32_bf16 v[90:93], v[142:145], v[192:195], v[90:93]
	v_mfma_f32_16x16x32_bf16 v[74:77], v[142:145], v[204:207], v[74:77]
	v_mfma_f32_16x16x32_bf16 v[78:81], v[134:137], v[204:207], v[78:81]
	s_setprio 0
	s_setprio 1
	v_mfma_f32_16x16x32_bf16 v[118:121], v[146:149], v[172:175], v[118:121]
	v_mfma_f32_16x16x32_bf16 v[114:117], v[154:157], v[172:175], v[114:117]
	v_mfma_f32_16x16x32_bf16 v[98:101], v[154:157], v[180:183], v[98:101]
	v_mfma_f32_16x16x32_bf16 v[102:105], v[146:149], v[180:183], v[102:105]
	v_mfma_f32_16x16x32_bf16 v[86:89], v[146:149], v[188:191], v[86:89]
	v_mfma_f32_16x16x32_bf16 v[82:85], v[154:157], v[188:191], v[82:85]
	v_mfma_f32_16x16x32_bf16 v[66:69], v[154:157], v[196:199], v[66:69]
	v_mfma_f32_16x16x32_bf16 v[70:73], v[146:149], v[196:199], v[70:73]
	v_mfma_f32_16x16x32_bf16 v[118:121], v[150:153], v[176:179], v[118:121]
	v_mfma_f32_16x16x32_bf16 v[114:117], v[168:171], v[176:179], v[114:117]
	v_mfma_f32_16x16x32_bf16 v[98:101], v[168:171], v[184:187], v[98:101]
	v_mfma_f32_16x16x32_bf16 v[102:105], v[150:153], v[184:187], v[102:105]
	s_setprio 0
	v_mfma_f32_16x16x32_bf16 v[86:89], v[150:153], v[192:195], v[86:89]
	v_mfma_f32_16x16x32_bf16 v[82:85], v[168:171], v[192:195], v[82:85]
	v_mfma_f32_16x16x32_bf16 v[66:69], v[168:171], v[204:207], v[66:69]
	v_mfma_f32_16x16x32_bf16 v[70:73], v[150:153], v[204:207], v[70:73]
	s_barrier
; #define PG8_STAGE(bufoff, gbase, voff) do { _Pragma("unroll") for (int _i = 0; _i < 2; ++_i) \
;         __builtin_amdgcn_global_load_lds((const unsigned*)((const char*)(gbase) + (voff)[_i]), (PG8_LAS unsigned*)(lds + (bufoff) + ldsw + _i * 8192), 16, 0, 0); } while (0)
; #define PG8_WAIT_V(n) asm volatile("s_waitcnt vmcnt(" #n ")" ::: "memory")
; #define PG8_WAIT_L(n) asm volatile("s_waitcnt lgkmcnt(" #n ")" ::: "memory")
; #define PG8_BAR __builtin_amdgcn_s_barrier()
; #define PG8_SCHED __builtin_amdgcn_sched_barrier(0)
; template <class Epi, class Sched, bool ALIGN_EPI, bool F8 = false>
; __device__ __forceinline__ void gemm_phase(PG8_LAS unsigned char* lds, const Gemm g, const Sched& S, const Epi& E, int tid) {
;     ...
;             PG8_LDA(At, 1, 1); PG8_STAGE(PG8_SB(1, 0), b3, voffB); PG8_STAGE(PG8_SB(1, 1), b3 + hstepB, voffB); PG8_STAGE(PG8_SA(1, 0), a3, voffA);
;             PG8_WAIT_V(8); PG8_WAIT_L(0); PG8_BAR; PG8_MMA(1, 0, At, B0); PG8_MMA(1, 1, At, B1); PG8_BAR; PG8_SCHED;
;         }
	s_add_i32 s7, s7, s35
	v_lshl_add_u64 v[208:209], v[208:209], 0, s[60:61]
	s_mov_b32 m0, s7
	ds_read_b128 v[172:175], v203 offset:49152
	ds_read_b128 v[176:179], v203 offset:50176
	ds_read_b128 v[180:183], v203 offset:51200
	ds_read_b128 v[184:187], v203 offset:52224
	ds_read_b128 v[188:191], v203 offset:53248
	ds_read_b128 v[192:195], v203 offset:54272
	ds_read_b128 v[196:199], v203 offset:55296
	ds_read_b128 v[204:207], v203 offset:56320
	global_load_lds_dwordx4 v[208:209], off
	s_add_i32 m0, s7, 0x2000
	s_add_u32 s26, s26, 0x80080
	v_lshl_add_u64 v[208:209], v[210:211], 0, s[60:61]
	s_addc_u32 s27, s27, 0
	s_add_i32 s7, s50, s35
	global_load_lds_dwordx4 v[208:209], off
	v_lshl_add_u64 v[208:209], s[26:27], 0, v[0:1]
	s_mov_b32 m0, s7
	s_nop 0
	global_load_lds_dwordx4 v[208:209], off
	v_lshl_add_u64 v[208:209], s[26:27], 0, v[158:159]
	s_add_i32 m0, s7, 0x2000
	s_nop 0
	global_load_lds_dwordx4 v[208:209], off
	v_lshl_add_u64 v[208:209], v[212:213], 0, s[60:61]
	s_mov_b32 m0, s68
	s_nop 0
	global_load_lds_dwordx4 v[208:209], off
	v_lshl_add_u64 v[208:209], v[214:215], 0, s[60:61]
	s_mov_b32 m0, s69
	s_nop 0
	global_load_lds_dwordx4 v[208:209], off
	s_waitcnt vmcnt(8)
	s_waitcnt lgkmcnt(0)
	s_barrier
	s_setprio 1
	s_waitcnt lgkmcnt(0)
	v_mfma_f32_16x16x32_bf16 v[62:65], v[130:133], v[172:175], v[62:65]
	v_mfma_f32_16x16x32_bf16 v[58:61], v[138:141], v[172:175], v[58:61]
	v_mfma_f32_16x16x32_bf16 v[42:45], v[138:141], v[180:183], v[42:45]
	v_mfma_f32_16x16x32_bf16 v[46:49], v[130:133], v[180:183], v[46:49]
	v_mfma_f32_16x16x32_bf16 v[30:33], v[130:133], v[188:191], v[30:33]
	v_mfma_f32_16x16x32_bf16 v[26:29], v[138:141], v[188:191], v[26:29]
	v_mfma_f32_16x16x32_bf16 v[10:13], v[138:141], v[196:199], v[10:13]
	v_mfma_f32_16x16x32_bf16 v[14:17], v[130:133], v[196:199], v[14:17]
	v_mfma_f32_16x16x32_bf16 v[62:65], v[134:137], v[176:179], v[62:65]
	v_mfma_f32_16x16x32_bf16 v[58:61], v[142:145], v[176:179], v[58:61]
	v_mfma_f32_16x16x32_bf16 v[42:45], v[142:145], v[184:187], v[42:45]
	v_mfma_f32_16x16x32_bf16 v[46:49], v[134:137], v[184:187], v[46:49]
	v_mfma_f32_16x16x32_bf16 v[30:33], v[134:137], v[192:195], v[30:33]
	v_mfma_f32_16x16x32_bf16 v[26:29], v[142:145], v[192:195], v[26:29]
	v_mfma_f32_16x16x32_bf16 v[10:13], v[142:145], v[204:207], v[10:13]
	v_mfma_f32_16x16x32_bf16 v[14:17], v[134:137], v[204:207], v[14:17]
	s_setprio 0
	s_setprio 1
	v_mfma_f32_16x16x32_bf16 v[54:57], v[146:149], v[172:175], v[54:57]
	v_mfma_f32_16x16x32_bf16 v[50:53], v[154:157], v[172:175], v[50:53]
	v_mfma_f32_16x16x32_bf16 v[34:37], v[154:157], v[180:183], v[34:37]
	v_mfma_f32_16x16x32_bf16 v[38:41], v[146:149], v[180:183], v[38:41]
	v_mfma_f32_16x16x32_bf16 v[22:25], v[146:149], v[188:191], v[22:25]
	v_mfma_f32_16x16x32_bf16 v[18:21], v[154:157], v[188:191], v[18:21]
	v_mfma_f32_16x16x32_bf16 v[2:5], v[154:157], v[196:199], v[2:5]
	v_mfma_f32_16x16x32_bf16 v[6:9], v[146:149], v[196:199], v[6:9]
	v_mfma_f32_16x16x32_bf16 v[54:57], v[150:153], v[176:179], v[54:57]
	v_mfma_f32_16x16x32_bf16 v[50:53], v[168:171], v[176:179], v[50:53]
	v_mfma_f32_16x16x32_bf16 v[34:37], v[168:171], v[184:187], v[34:37]
	v_mfma_f32_16x16x32_bf16 v[38:41], v[150:153], v[184:187], v[38:41]
	s_setprio 0
	v_mfma_f32_16x16x32_bf16 v[22:25], v[150:153], v[192:195], v[22:25]
	v_mfma_f32_16x16x32_bf16 v[18:21], v[168:171], v[192:195], v[18:21]
	v_mfma_f32_16x16x32_bf16 v[2:5], v[168:171], v[204:207], v[2:5]
	v_mfma_f32_16x16x32_bf16 v[6:9], v[150:153], v[204:207], v[6:9]
	s_barrier
	s_add_i32 s6, s6, 2
	s_add_u32 s24, s24, 0x100
	s_addc_u32 s25, s25, 0
	s_add_u32 s17, s17, 0x100
	s_addc_u32 s19, s19, 0
	s_cmp_gt_u32 s6, 29
	s_cbranch_scc0 .LBB0_1397
; __device__ __forceinline__ float sum_xor16(float v) { auto r = __builtin_amdgcn_permlane16_swap(__float_as_uint(v), __float_as_uint(v), false, false); return __uint_as_float(r[0]) + __uint_as_float(r[1]); }
; __device__ __forceinline__ float sum_xor32(float v) { auto r = __builtin_amdgcn_permlane32_swap(__float_as_uint(v), __float_as_uint(v), false, false); return __uint_as_float(r[0]) + __uint_as_float(r[1]); }
; __device__ __forceinline__ unsigned cvt_pk_bf16(float lo, float hi) { unsigned r; asm volatile("v_cvt_pk_bf16_f32 %0, %1, %2" : "=v"(r) : "v"(lo), "v"(hi)); return r; }
; __device__ __forceinline__ float bf_lo(unsigned w) { return __uint_as_float(w << 16); }
; __device__ __forceinline__ float bf_hi(unsigned w) { return __uint_as_float(w & 0xffff0000u); }
;     __device__ __forceinline__ void operator()(const f32x4 (&acc)[2][2][4][2], const Unit& u, int wr, int wc, int fr, int fq) const {
;     ...
;                 for (int bj = 0; bj < 2; ++bj) old[m][bj] = *(const u32x4*)(xb + (size_t)(row0 + ai * HALF + m * 16) * 2048 + col0 + bj * HALF);
; #pragma unroll
;             for (int m = 0; m < 4; ++m) { const size_t row = (size_t)(row0 + ai * HALF + m * 16); bf16_t* rowp = xb + row * 2048 + col0; float ss = 0.f;
; #pragma unroll
;                 for (int bj = 0; bj < 2; ++bj) { const u32x4 oo = old[m][bj]; const f32x4 a0 = acc[ai][bj][m][0], a1 = acc[ai][bj][m][1];
;                     const float x0 = a0[0] + bf_lo(oo.x), x1 = a0[1] + bf_hi(oo.x), x2 = a0[2] + bf_lo(oo.y), x3 = a0[3] + bf_hi(oo.y), x4 = a1[0] + bf_lo(oo.z), x5 = a1[1] + bf_hi(oo.z), x6 = a1[2] + bf_lo(oo.w), x7 = a1[3] + bf_hi(oo.w);
;                     ss += (x0 * x0 + x1 * x1) + (x2 * x2 + x3 * x3) + (x4 * x4 + x5 * x5) + (x6 * x6 + x7 * x7);
;                     u32x4 w; w.x = cvt_pk_bf16(x0, x1); w.y = cvt_pk_bf16(x2, x3); w.z = cvt_pk_bf16(x4, x5); w.w = cvt_pk_bf16(x6, x7);
;                     *(u32x4*)(rowp + bj * HALF) = w;
;                     if (h8) { u32x2 q; q.x = pk4_fp8_(x0 * F8_SA_, x1 * F8_SA_, x2 * F8_SA_, x3 * F8_SA_); q.y = pk4_fp8_(x4 * F8_SA_, x5 * F8_SA_, x6 * F8_SA_, x7 * F8_SA_);
;                         *(u32x2*)(h8 + row * 2048 + col0 + bj * HALF) = q; } }
;                 ss = sum_xor32(sum_xor16(ss));
;                 if (fq == 0) SS[row * 32 + u.pn * 4 + wc] = ss; }
	v_lshl_or_b32 v168, s83, 8, v202
	v_lshl_add_u32 v172, s84, 8, v200
	v_ashrrev_i32_e32 v169, 31, v168
	v_lshlrev_b64 v[182:183], 1, v[168:169]
	v_ashrrev_i32_e32 v173, 31, v172
	v_lshl_add_u64 v[170:171], s[12:13], 0, v[182:183]
	v_lshlrev_b64 v[184:185], 12, v[172:173]
	v_lshl_add_u64 v[130:131], v[170:171], 0, v[184:185]
	global_load_dwordx4 v[178:181], v[130:131], off
	global_load_dwordx4 v[154:157], v[130:131], off offset:256
	v_or_b32_e32 v192, 16, v172
	v_ashrrev_i32_e32 v193, 31, v192
	v_or_b32_e32 v176, 32, v172
	v_lshlrev_b64 v[196:197], 12, v[192:193]
	v_ashrrev_i32_e32 v177, 31, v176
	v_or_b32_e32 v174, 48, v172
	v_lshl_add_u64 v[130:131], v[170:171], 0, v[196:197]
	v_lshlrev_b64 v[194:195], 12, v[176:177]
	v_ashrrev_i32_e32 v175, 31, v174
	global_load_dwordx4 v[150:153], v[130:131], off
	global_load_dwordx4 v[146:149], v[130:131], off offset:256
	v_lshl_add_u64 v[130:131], v[170:171], 0, v[194:195]
	v_lshlrev_b64 v[190:191], 12, v[174:175]
	global_load_dwordx4 v[142:145], v[130:131], off
	global_load_dwordx4 v[138:141], v[130:131], off offset:256
	v_lshl_add_u64 v[130:131], v[170:171], 0, v[190:191]
	global_load_dwordx4 v[134:137], v[130:131], off
	s_nop 0
	global_load_dwordx4 v[130:133], v[130:131], off offset:256
	v_lshl_add_u64 v[184:185], s[12:13], 0, v[184:185]
	v_lshl_add_u64 v[198:199], v[184:185], 0, v[182:183]
	s_waitcnt vmcnt(0)
	v_lshlrev_b32_e32 v182, 16, v178
	v_and_b32_e32 v178, 0xffff0000, v178
	v_add_f32_e32 v127, v127, v178
	v_lshlrev_b32_e32 v178, 16, v179
	v_add_f32_e32 v128, v128, v178
	v_and_b32_e32 v178, 0xffff0000, v179
	v_add_f32_e32 v129, v129, v178
	v_lshlrev_b32_e32 v178, 16, v180
	v_add_f32_e32 v178, v122, v178
	v_and_b32_e32 v122, 0xffff0000, v180
	v_add_f32_e32 v179, v123, v122
	v_lshlrev_b32_e32 v122, 16, v181
	v_add_f32_e32 v180, v124, v122
	v_and_b32_e32 v122, 0xffff0000, v181
	v_add_f32_e32 v126, v126, v182
	v_add_f32_e32 v125, v125, v122
	v_mul_f32_e32 v122, v127, v127
	v_mul_f32_e32 v123, v129, v129
	v_fmac_f32_e32 v122, v126, v126
	v_fmac_f32_e32 v123, v128, v128
	v_add_f32_e32 v122, v122, v123
	v_mul_f32_e32 v123, v179, v179
	v_fmac_f32_e32 v123, v178, v178
	v_add_f32_e32 v122, v123, v122
	v_mul_f32_e32 v123, v125, v125
	v_fmac_f32_e32 v123, v180, v180
	v_add_f32_e32 v181, v123, v122
	v_cvt_pk_bf16_f32 v122, v126, v127
	v_cvt_pk_bf16_f32 v123, v128, v129
	v_cvt_pk_bf16_f32 v124, v178, v179
	v_cvt_pk_bf16_f32 v125, v180, v125
	global_store_dwordx4 v[198:199], v[122:125], off
	s_nop 1
	v_lshlrev_b32_e32 v122, 16, v154
	v_add_f32_e32 v118, v118, v122
	v_and_b32_e32 v122, 0xffff0000, v154
	v_add_f32_e32 v119, v119, v122
	v_lshlrev_b32_e32 v122, 16, v155
	v_add_f32_e32 v120, v120, v122
	v_and_b32_e32 v122, 0xffff0000, v155
	v_add_f32_e32 v121, v121, v122
	v_lshlrev_b32_e32 v122, 16, v156
	v_add_f32_e32 v122, v114, v122
	v_and_b32_e32 v114, 0xffff0000, v156
	v_add_f32_e32 v123, v115, v114
	v_lshlrev_b32_e32 v114, 16, v157
	v_add_f32_e32 v124, v116, v114
	v_and_b32_e32 v114, 0xffff0000, v157
	v_add_f32_e32 v117, v117, v114
	v_mul_f32_e32 v114, v119, v119
	v_mul_f32_e32 v115, v121, v121
	v_fmac_f32_e32 v114, v118, v118
	v_fmac_f32_e32 v115, v120, v120
	v_add_f32_e32 v114, v114, v115
	v_mul_f32_e32 v115, v123, v123
	v_fmac_f32_e32 v115, v122, v122
	v_add_f32_e32 v114, v115, v114
	v_mul_f32_e32 v115, v117, v117
	v_fmac_f32_e32 v115, v124, v124
	v_add_f32_e32 v114, v115, v114
	v_add_f32_e32 v125, v181, v114
	v_cvt_pk_bf16_f32 v114, v118, v119
	v_cvt_pk_bf16_f32 v115, v120, v121
	v_cvt_pk_bf16_f32 v116, v122, v123
	v_cvt_pk_bf16_f32 v117, v124, v117
	global_store_dwordx4 v[198:199], v[114:117], off offset:256
	s_nop 1
	v_mov_b32_e32 v114, v125
	s_nop 1
	v_permlane16_swap_b32_e32 v125, v114
	v_add_f32_e32 v114, v125, v114
	v_mov_b32_e32 v115, v114
	s_nop 1
	v_permlane32_swap_b32_e32 v114, v115
	s_and_saveexec_b64 s[24:25], s[8:9]
	s_cbranch_execz .LBB0_1400
	v_add_f32_e32 v116, v114, v115
	s_lshl_b32 s6, s83, 2
	v_lshlrev_b64 v[114:115], 7, v[172:173]
	s_ashr_i32 s7, s6, 31
	v_lshl_add_u64 v[114:115], s[14:15], 0, v[114:115]
	v_lshl_add_u64 v[114:115], s[6:7], 2, v[114:115]
	s_lshl_b32 s94, s51, 2
	v_lshl_add_u64 v[114:115], v[114:115], 0, s[94:95]
	global_store_dword v[114:115], v116, off

; #define PG8_STAGE(bufoff, gbase, voff) do { _Pragma("unroll") for (int _i = 0; _i < 2; ++_i) \
;         __builtin_amdgcn_global_load_lds((const unsigned*)((const char*)(gbase) + (voff)[_i]), (PG8_LAS unsigned*)(lds + (bufoff) + ldsw + _i * 8192), 16, 0, 0); } while (0)
; #define PG8_WAIT_V(n) asm volatile("s_waitcnt vmcnt(" #n ")" ::: "memory")
; #define PG8_WAIT_L(n) asm volatile("s_waitcnt lgkmcnt(" #n ")" ::: "memory")
; #define PG8_BAR __builtin_amdgcn_s_barrier()
; #define PG8_SCHED __builtin_amdgcn_sched_barrier(0)
; template <class Epi, class Sched, bool ALIGN_EPI, bool F8 = false>
; __device__ __forceinline__ void gemm_phase(PG8_LAS unsigned char* lds, const Gemm g, const Sched& S, const Epi& E, int tid) {
;     ...
;             const bool last = (t == nt - 2);
;             const char* a1 = cA + (size_t)(t + 1) * kstep;
;             const char* a2 = last ? nA : cA + (size_t)(t + 2) * kstep; const char* b2 = last ? nB : cB + (size_t)(t + 2) * kstep;
;             const char* a3 = a2 + kstep; const char* b3 = b2 + kstep;
;             if (last && has_next) S.a_ready(nxt);
;             PG8_LDB(B0, 0, 0); PG8_LDB(B1, 0, 1); PG8_SCHED; PG8_LDA(At, 0, 0); PG8_STAGE(PG8_SA(1, 1), a1 + hstepA, voffA);
;             PG8_WAIT_V(8); PG8_WAIT_L(0); PG8_BAR; PG8_MMA(0, 0, At, B0); PG8_MMA(0, 1, At, B1); PG8_BAR; PG8_SCHED;
;             PG8_LDA(At, 0, 1); PG8_STAGE(PG8_SB(0, 0), b2, voffB); PG8_STAGE(PG8_SB(0, 1), b2 + hstepB, voffB); PG8_STAGE(PG8_SA(0, 0), a2, voffA);
.LBB0_1454:
	s_add_u32 s8, s14, 0xfff80080
	s_addc_u32 s9, s15, -1
	s_add_i32 s18, 0, 0x10000
	s_cmp_eq_u32 s7, 28
	s_cselect_b32 s45, s27, s9
	s_cselect_b32 s44, vcc_lo, s8
	s_cselect_b32 s39, s25, s6
	s_cselect_b32 s38, vcc_hi, s50
	s_add_i32 s19, 0, 0x14000
	v_add_u32_e32 v152, s18, v160
	v_add_u32_e32 v156, s19, v160
	ds_read_b128 v[140:143], v152
	ds_read_b128 v[144:147], v152 offset:1024
	ds_read_b128 v[148:151], v152 offset:2048
	ds_read_b128 v[152:155], v152 offset:3072
	ds_read_b128 v[174:177], v156
	ds_read_b128 v[178:181], v156 offset:1024
	ds_read_b128 v[182:185], v156 offset:2048
	ds_read_b128 v[186:189], v156 offset:3072
	v_lshl_add_u64 v[156:157], s[14:15], 0, v[136:137]
	s_add_i32 m0, s82, 0xc000
	ds_read_b128 v[190:193], v173
	ds_read_b128 v[194:197], v173 offset:1024
	ds_read_b128 v[198:201], v173 offset:2048
	ds_read_b128 v[202:205], v173 offset:3072
	ds_read_b128 v[206:209], v173 offset:4096
	ds_read_b128 v[210:213], v173 offset:5120
	ds_read_b128 v[214:217], v173 offset:6144
	ds_read_b128 v[218:221], v173 offset:7168
	global_load_lds_dwordx4 v[156:157], off
	v_lshl_add_u64 v[156:157], s[14:15], 0, v[138:139]
	s_add_i32 m0, s82, 0xe000
	s_nop 0
	global_load_lds_dwordx4 v[156:157], off
	s_waitcnt vmcnt(8)
	s_waitcnt lgkmcnt(0)
	s_barrier
	s_setprio 1
	s_waitcnt lgkmcnt(0)
	v_mfma_f32_16x16x32_bf16 v[126:129], v[140:143], v[190:193], v[126:129]
	v_mfma_f32_16x16x32_bf16 v[122:125], v[148:151], v[190:193], v[122:125]
	v_mfma_f32_16x16x32_bf16 v[106:109], v[148:151], v[198:201], v[106:109]
	v_mfma_f32_16x16x32_bf16 v[110:113], v[140:143], v[198:201], v[110:113]
	v_mfma_f32_16x16x32_bf16 v[94:97], v[140:143], v[206:209], v[94:97]
	v_mfma_f32_16x16x32_bf16 v[90:93], v[148:151], v[206:209], v[90:93]
	v_mfma_f32_16x16x32_bf16 v[74:77], v[148:151], v[214:217], v[74:77]
	v_mfma_f32_16x16x32_bf16 v[78:81], v[140:143], v[214:217], v[78:81]
	v_mfma_f32_16x16x32_bf16 v[126:129], v[144:147], v[194:197], v[126:129]
	v_mfma_f32_16x16x32_bf16 v[122:125], v[152:155], v[194:197], v[122:125]
	v_mfma_f32_16x16x32_bf16 v[106:109], v[152:155], v[202:205], v[106:109]
	v_mfma_f32_16x16x32_bf16 v[110:113], v[144:147], v[202:205], v[110:113]
	v_mfma_f32_16x16x32_bf16 v[94:97], v[144:147], v[210:213], v[94:97]
	v_mfma_f32_16x16x32_bf16 v[90:93], v[152:155], v[210:213], v[90:93]
	v_mfma_f32_16x16x32_bf16 v[74:77], v[152:155], v[218:221], v[74:77]
	v_mfma_f32_16x16x32_bf16 v[78:81], v[144:147], v[218:221], v[78:81]
	s_setprio 0
	s_setprio 1
	v_mfma_f32_16x16x32_bf16 v[118:121], v[174:177], v[190:193], v[118:121]
	v_mfma_f32_16x16x32_bf16 v[114:117], v[182:185], v[190:193], v[114:117]
	v_mfma_f32_16x16x32_bf16 v[98:101], v[182:185], v[198:201], v[98:101]
	v_mfma_f32_16x16x32_bf16 v[102:105], v[174:177], v[198:201], v[102:105]
	v_mfma_f32_16x16x32_bf16 v[86:89], v[174:177], v[206:209], v[86:89]
	v_mfma_f32_16x16x32_bf16 v[82:85], v[182:185], v[206:209], v[82:85]
	v_mfma_f32_16x16x32_bf16 v[66:69], v[182:185], v[214:217], v[66:69]
	v_mfma_f32_16x16x32_bf16 v[70:73], v[174:177], v[214:217], v[70:73]
	v_mfma_f32_16x16x32_bf16 v[118:121], v[178:181], v[194:197], v[118:121]
	v_mfma_f32_16x16x32_bf16 v[114:117], v[186:189], v[194:197], v[114:117]
	v_mfma_f32_16x16x32_bf16 v[98:101], v[186:189], v[202:205], v[98:101]
	v_mfma_f32_16x16x32_bf16 v[102:105], v[178:181], v[202:205], v[102:105]
	s_setprio 0
	v_mfma_f32_16x16x32_bf16 v[86:89], v[178:181], v[210:213], v[86:89]
	v_mfma_f32_16x16x32_bf16 v[82:85], v[186:189], v[210:213], v[82:85]
	v_mfma_f32_16x16x32_bf16 v[66:69], v[186:189], v[218:221], v[66:69]
	v_mfma_f32_16x16x32_bf16 v[70:73], v[178:181], v[218:221], v[70:73]
	s_barrier
	s_add_i32 s8, s18, s69
	v_lshl_add_u64 v[156:157], s[38:39], 0, v[0:1]
	s_mov_b32 m0, s8
	ds_read_b128 v[190:193], v173 offset:16384
	ds_read_b128 v[194:197], v173 offset:17408
	ds_read_b128 v[198:201], v173 offset:18432
	ds_read_b128 v[202:205], v173 offset:19456
	ds_read_b128 v[206:209], v173 offset:20480
	ds_read_b128 v[210:213], v173 offset:21504
	ds_read_b128 v[214:217], v173 offset:22528
	ds_read_b128 v[218:221], v173 offset:23552
	global_load_lds_dwordx4 v[156:157], off
	s_add_i32 m0, s8, 0x2000
	s_add_u32 s8, s38, 0x80000
	v_lshl_add_u64 v[226:227], s[38:39], 0, v[130:131]
	s_addc_u32 s9, s39, 0
	s_add_i32 s18, s19, s69
	global_load_lds_dwordx4 v[226:227], off
	v_lshl_add_u64 v[228:229], s[8:9], 0, v[0:1]
	s_mov_b32 m0, s18
	v_lshl_add_u64 v[236:237], s[44:45], 0, v[132:133]
	global_load_lds_dwordx4 v[228:229], off
	v_lshl_add_u64 v[228:229], s[8:9], 0, v[130:131]
	s_add_i32 m0, s18, 0x2000
	s_nop 0
	global_load_lds_dwordx4 v[228:229], off
	v_lshl_add_u64 v[228:229], s[44:45], 0, v[134:135]
	s_mov_b32 m0, s82
	s_nop 0
	global_load_lds_dwordx4 v[228:229], off
	s_mov_b32 m0, s83
	s_nop 0
	global_load_lds_dwordx4 v[236:237], off
	s_waitcnt vmcnt(8)
	s_waitcnt lgkmcnt(0)
	s_barrier
; #define PG8_STAGE(bufoff, gbase, voff) do { _Pragma("unroll") for (int _i = 0; _i < 2; ++_i) \
;         __builtin_amdgcn_global_load_lds((const unsigned*)((const char*)(gbase) + (voff)[_i]), (PG8_LAS unsigned*)(lds + (bufoff) + ldsw + _i * 8192), 16, 0, 0); } while (0)
; #define PG8_WAIT_V(n) asm volatile("s_waitcnt vmcnt(" #n ")" ::: "memory")
; #define PG8_WAIT_L(n) asm volatile("s_waitcnt lgkmcnt(" #n ")" ::: "memory")
; #define PG8_BAR __builtin_amdgcn_s_barrier()
; #define PG8_SCHED __builtin_amdgcn_sched_barrier(0)
; template <class Epi, class Sched, bool ALIGN_EPI, bool F8 = false>
; __device__ __forceinline__ void gemm_phase(PG8_LAS unsigned char* lds, const Gemm g, const Sched& S, const Epi& E, int tid) {
;     ...
;             PG8_WAIT_V(8); PG8_WAIT_L(0); PG8_BAR; PG8_MMA(1, 0, At, B0); PG8_MMA(1, 1, At, B1); PG8_BAR; PG8_SCHED;
;             PG8_LDB(B0, 1, 0); PG8_LDB(B1, 1, 1); PG8_SCHED; PG8_LDA(At, 1, 0); PG8_STAGE(PG8_SA(0, 1), a2 + hstepA, voffA);
;             PG8_WAIT_V(8); PG8_WAIT_L(0); PG8_BAR; PG8_MMA(0, 0, At, B0); PG8_MMA(0, 1, At, B1); PG8_BAR; PG8_SCHED;
	s_setprio 1
	s_waitcnt lgkmcnt(0)
	v_mfma_f32_16x16x32_bf16 v[62:65], v[140:143], v[190:193], v[62:65]
	v_mfma_f32_16x16x32_bf16 v[58:61], v[148:151], v[190:193], v[58:61]
	v_mfma_f32_16x16x32_bf16 v[42:45], v[148:151], v[198:201], v[42:45]
	v_mfma_f32_16x16x32_bf16 v[46:49], v[140:143], v[198:201], v[46:49]
	v_mfma_f32_16x16x32_bf16 v[30:33], v[140:143], v[206:209], v[30:33]
	v_mfma_f32_16x16x32_bf16 v[26:29], v[148:151], v[206:209], v[26:29]
	v_mfma_f32_16x16x32_bf16 v[10:13], v[148:151], v[214:217], v[10:13]
	v_mfma_f32_16x16x32_bf16 v[14:17], v[140:143], v[214:217], v[14:17]
	v_mfma_f32_16x16x32_bf16 v[62:65], v[144:147], v[194:197], v[62:65]
	v_mfma_f32_16x16x32_bf16 v[58:61], v[152:155], v[194:197], v[58:61]
	v_mfma_f32_16x16x32_bf16 v[42:45], v[152:155], v[202:205], v[42:45]
	v_mfma_f32_16x16x32_bf16 v[46:49], v[144:147], v[202:205], v[46:49]
	v_mfma_f32_16x16x32_bf16 v[30:33], v[144:147], v[210:213], v[30:33]
	v_mfma_f32_16x16x32_bf16 v[26:29], v[152:155], v[210:213], v[26:29]
	v_mfma_f32_16x16x32_bf16 v[10:13], v[152:155], v[218:221], v[10:13]
	v_mfma_f32_16x16x32_bf16 v[14:17], v[144:147], v[218:221], v[14:17]
	s_setprio 0
	s_setprio 1
	v_mfma_f32_16x16x32_bf16 v[54:57], v[174:177], v[190:193], v[54:57]
	v_mfma_f32_16x16x32_bf16 v[50:53], v[182:185], v[190:193], v[50:53]
	v_mfma_f32_16x16x32_bf16 v[34:37], v[182:185], v[198:201], v[34:37]
	v_mfma_f32_16x16x32_bf16 v[38:41], v[174:177], v[198:201], v[38:41]
	v_mfma_f32_16x16x32_bf16 v[22:25], v[174:177], v[206:209], v[22:25]
	v_mfma_f32_16x16x32_bf16 v[18:21], v[182:185], v[206:209], v[18:21]
	v_mfma_f32_16x16x32_bf16 v[2:5], v[182:185], v[214:217], v[2:5]
	v_mfma_f32_16x16x32_bf16 v[6:9], v[174:177], v[214:217], v[6:9]
	v_mfma_f32_16x16x32_bf16 v[54:57], v[178:181], v[194:197], v[54:57]
	v_mfma_f32_16x16x32_bf16 v[50:53], v[186:189], v[194:197], v[50:53]
	v_mfma_f32_16x16x32_bf16 v[34:37], v[186:189], v[202:205], v[34:37]
	v_mfma_f32_16x16x32_bf16 v[38:41], v[178:181], v[202:205], v[38:41]
	s_setprio 0
	v_mfma_f32_16x16x32_bf16 v[22:25], v[178:181], v[210:213], v[22:25]
	v_mfma_f32_16x16x32_bf16 v[18:21], v[186:189], v[210:213], v[18:21]
	v_mfma_f32_16x16x32_bf16 v[2:5], v[186:189], v[218:221], v[2:5]
	v_mfma_f32_16x16x32_bf16 v[6:9], v[178:181], v[218:221], v[6:9]
	s_barrier
	s_add_i32 s18, 0, 0x18000
	s_add_i32 s19, 0, 0x1c000
	v_add_u32_e32 v152, s18, v160
	v_add_u32_e32 v186, s19, v160
	ds_read_b128 v[140:143], v152
	ds_read_b128 v[144:147], v152 offset:1024
	ds_read_b128 v[148:151], v152 offset:2048
	ds_read_b128 v[152:155], v152 offset:3072
	ds_read_b128 v[174:177], v186
	ds_read_b128 v[178:181], v186 offset:1024
	ds_read_b128 v[182:185], v186 offset:2048
	ds_read_b128 v[186:189], v186 offset:3072
	s_add_u32 s8, s44, 0x80000
	s_addc_u32 s9, s45, 0
	s_mov_b32 m0, s84
	v_lshl_add_u64 v[238:239], s[8:9], 0, v[134:135]
	ds_read_b128 v[190:193], v173 offset:32768
	ds_read_b128 v[194:197], v173 offset:33792
	ds_read_b128 v[198:201], v173 offset:34816
	ds_read_b128 v[202:205], v173 offset:35840
	ds_read_b128 v[206:209], v173 offset:36864
	ds_read_b128 v[210:213], v173 offset:37888
	ds_read_b128 v[214:217], v173 offset:38912
	ds_read_b128 v[218:221], v173 offset:39936
	global_load_lds_dwordx4 v[238:239], off
	v_lshl_add_u64 v[238:239], s[8:9], 0, v[132:133]
	s_mov_b32 m0, s85
	s_nop 0
	global_load_lds_dwordx4 v[238:239], off
	s_waitcnt vmcnt(8)
	s_waitcnt lgkmcnt(0)
	s_barrier
	s_setprio 1
	s_waitcnt lgkmcnt(0)
	v_mfma_f32_16x16x32_bf16 v[126:129], v[140:143], v[190:193], v[126:129]
	v_mfma_f32_16x16x32_bf16 v[122:125], v[148:151], v[190:193], v[122:125]
	v_mfma_f32_16x16x32_bf16 v[106:109], v[148:151], v[198:201], v[106:109]
	v_mfma_f32_16x16x32_bf16 v[110:113], v[140:143], v[198:201], v[110:113]
	v_mfma_f32_16x16x32_bf16 v[94:97], v[140:143], v[206:209], v[94:97]
	v_mfma_f32_16x16x32_bf16 v[90:93], v[148:151], v[206:209], v[90:93]
	v_mfma_f32_16x16x32_bf16 v[74:77], v[148:151], v[214:217], v[74:77]
	v_mfma_f32_16x16x32_bf16 v[78:81], v[140:143], v[214:217], v[78:81]
	v_mfma_f32_16x16x32_bf16 v[126:129], v[144:147], v[194:197], v[126:129]
	v_mfma_f32_16x16x32_bf16 v[122:125], v[152:155], v[194:197], v[122:125]
	v_mfma_f32_16x16x32_bf16 v[106:109], v[152:155], v[202:205], v[106:109]
	v_mfma_f32_16x16x32_bf16 v[110:113], v[144:147], v[202:205], v[110:113]
	v_mfma_f32_16x16x32_bf16 v[94:97], v[144:147], v[210:213], v[94:97]
	v_mfma_f32_16x16x32_bf16 v[90:93], v[152:155], v[210:213], v[90:93]
	v_mfma_f32_16x16x32_bf16 v[74:77], v[152:155], v[218:221], v[74:77]
	v_mfma_f32_16x16x32_bf16 v[78:81], v[144:147], v[218:221], v[78:81]
	s_setprio 0
	s_setprio 1
	v_mfma_f32_16x16x32_bf16 v[118:121], v[174:177], v[190:193], v[118:121]
	v_mfma_f32_16x16x32_bf16 v[114:117], v[182:185], v[190:193], v[114:117]
	v_mfma_f32_16x16x32_bf16 v[98:101], v[182:185], v[198:201], v[98:101]
	v_mfma_f32_16x16x32_bf16 v[102:105], v[174:177], v[198:201], v[102:105]
	v_mfma_f32_16x16x32_bf16 v[86:89], v[174:177], v[206:209], v[86:89]
	v_mfma_f32_16x16x32_bf16 v[82:85], v[182:185], v[206:209], v[82:85]
	v_mfma_f32_16x16x32_bf16 v[66:69], v[182:185], v[214:217], v[66:69]
	v_mfma_f32_16x16x32_bf16 v[70:73], v[174:177], v[214:217], v[70:73]
	v_mfma_f32_16x16x32_bf16 v[118:121], v[178:181], v[194:197], v[118:121]
	v_mfma_f32_16x16x32_bf16 v[114:117], v[186:189], v[194:197], v[114:117]
	v_mfma_f32_16x16x32_bf16 v[98:101], v[186:189], v[202:205], v[98:101]
	v_mfma_f32_16x16x32_bf16 v[102:105], v[178:181], v[202:205], v[102:105]
	s_setprio 0
	v_mfma_f32_16x16x32_bf16 v[86:89], v[178:181], v[210:213], v[86:89]
	v_mfma_f32_16x16x32_bf16 v[82:85], v[186:189], v[210:213], v[82:85]
	v_mfma_f32_16x16x32_bf16 v[66:69], v[186:189], v[218:221], v[66:69]
	v_mfma_f32_16x16x32_bf16 v[70:73], v[178:181], v[218:221], v[70:73]
	s_barrier
; #define PG8_STAGE(bufoff, gbase, voff) do { _Pragma("unroll") for (int _i = 0; _i < 2; ++_i) \
;         __builtin_amdgcn_global_load_lds((const unsigned*)((const char*)(gbase) + (voff)[_i]), (PG8_LAS unsigned*)(lds + (bufoff) + ldsw + _i * 8192), 16, 0, 0); } while (0)
; #define PG8_WAIT_V(n) asm volatile("s_waitcnt vmcnt(" #n ")" ::: "memory")
; #define PG8_WAIT_L(n) asm volatile("s_waitcnt lgkmcnt(" #n ")" ::: "memory")
; #define PG8_BAR __builtin_amdgcn_s_barrier()
; #define PG8_SCHED __builtin_amdgcn_sched_barrier(0)
; template <class Epi, class Sched, bool ALIGN_EPI, bool F8 = false>
; __device__ __forceinline__ void gemm_phase(PG8_LAS unsigned char* lds, const Gemm g, const Sched& S, const Epi& E, int tid) {
;     ...
;             PG8_LDA(At, 1, 1); PG8_STAGE(PG8_SB(1, 0), b3, voffB); PG8_STAGE(PG8_SB(1, 1), b3 + hstepB, voffB); PG8_STAGE(PG8_SA(1, 0), a3, voffA);
;             PG8_WAIT_V(8); PG8_WAIT_L(0); PG8_BAR; PG8_MMA(1, 0, At, B0); PG8_MMA(1, 1, At, B1); PG8_BAR; PG8_SCHED;
;         }
;         if constexpr (ALIGN_EPI) { if (wr == 0) PG8_BAR; }
	s_add_i32 s8, s18, s69
	v_lshl_add_u64 v[156:157], v[156:157], 0, s[60:61]
	s_mov_b32 m0, s8
	ds_read_b128 v[190:193], v173 offset:49152
	ds_read_b128 v[194:197], v173 offset:50176
	ds_read_b128 v[198:201], v173 offset:51200
	ds_read_b128 v[202:205], v173 offset:52224
	ds_read_b128 v[206:209], v173 offset:53248
	ds_read_b128 v[210:213], v173 offset:54272
	ds_read_b128 v[214:217], v173 offset:55296
	ds_read_b128 v[218:221], v173 offset:56320
	global_load_lds_dwordx4 v[156:157], off
	s_add_i32 m0, s8, 0x2000
	s_add_u32 s8, s38, 0x80080
	v_lshl_add_u64 v[156:157], v[226:227], 0, s[60:61]
	s_addc_u32 s9, s39, 0
	s_add_i32 s18, s19, s69
	global_load_lds_dwordx4 v[156:157], off
	v_lshl_add_u64 v[156:157], s[8:9], 0, v[0:1]
	s_mov_b32 m0, s18
	s_nop 0
	global_load_lds_dwordx4 v[156:157], off
	v_lshl_add_u64 v[156:157], s[8:9], 0, v[130:131]
	s_add_i32 m0, s18, 0x2000
	s_nop 0
	global_load_lds_dwordx4 v[156:157], off
	v_lshl_add_u64 v[156:157], v[228:229], 0, s[60:61]
	s_mov_b32 m0, s86
	s_nop 0
	global_load_lds_dwordx4 v[156:157], off
	v_lshl_add_u64 v[156:157], v[236:237], 0, s[60:61]
	s_mov_b32 m0, s87
	s_nop 0
	global_load_lds_dwordx4 v[156:157], off
	s_waitcnt vmcnt(8)
	s_waitcnt lgkmcnt(0)
	s_barrier
	s_setprio 1
	s_waitcnt lgkmcnt(0)
	v_mfma_f32_16x16x32_bf16 v[62:65], v[140:143], v[190:193], v[62:65]
	v_mfma_f32_16x16x32_bf16 v[58:61], v[148:151], v[190:193], v[58:61]
	v_mfma_f32_16x16x32_bf16 v[42:45], v[148:151], v[198:201], v[42:45]
	v_mfma_f32_16x16x32_bf16 v[46:49], v[140:143], v[198:201], v[46:49]
	v_mfma_f32_16x16x32_bf16 v[30:33], v[140:143], v[206:209], v[30:33]
	v_mfma_f32_16x16x32_bf16 v[26:29], v[148:151], v[206:209], v[26:29]
	v_mfma_f32_16x16x32_bf16 v[10:13], v[148:151], v[214:217], v[10:13]
	v_mfma_f32_16x16x32_bf16 v[14:17], v[140:143], v[214:217], v[14:17]
	v_mfma_f32_16x16x32_bf16 v[62:65], v[144:147], v[194:197], v[62:65]
	v_mfma_f32_16x16x32_bf16 v[58:61], v[152:155], v[194:197], v[58:61]
	v_mfma_f32_16x16x32_bf16 v[42:45], v[152:155], v[202:205], v[42:45]
	v_mfma_f32_16x16x32_bf16 v[46:49], v[144:147], v[202:205], v[46:49]
	v_mfma_f32_16x16x32_bf16 v[30:33], v[144:147], v[210:213], v[30:33]
	v_mfma_f32_16x16x32_bf16 v[26:29], v[152:155], v[210:213], v[26:29]
	v_mfma_f32_16x16x32_bf16 v[10:13], v[152:155], v[218:221], v[10:13]
	v_mfma_f32_16x16x32_bf16 v[14:17], v[144:147], v[218:221], v[14:17]
	s_setprio 0
	s_setprio 1
	v_mfma_f32_16x16x32_bf16 v[54:57], v[174:177], v[190:193], v[54:57]
	v_mfma_f32_16x16x32_bf16 v[50:53], v[182:185], v[190:193], v[50:53]
	v_mfma_f32_16x16x32_bf16 v[34:37], v[182:185], v[198:201], v[34:37]
	v_mfma_f32_16x16x32_bf16 v[38:41], v[174:177], v[198:201], v[38:41]
	v_mfma_f32_16x16x32_bf16 v[22:25], v[174:177], v[206:209], v[22:25]
	v_mfma_f32_16x16x32_bf16 v[18:21], v[182:185], v[206:209], v[18:21]
	v_mfma_f32_16x16x32_bf16 v[2:5], v[182:185], v[214:217], v[2:5]
	v_mfma_f32_16x16x32_bf16 v[6:9], v[174:177], v[214:217], v[6:9]
	v_mfma_f32_16x16x32_bf16 v[54:57], v[178:181], v[194:197], v[54:57]
	v_mfma_f32_16x16x32_bf16 v[50:53], v[186:189], v[194:197], v[50:53]
	v_mfma_f32_16x16x32_bf16 v[34:37], v[186:189], v[202:205], v[34:37]
	v_mfma_f32_16x16x32_bf16 v[38:41], v[178:181], v[202:205], v[38:41]
	s_setprio 0
	v_mfma_f32_16x16x32_bf16 v[22:25], v[178:181], v[210:213], v[22:25]
	v_mfma_f32_16x16x32_bf16 v[18:21], v[186:189], v[210:213], v[18:21]
	v_mfma_f32_16x16x32_bf16 v[2:5], v[186:189], v[218:221], v[2:5]
	v_mfma_f32_16x16x32_bf16 v[6:9], v[178:181], v[218:221], v[6:9]
	s_barrier
	s_add_i32 s7, s7, 2
	s_add_u32 s14, s14, 0x100
	s_addc_u32 s15, s15, 0
	s_add_u32 s50, s50, 0x100
	s_addc_u32 s6, s6, 0
	s_cmp_gt_u32 s7, 29
	s_cbranch_scc0 .LBB0_1454
	s_and_b64 vcc, exec, s[22:23]
	s_cbranch_vccz .LBB0_1457
	s_barrier

; #define PG8_STAGE(bufoff, gbase, voff) do { _Pragma("unroll") for (int _i = 0; _i < 2; ++_i) \
;         __builtin_amdgcn_global_load_lds((const unsigned*)((const char*)(gbase) + (voff)[_i]), (PG8_LAS unsigned*)(lds + (bufoff) + ldsw + _i * 8192), 16, 0, 0); } while (0)
; #define PG8_WAIT_V(n) asm volatile("s_waitcnt vmcnt(" #n ")" ::: "memory")
; #define PG8_WAIT_L(n) asm volatile("s_waitcnt lgkmcnt(" #n ")" ::: "memory")
; #define PG8_BAR __builtin_amdgcn_s_barrier()
; #define PG8_SCHED __builtin_amdgcn_sched_barrier(0)
; template <class Epi, class Sched, bool ALIGN_EPI, bool F8 = false>
; __device__ __forceinline__ void gemm_phase(PG8_LAS unsigned char* lds, const Gemm g, const Sched& S, const Epi& E, int tid) {
;     ...
;             const bool last = (t == nt - 2);
;             const char* a1 = cA + (size_t)(t + 1) * kstep;
;             const char* a2 = last ? nA : cA + (size_t)(t + 2) * kstep; const char* b2 = last ? nB : cB + (size_t)(t + 2) * kstep;
;             const char* a3 = a2 + kstep; const char* b3 = b2 + kstep;
;             if (last && has_next) S.a_ready(nxt);
;             PG8_LDB(B0, 0, 0); PG8_LDB(B1, 0, 1); PG8_SCHED; PG8_LDA(At, 0, 0); PG8_STAGE(PG8_SA(1, 1), a1 + hstepA, voffA);
;             PG8_WAIT_V(8); PG8_WAIT_L(0); PG8_BAR; PG8_MMA(0, 0, At, B0); PG8_MMA(0, 1, At, B1); PG8_BAR; PG8_SCHED;
;             PG8_LDA(At, 0, 1); PG8_STAGE(PG8_SB(0, 0), b2, voffB); PG8_STAGE(PG8_SB(0, 1), b2 + hstepB, voffB); PG8_STAGE(PG8_SA(0, 0), a2, voffA);
.LBB0_1508:
	s_add_u32 s7, s28, 0xfff80080
	s_addc_u32 s30, s29, -1
	s_add_i32 s94, 0, 0x10000
	s_cmp_eq_u32 s6, 28
	s_cselect_b32 s35, s21, s30
	s_cselect_b32 s34, s87, s7
	s_cselect_b32 s31, s19, s50
	s_cselect_b32 s30, s88, s89
	s_add_i32 s7, 0, 0x14000
	v_add_u32_e32 v152, s94, v215
	v_add_u32_e32 v168, s7, v215
	ds_read_b128 v[140:143], v152
	ds_read_b128 v[144:147], v152 offset:1024
	ds_read_b128 v[148:151], v152 offset:2048
	ds_read_b128 v[152:155], v152 offset:3072
	ds_read_b128 v[156:159], v168
	ds_read_b128 v[160:163], v168 offset:1024
	ds_read_b128 v[164:167], v168 offset:2048
	ds_read_b128 v[168:171], v168 offset:3072
	v_lshl_add_u64 v[204:205], s[28:29], 0, v[136:137]
	s_add_i32 m0, s39, 0xc000
	ds_read_b128 v[172:175], v244
	ds_read_b128 v[176:179], v244 offset:1024
	ds_read_b128 v[180:183], v244 offset:2048
	ds_read_b128 v[184:187], v244 offset:3072
	ds_read_b128 v[188:191], v244 offset:4096
	ds_read_b128 v[192:195], v244 offset:5120
	ds_read_b128 v[196:199], v244 offset:6144
	ds_read_b128 v[200:203], v244 offset:7168
	global_load_lds_dwordx4 v[204:205], off
	v_lshl_add_u64 v[204:205], s[28:29], 0, v[138:139]
	s_add_i32 m0, s39, 0xe000
	s_nop 0
	global_load_lds_dwordx4 v[204:205], off
	s_waitcnt vmcnt(8)
	s_waitcnt lgkmcnt(0)
	s_barrier
	s_setprio 1
	s_waitcnt lgkmcnt(0)
	v_mfma_f32_16x16x32_bf16 v[126:129], v[140:143], v[172:175], v[126:129]
	v_mfma_f32_16x16x32_bf16 v[122:125], v[148:151], v[172:175], v[122:125]
	v_mfma_f32_16x16x32_bf16 v[106:109], v[148:151], v[180:183], v[106:109]
	v_mfma_f32_16x16x32_bf16 v[110:113], v[140:143], v[180:183], v[110:113]
	v_mfma_f32_16x16x32_bf16 v[94:97], v[140:143], v[188:191], v[94:97]
	v_mfma_f32_16x16x32_bf16 v[90:93], v[148:151], v[188:191], v[90:93]
	v_mfma_f32_16x16x32_bf16 v[74:77], v[148:151], v[196:199], v[74:77]
	v_mfma_f32_16x16x32_bf16 v[78:81], v[140:143], v[196:199], v[78:81]
	v_mfma_f32_16x16x32_bf16 v[126:129], v[144:147], v[176:179], v[126:129]
	v_mfma_f32_16x16x32_bf16 v[122:125], v[152:155], v[176:179], v[122:125]
	v_mfma_f32_16x16x32_bf16 v[106:109], v[152:155], v[184:187], v[106:109]
	v_mfma_f32_16x16x32_bf16 v[110:113], v[144:147], v[184:187], v[110:113]
	v_mfma_f32_16x16x32_bf16 v[94:97], v[144:147], v[192:195], v[94:97]
	v_mfma_f32_16x16x32_bf16 v[90:93], v[152:155], v[192:195], v[90:93]
	v_mfma_f32_16x16x32_bf16 v[74:77], v[152:155], v[200:203], v[74:77]
	v_mfma_f32_16x16x32_bf16 v[78:81], v[144:147], v[200:203], v[78:81]
	s_setprio 0
	s_setprio 1
	v_mfma_f32_16x16x32_bf16 v[118:121], v[156:159], v[172:175], v[118:121]
	v_mfma_f32_16x16x32_bf16 v[114:117], v[164:167], v[172:175], v[114:117]
	v_mfma_f32_16x16x32_bf16 v[98:101], v[164:167], v[180:183], v[98:101]
	v_mfma_f32_16x16x32_bf16 v[102:105], v[156:159], v[180:183], v[102:105]
	v_mfma_f32_16x16x32_bf16 v[86:89], v[156:159], v[188:191], v[86:89]
	v_mfma_f32_16x16x32_bf16 v[82:85], v[164:167], v[188:191], v[82:85]
	v_mfma_f32_16x16x32_bf16 v[66:69], v[164:167], v[196:199], v[66:69]
	v_mfma_f32_16x16x32_bf16 v[70:73], v[156:159], v[196:199], v[70:73]
	v_mfma_f32_16x16x32_bf16 v[118:121], v[160:163], v[176:179], v[118:121]
	v_mfma_f32_16x16x32_bf16 v[114:117], v[168:171], v[176:179], v[114:117]
	v_mfma_f32_16x16x32_bf16 v[98:101], v[168:171], v[184:187], v[98:101]
	v_mfma_f32_16x16x32_bf16 v[102:105], v[160:163], v[184:187], v[102:105]
	s_setprio 0
	v_mfma_f32_16x16x32_bf16 v[86:89], v[160:163], v[192:195], v[86:89]
	v_mfma_f32_16x16x32_bf16 v[82:85], v[168:171], v[192:195], v[82:85]
	v_mfma_f32_16x16x32_bf16 v[66:69], v[168:171], v[200:203], v[66:69]
	v_mfma_f32_16x16x32_bf16 v[70:73], v[160:163], v[200:203], v[70:73]
	s_barrier
	s_add_i32 s94, s94, s38
	v_lshl_add_u64 v[204:205], s[30:31], 0, v[0:1]
	s_mov_b32 m0, s94
	ds_read_b128 v[172:175], v244 offset:16384
	ds_read_b128 v[176:179], v244 offset:17408
	ds_read_b128 v[180:183], v244 offset:18432
	ds_read_b128 v[184:187], v244 offset:19456
	ds_read_b128 v[188:191], v244 offset:20480
	ds_read_b128 v[192:195], v244 offset:21504
	ds_read_b128 v[196:199], v244 offset:22528
	ds_read_b128 v[200:203], v244 offset:23552
	global_load_lds_dwordx4 v[204:205], off
	s_add_i32 m0, s94, 0x2000
	s_add_u32 vcc_lo, s30, 0x80000
	v_lshl_add_u64 v[206:207], s[30:31], 0, v[130:131]
	s_addc_u32 vcc_hi, s31, 0
	s_add_i32 s7, s7, s38
	global_load_lds_dwordx4 v[206:207], off
	v_lshl_add_u64 v[208:209], vcc, 0, v[0:1]
	s_mov_b32 m0, s7
	v_lshl_add_u64 v[210:211], s[34:35], 0, v[132:133]
	global_load_lds_dwordx4 v[208:209], off
	v_lshl_add_u64 v[208:209], vcc, 0, v[130:131]
	s_add_i32 m0, s7, 0x2000
	s_nop 0
	global_load_lds_dwordx4 v[208:209], off
	v_lshl_add_u64 v[208:209], s[34:35], 0, v[134:135]
	s_mov_b32 m0, s39
	s_nop 0
	global_load_lds_dwordx4 v[208:209], off
	s_mov_b32 m0, s44
	s_nop 0
	global_load_lds_dwordx4 v[210:211], off
	s_waitcnt vmcnt(8)
	s_waitcnt lgkmcnt(0)
	s_barrier
; #define PG8_STAGE(bufoff, gbase, voff) do { _Pragma("unroll") for (int _i = 0; _i < 2; ++_i) \
;         __builtin_amdgcn_global_load_lds((const unsigned*)((const char*)(gbase) + (voff)[_i]), (PG8_LAS unsigned*)(lds + (bufoff) + ldsw + _i * 8192), 16, 0, 0); } while (0)
; #define PG8_WAIT_V(n) asm volatile("s_waitcnt vmcnt(" #n ")" ::: "memory")
; #define PG8_WAIT_L(n) asm volatile("s_waitcnt lgkmcnt(" #n ")" ::: "memory")
; #define PG8_BAR __builtin_amdgcn_s_barrier()
; #define PG8_SCHED __builtin_amdgcn_sched_barrier(0)
; template <class Epi, class Sched, bool ALIGN_EPI, bool F8 = false>
; __device__ __forceinline__ void gemm_phase(PG8_LAS unsigned char* lds, const Gemm g, const Sched& S, const Epi& E, int tid) {
;     ...
;         for (int t = 0; t < nt; t += 2) {
;             const bool last = (t == nt - 2);
;             const char* a1 = cA + (size_t)(t + 1) * kstep;
;             const char* a2 = last ? nA : cA + (size_t)(t + 2) * kstep; const char* b2 = last ? nB : cB + (size_t)(t + 2) * kstep;
;             const char* a3 = a2 + kstep; const char* b3 = b2 + kstep;
;             if (last && has_next) S.a_ready(nxt);
;             PG8_LDB(B0, 0, 0); PG8_LDB(B1, 0, 1); PG8_SCHED; PG8_LDA(At, 0, 0); PG8_STAGE(PG8_SA(1, 1), a1 + hstepA, voffA);
;             PG8_WAIT_V(8); PG8_WAIT_L(0); PG8_BAR; PG8_MMA(0, 0, At, B0); PG8_MMA(0, 1, At, B1); PG8_BAR; PG8_SCHED;
;             PG8_LDA(At, 0, 1); PG8_STAGE(PG8_SB(0, 0), b2, voffB); PG8_STAGE(PG8_SB(0, 1), b2 + hstepB, voffB); PG8_STAGE(PG8_SA(0, 0), a2, voffA);
;             PG8_WAIT_V(8); PG8_WAIT_L(0); PG8_BAR; PG8_MMA(1, 0, At, B0); PG8_MMA(1, 1, At, B1); PG8_BAR; PG8_SCHED;
;             PG8_LDB(B0, 1, 0); PG8_LDB(B1, 1, 1); PG8_SCHED; PG8_LDA(At, 1, 0); PG8_STAGE(PG8_SA(0, 1), a2 + hstepA, voffA);
;             PG8_WAIT_V(8); PG8_WAIT_L(0); PG8_BAR; PG8_MMA(0, 0, At, B0); PG8_MMA(0, 1, At, B1); PG8_BAR; PG8_SCHED;
;             PG8_LDA(At, 1, 1); PG8_STAGE(PG8_SB(1, 0), b3, voffB); PG8_STAGE(PG8_SB(1, 1), b3 + hstepB, voffB); PG8_STAGE(PG8_SA(1, 0), a3, voffA);
;             PG8_WAIT_V(8); PG8_WAIT_L(0); PG8_BAR; PG8_MMA(1, 0, At, B0); PG8_MMA(1, 1, At, B1); PG8_BAR; PG8_SCHED;
;         }
	s_setprio 1
	s_waitcnt lgkmcnt(0)
	v_mfma_f32_16x16x32_bf16 v[62:65], v[140:143], v[172:175], v[62:65]
	v_mfma_f32_16x16x32_bf16 v[58:61], v[148:151], v[172:175], v[58:61]
	v_mfma_f32_16x16x32_bf16 v[42:45], v[148:151], v[180:183], v[42:45]
	v_mfma_f32_16x16x32_bf16 v[46:49], v[140:143], v[180:183], v[46:49]
	v_mfma_f32_16x16x32_bf16 v[30:33], v[140:143], v[188:191], v[30:33]
	v_mfma_f32_16x16x32_bf16 v[26:29], v[148:151], v[188:191], v[26:29]
	v_mfma_f32_16x16x32_bf16 v[10:13], v[148:151], v[196:199], v[10:13]
	v_mfma_f32_16x16x32_bf16 v[14:17], v[140:143], v[196:199], v[14:17]
	v_mfma_f32_16x16x32_bf16 v[62:65], v[144:147], v[176:179], v[62:65]
	v_mfma_f32_16x16x32_bf16 v[58:61], v[152:155], v[176:179], v[58:61]
	v_mfma_f32_16x16x32_bf16 v[42:45], v[152:155], v[184:187], v[42:45]
	v_mfma_f32_16x16x32_bf16 v[46:49], v[144:147], v[184:187], v[46:49]
	v_mfma_f32_16x16x32_bf16 v[30:33], v[144:147], v[192:195], v[30:33]
	v_mfma_f32_16x16x32_bf16 v[26:29], v[152:155], v[192:195], v[26:29]
	v_mfma_f32_16x16x32_bf16 v[10:13], v[152:155], v[200:203], v[10:13]
	v_mfma_f32_16x16x32_bf16 v[14:17], v[144:147], v[200:203], v[14:17]
	s_setprio 0
	s_setprio 1
	v_mfma_f32_16x16x32_bf16 v[54:57], v[156:159], v[172:175], v[54:57]
	v_mfma_f32_16x16x32_bf16 v[50:53], v[164:167], v[172:175], v[50:53]
	v_mfma_f32_16x16x32_bf16 v[34:37], v[164:167], v[180:183], v[34:37]
	v_mfma_f32_16x16x32_bf16 v[38:41], v[156:159], v[180:183], v[38:41]
	v_mfma_f32_16x16x32_bf16 v[22:25], v[156:159], v[188:191], v[22:25]
	v_mfma_f32_16x16x32_bf16 v[18:21], v[164:167], v[188:191], v[18:21]
	v_mfma_f32_16x16x32_bf16 v[2:5], v[164:167], v[196:199], v[2:5]
	v_mfma_f32_16x16x32_bf16 v[6:9], v[156:159], v[196:199], v[6:9]
	v_mfma_f32_16x16x32_bf16 v[54:57], v[160:163], v[176:179], v[54:57]
	v_mfma_f32_16x16x32_bf16 v[50:53], v[168:171], v[176:179], v[50:53]
	v_mfma_f32_16x16x32_bf16 v[34:37], v[168:171], v[184:187], v[34:37]
	v_mfma_f32_16x16x32_bf16 v[38:41], v[160:163], v[184:187], v[38:41]
	s_setprio 0
	v_mfma_f32_16x16x32_bf16 v[22:25], v[160:163], v[192:195], v[22:25]
	v_mfma_f32_16x16x32_bf16 v[18:21], v[168:171], v[192:195], v[18:21]
	v_mfma_f32_16x16x32_bf16 v[2:5], v[168:171], v[200:203], v[2:5]
	v_mfma_f32_16x16x32_bf16 v[6:9], v[160:163], v[200:203], v[6:9]
	s_barrier
	s_add_i32 s7, 0, 0x18000
	s_add_i32 s94, 0, 0x1c000
	v_add_u32_e32 v152, s7, v215
	v_add_u32_e32 v168, s94, v215
	ds_read_b128 v[140:143], v152
	ds_read_b128 v[144:147], v152 offset:1024
	ds_read_b128 v[148:151], v152 offset:2048
	ds_read_b128 v[152:155], v152 offset:3072
	ds_read_b128 v[156:159], v168
	ds_read_b128 v[160:163], v168 offset:1024
	ds_read_b128 v[164:167], v168 offset:2048
	ds_read_b128 v[168:171], v168 offset:3072
	s_add_u32 s34, s34, 0x80000
	s_addc_u32 s35, s35, 0
	s_mov_b32 m0, s45
	v_lshl_add_u64 v[212:213], s[34:35], 0, v[134:135]
	ds_read_b128 v[172:175], v244 offset:32768
	ds_read_b128 v[176:179], v244 offset:33792
	ds_read_b128 v[180:183], v244 offset:34816
	ds_read_b128 v[184:187], v244 offset:35840
	ds_read_b128 v[188:191], v244 offset:36864
	ds_read_b128 v[192:195], v244 offset:37888
	ds_read_b128 v[196:199], v244 offset:38912
	ds_read_b128 v[200:203], v244 offset:39936
	global_load_lds_dwordx4 v[212:213], off
	v_lshl_add_u64 v[212:213], s[34:35], 0, v[132:133]
	s_mov_b32 m0, s69
	s_nop 0
	global_load_lds_dwordx4 v[212:213], off
	s_waitcnt vmcnt(8)
	s_waitcnt lgkmcnt(0)
	s_barrier
	s_setprio 1
	s_waitcnt lgkmcnt(0)
	v_mfma_f32_16x16x32_bf16 v[126:129], v[140:143], v[172:175], v[126:129]
	v_mfma_f32_16x16x32_bf16 v[122:125], v[148:151], v[172:175], v[122:125]
	v_mfma_f32_16x16x32_bf16 v[106:109], v[148:151], v[180:183], v[106:109]
	v_mfma_f32_16x16x32_bf16 v[110:113], v[140:143], v[180:183], v[110:113]
	v_mfma_f32_16x16x32_bf16 v[94:97], v[140:143], v[188:191], v[94:97]
	v_mfma_f32_16x16x32_bf16 v[90:93], v[148:151], v[188:191], v[90:93]
	v_mfma_f32_16x16x32_bf16 v[74:77], v[148:151], v[196:199], v[74:77]
	v_mfma_f32_16x16x32_bf16 v[78:81], v[140:143], v[196:199], v[78:81]
	v_mfma_f32_16x16x32_bf16 v[126:129], v[144:147], v[176:179], v[126:129]
	v_mfma_f32_16x16x32_bf16 v[122:125], v[152:155], v[176:179], v[122:125]
	v_mfma_f32_16x16x32_bf16 v[106:109], v[152:155], v[184:187], v[106:109]
	v_mfma_f32_16x16x32_bf16 v[110:113], v[144:147], v[184:187], v[110:113]
	v_mfma_f32_16x16x32_bf16 v[94:97], v[144:147], v[192:195], v[94:97]
	v_mfma_f32_16x16x32_bf16 v[90:93], v[152:155], v[192:195], v[90:93]
	v_mfma_f32_16x16x32_bf16 v[74:77], v[152:155], v[200:203], v[74:77]
	v_mfma_f32_16x16x32_bf16 v[78:81], v[144:147], v[200:203], v[78:81]
	s_setprio 0
	s_setprio 1
	v_mfma_f32_16x16x32_bf16 v[118:121], v[156:159], v[172:175], v[118:121]
	v_mfma_f32_16x16x32_bf16 v[114:117], v[164:167], v[172:175], v[114:117]
	v_mfma_f32_16x16x32_bf16 v[98:101], v[164:167], v[180:183], v[98:101]
	v_mfma_f32_16x16x32_bf16 v[102:105], v[156:159], v[180:183], v[102:105]
	v_mfma_f32_16x16x32_bf16 v[86:89], v[156:159], v[188:191], v[86:89]
	v_mfma_f32_16x16x32_bf16 v[82:85], v[164:167], v[188:191], v[82:85]
	v_mfma_f32_16x16x32_bf16 v[66:69], v[164:167], v[196:199], v[66:69]
	v_mfma_f32_16x16x32_bf16 v[70:73], v[156:159], v[196:199], v[70:73]
	v_mfma_f32_16x16x32_bf16 v[118:121], v[160:163], v[176:179], v[118:121]
	v_mfma_f32_16x16x32_bf16 v[114:117], v[168:171], v[176:179], v[114:117]
	v_mfma_f32_16x16x32_bf16 v[98:101], v[168:171], v[184:187], v[98:101]
	v_mfma_f32_16x16x32_bf16 v[102:105], v[160:163], v[184:187], v[102:105]
	s_setprio 0
	v_mfma_f32_16x16x32_bf16 v[86:89], v[160:163], v[192:195], v[86:89]
	v_mfma_f32_16x16x32_bf16 v[82:85], v[168:171], v[192:195], v[82:85]
	v_mfma_f32_16x16x32_bf16 v[66:69], v[168:171], v[200:203], v[66:69]
	v_mfma_f32_16x16x32_bf16 v[70:73], v[160:163], v[200:203], v[70:73]
	s_barrier
; #define PG8_STAGE(bufoff, gbase, voff) do { _Pragma("unroll") for (int _i = 0; _i < 2; ++_i) \
;         __builtin_amdgcn_global_load_lds((const unsigned*)((const char*)(gbase) + (voff)[_i]), (PG8_LAS unsigned*)(lds + (bufoff) + ldsw + _i * 8192), 16, 0, 0); } while (0)
; #define PG8_WAIT_V(n) asm volatile("s_waitcnt vmcnt(" #n ")" ::: "memory")
; #define PG8_WAIT_L(n) asm volatile("s_waitcnt lgkmcnt(" #n ")" ::: "memory")
; #define PG8_BAR __builtin_amdgcn_s_barrier()
; #define PG8_SCHED __builtin_amdgcn_sched_barrier(0)
; template <class Epi, class Sched, bool ALIGN_EPI, bool F8 = false>
; __device__ __forceinline__ void gemm_phase(PG8_LAS unsigned char* lds, const Gemm g, const Sched& S, const Epi& E, int tid) {
;     ...
;         for (int t = 0; t < nt; t += 2) {
;             const bool last = (t == nt - 2);
;             const char* a1 = cA + (size_t)(t + 1) * kstep;
;             const char* a2 = last ? nA : cA + (size_t)(t + 2) * kstep; const char* b2 = last ? nB : cB + (size_t)(t + 2) * kstep;
;             const char* a3 = a2 + kstep; const char* b3 = b2 + kstep;
;             if (last && has_next) S.a_ready(nxt);
;             PG8_LDB(B0, 0, 0); PG8_LDB(B1, 0, 1); PG8_SCHED; PG8_LDA(At, 0, 0); PG8_STAGE(PG8_SA(1, 1), a1 + hstepA, voffA);
;             PG8_WAIT_V(8); PG8_WAIT_L(0); PG8_BAR; PG8_MMA(0, 0, At, B0); PG8_MMA(0, 1, At, B1); PG8_BAR; PG8_SCHED;
;             PG8_LDA(At, 0, 1); PG8_STAGE(PG8_SB(0, 0), b2, voffB); PG8_STAGE(PG8_SB(0, 1), b2 + hstepB, voffB); PG8_STAGE(PG8_SA(0, 0), a2, voffA);
;             PG8_WAIT_V(8); PG8_WAIT_L(0); PG8_BAR; PG8_MMA(1, 0, At, B0); PG8_MMA(1, 1, At, B1); PG8_BAR; PG8_SCHED;
;             PG8_LDB(B0, 1, 0); PG8_LDB(B1, 1, 1); PG8_SCHED; PG8_LDA(At, 1, 0); PG8_STAGE(PG8_SA(0, 1), a2 + hstepA, voffA);
;             PG8_WAIT_V(8); PG8_WAIT_L(0); PG8_BAR; PG8_MMA(0, 0, At, B0); PG8_MMA(0, 1, At, B1); PG8_BAR; PG8_SCHED;
;             PG8_LDA(At, 1, 1); PG8_STAGE(PG8_SB(1, 0), b3, voffB); PG8_STAGE(PG8_SB(1, 1), b3 + hstepB, voffB); PG8_STAGE(PG8_SA(1, 0), a3, voffA);
;             PG8_WAIT_V(8); PG8_WAIT_L(0); PG8_BAR; PG8_MMA(1, 0, At, B0); PG8_MMA(1, 1, At, B1); PG8_BAR; PG8_SCHED;
;         }
;         if constexpr (ALIGN_EPI) { if (wr == 0) PG8_BAR; }
	s_add_i32 s7, s7, s38
	v_lshl_add_u64 v[204:205], v[204:205], 0, s[60:61]
	s_mov_b32 m0, s7
	ds_read_b128 v[172:175], v244 offset:49152
	ds_read_b128 v[176:179], v244 offset:50176
	ds_read_b128 v[180:183], v244 offset:51200
	ds_read_b128 v[184:187], v244 offset:52224
	ds_read_b128 v[188:191], v244 offset:53248
	ds_read_b128 v[192:195], v244 offset:54272
	ds_read_b128 v[196:199], v244 offset:55296
	ds_read_b128 v[200:203], v244 offset:56320
	global_load_lds_dwordx4 v[204:205], off
	s_add_i32 m0, s7, 0x2000
	s_add_u32 s30, s30, 0x80080
	v_lshl_add_u64 v[204:205], v[206:207], 0, s[60:61]
	s_addc_u32 s31, s31, 0
	s_add_i32 s7, s94, s38
	global_load_lds_dwordx4 v[204:205], off
	v_lshl_add_u64 v[204:205], s[30:31], 0, v[0:1]
	s_mov_b32 m0, s7
	s_nop 0
	global_load_lds_dwordx4 v[204:205], off
	v_lshl_add_u64 v[204:205], s[30:31], 0, v[130:131]
	s_add_i32 m0, s7, 0x2000
	s_nop 0
	global_load_lds_dwordx4 v[204:205], off
	v_lshl_add_u64 v[204:205], v[208:209], 0, s[60:61]
	s_mov_b32 m0, s82
	s_nop 0
	global_load_lds_dwordx4 v[204:205], off
	v_lshl_add_u64 v[204:205], v[210:211], 0, s[60:61]
	s_mov_b32 m0, s83
	s_nop 0
	global_load_lds_dwordx4 v[204:205], off
	s_waitcnt vmcnt(8)
	s_waitcnt lgkmcnt(0)
	s_barrier
	s_setprio 1
	s_waitcnt lgkmcnt(0)
	v_mfma_f32_16x16x32_bf16 v[62:65], v[140:143], v[172:175], v[62:65]
	v_mfma_f32_16x16x32_bf16 v[58:61], v[148:151], v[172:175], v[58:61]
	v_mfma_f32_16x16x32_bf16 v[42:45], v[148:151], v[180:183], v[42:45]
	v_mfma_f32_16x16x32_bf16 v[46:49], v[140:143], v[180:183], v[46:49]
	v_mfma_f32_16x16x32_bf16 v[30:33], v[140:143], v[188:191], v[30:33]
	v_mfma_f32_16x16x32_bf16 v[26:29], v[148:151], v[188:191], v[26:29]
	v_mfma_f32_16x16x32_bf16 v[10:13], v[148:151], v[196:199], v[10:13]
	v_mfma_f32_16x16x32_bf16 v[14:17], v[140:143], v[196:199], v[14:17]
	v_mfma_f32_16x16x32_bf16 v[62:65], v[144:147], v[176:179], v[62:65]
	v_mfma_f32_16x16x32_bf16 v[58:61], v[152:155], v[176:179], v[58:61]
	v_mfma_f32_16x16x32_bf16 v[42:45], v[152:155], v[184:187], v[42:45]
	v_mfma_f32_16x16x32_bf16 v[46:49], v[144:147], v[184:187], v[46:49]
	v_mfma_f32_16x16x32_bf16 v[30:33], v[144:147], v[192:195], v[30:33]
	v_mfma_f32_16x16x32_bf16 v[26:29], v[152:155], v[192:195], v[26:29]
	v_mfma_f32_16x16x32_bf16 v[10:13], v[152:155], v[200:203], v[10:13]
	v_mfma_f32_16x16x32_bf16 v[14:17], v[144:147], v[200:203], v[14:17]
	s_setprio 0
	s_setprio 1
	v_mfma_f32_16x16x32_bf16 v[54:57], v[156:159], v[172:175], v[54:57]
	v_mfma_f32_16x16x32_bf16 v[50:53], v[164:167], v[172:175], v[50:53]
	v_mfma_f32_16x16x32_bf16 v[34:37], v[164:167], v[180:183], v[34:37]
	v_mfma_f32_16x16x32_bf16 v[38:41], v[156:159], v[180:183], v[38:41]
	v_mfma_f32_16x16x32_bf16 v[22:25], v[156:159], v[188:191], v[22:25]
	v_mfma_f32_16x16x32_bf16 v[18:21], v[164:167], v[188:191], v[18:21]
	v_mfma_f32_16x16x32_bf16 v[2:5], v[164:167], v[196:199], v[2:5]
	v_mfma_f32_16x16x32_bf16 v[6:9], v[156:159], v[196:199], v[6:9]
	v_mfma_f32_16x16x32_bf16 v[54:57], v[160:163], v[176:179], v[54:57]
	v_mfma_f32_16x16x32_bf16 v[50:53], v[168:171], v[176:179], v[50:53]
	v_mfma_f32_16x16x32_bf16 v[34:37], v[168:171], v[184:187], v[34:37]
	v_mfma_f32_16x16x32_bf16 v[38:41], v[160:163], v[184:187], v[38:41]
	s_setprio 0
	v_mfma_f32_16x16x32_bf16 v[22:25], v[160:163], v[192:195], v[22:25]
	v_mfma_f32_16x16x32_bf16 v[18:21], v[168:171], v[192:195], v[18:21]
	v_mfma_f32_16x16x32_bf16 v[2:5], v[168:171], v[200:203], v[2:5]
	v_mfma_f32_16x16x32_bf16 v[6:9], v[160:163], v[200:203], v[6:9]
	s_barrier
	s_add_i32 s6, s6, 2
	s_add_u32 s28, s28, 0x100
	s_addc_u32 s29, s29, 0
	s_add_u32 s89, s89, 0x100
	s_addc_u32 s50, s50, 0
	s_cmp_gt_u32 s6, 29
	s_cbranch_scc0 .LBB0_1508
	s_and_b64 vcc, exec, s[14:15]
	s_cbranch_vccz .LBB0_1511
	s_barrier

; #define PG8_STAGE(bufoff, gbase, voff) do { _Pragma("unroll") for (int _i = 0; _i < 2; ++_i) \
;         __builtin_amdgcn_global_load_lds((const unsigned*)((const char*)(gbase) + (voff)[_i]), (PG8_LAS unsigned*)(lds + (bufoff) + ldsw + _i * 8192), 16, 0, 0); } while (0)
; #define PG8_WAIT_V(n) asm volatile("s_waitcnt vmcnt(" #n ")" ::: "memory")
; #define PG8_WAIT_L(n) asm volatile("s_waitcnt lgkmcnt(" #n ")" ::: "memory")
; #define PG8_BAR __builtin_amdgcn_s_barrier()
; #define PG8_SCHED __builtin_amdgcn_sched_barrier(0)
; template <class Epi, class Sched, bool ALIGN_EPI, bool F8 = false>
; __device__ __forceinline__ void gemm_phase(PG8_LAS unsigned char* lds, const Gemm g, const Sched& S, const Epi& E, int tid) {
;     ...
;         for (int t = 0; t < nt; t += 2) {
;             const bool last = (t == nt - 2);
;             const char* a1 = cA + (size_t)(t + 1) * kstep;
;             const char* a2 = last ? nA : cA + (size_t)(t + 2) * kstep; const char* b2 = last ? nB : cB + (size_t)(t + 2) * kstep;
;             const char* a3 = a2 + kstep; const char* b3 = b2 + kstep;
;             if (last && has_next) S.a_ready(nxt);
;             PG8_LDB(B0, 0, 0); PG8_LDB(B1, 0, 1); PG8_SCHED; PG8_LDA(At, 0, 0); PG8_STAGE(PG8_SA(1, 1), a1 + hstepA, voffA);
;             PG8_WAIT_V(8); PG8_WAIT_L(0); PG8_BAR; PG8_MMA(0, 0, At, B0); PG8_MMA(0, 1, At, B1); PG8_BAR; PG8_SCHED;
;             PG8_LDA(At, 0, 1); PG8_STAGE(PG8_SB(0, 0), b2, voffB); PG8_STAGE(PG8_SB(0, 1), b2 + hstepB, voffB); PG8_STAGE(PG8_SA(0, 0), a2, voffA);
;             PG8_WAIT_V(8); PG8_WAIT_L(0); PG8_BAR; PG8_MMA(1, 0, At, B0); PG8_MMA(1, 1, At, B1); PG8_BAR; PG8_SCHED;
;             PG8_LDB(B0, 1, 0); PG8_LDB(B1, 1, 1); PG8_SCHED; PG8_LDA(At, 1, 0); PG8_STAGE(PG8_SA(0, 1), a2 + hstepA, voffA);
;             PG8_WAIT_V(8); PG8_WAIT_L(0); PG8_BAR; PG8_MMA(0, 0, At, B0); PG8_MMA(0, 1, At, B1); PG8_BAR; PG8_SCHED;
;             PG8_LDA(At, 1, 1); PG8_STAGE(PG8_SB(1, 0), b3, voffB); PG8_STAGE(PG8_SB(1, 1), b3 + hstepB, voffB); PG8_STAGE(PG8_SA(1, 0), a3, voffA);
;             PG8_WAIT_V(8); PG8_WAIT_L(0); PG8_BAR; PG8_MMA(1, 0, At, B0); PG8_MMA(1, 1, At, B1); PG8_BAR; PG8_SCHED;
;         }
.LBB0_1568:
	s_add_u32 s28, s26, 0xfffc0080
	s_addc_u32 s29, s27, -1
	s_add_i32 s89, 0, 0x10000
	s_cmp_eq_u32 s7, 12
	s_cselect_b32 s31, s19, s29
	s_cselect_b32 s30, s87, s28
	s_cselect_b32 s29, s17, s6
	s_cselect_b32 s28, s88, s50
	s_add_i32 s94, 0, 0x14000
	v_add_u32_e32 v142, s89, v201
	v_add_u32_e32 v168, s94, v201
	ds_read_b128 v[130:133], v142
	ds_read_b128 v[134:137], v142 offset:1024
	ds_read_b128 v[138:141], v142 offset:2048
	ds_read_b128 v[142:145], v142 offset:3072
	ds_read_b128 v[146:149], v168
	ds_read_b128 v[150:153], v168 offset:1024
	ds_read_b128 v[154:157], v168 offset:2048
	ds_read_b128 v[168:171], v168 offset:3072
	v_lshl_add_u64 v[208:209], s[26:27], 0, v[164:165]
	s_add_i32 m0, s44, 0xc000
	ds_read_b128 v[172:175], v203
	ds_read_b128 v[176:179], v203 offset:1024
	ds_read_b128 v[180:183], v203 offset:2048
	ds_read_b128 v[184:187], v203 offset:3072
	ds_read_b128 v[188:191], v203 offset:4096
	ds_read_b128 v[192:195], v203 offset:5120
	ds_read_b128 v[196:199], v203 offset:6144
	ds_read_b128 v[204:207], v203 offset:7168
	global_load_lds_dwordx4 v[208:209], off
	v_lshl_add_u64 v[208:209], s[26:27], 0, v[166:167]
	s_add_i32 m0, s44, 0xe000
	s_nop 0
	global_load_lds_dwordx4 v[208:209], off
	s_waitcnt vmcnt(8)
	s_waitcnt lgkmcnt(0)
	s_barrier
	s_setprio 1
	s_waitcnt lgkmcnt(0)
	v_mfma_f32_16x16x32_bf16 v[126:129], v[130:133], v[172:175], v[126:129]
	v_mfma_f32_16x16x32_bf16 v[122:125], v[138:141], v[172:175], v[122:125]
	v_mfma_f32_16x16x32_bf16 v[106:109], v[138:141], v[180:183], v[106:109]
	v_mfma_f32_16x16x32_bf16 v[110:113], v[130:133], v[180:183], v[110:113]
	v_mfma_f32_16x16x32_bf16 v[94:97], v[130:133], v[188:191], v[94:97]
	v_mfma_f32_16x16x32_bf16 v[90:93], v[138:141], v[188:191], v[90:93]
	v_mfma_f32_16x16x32_bf16 v[74:77], v[138:141], v[196:199], v[74:77]
	v_mfma_f32_16x16x32_bf16 v[78:81], v[130:133], v[196:199], v[78:81]
	v_mfma_f32_16x16x32_bf16 v[126:129], v[134:137], v[176:179], v[126:129]
	v_mfma_f32_16x16x32_bf16 v[122:125], v[142:145], v[176:179], v[122:125]
	v_mfma_f32_16x16x32_bf16 v[106:109], v[142:145], v[184:187], v[106:109]
	v_mfma_f32_16x16x32_bf16 v[110:113], v[134:137], v[184:187], v[110:113]
	v_mfma_f32_16x16x32_bf16 v[94:97], v[134:137], v[192:195], v[94:97]
	v_mfma_f32_16x16x32_bf16 v[90:93], v[142:145], v[192:195], v[90:93]
	v_mfma_f32_16x16x32_bf16 v[74:77], v[142:145], v[204:207], v[74:77]
	v_mfma_f32_16x16x32_bf16 v[78:81], v[134:137], v[204:207], v[78:81]
	s_setprio 0
	s_setprio 1
	v_mfma_f32_16x16x32_bf16 v[118:121], v[146:149], v[172:175], v[118:121]
	v_mfma_f32_16x16x32_bf16 v[114:117], v[154:157], v[172:175], v[114:117]
	v_mfma_f32_16x16x32_bf16 v[98:101], v[154:157], v[180:183], v[98:101]
	v_mfma_f32_16x16x32_bf16 v[102:105], v[146:149], v[180:183], v[102:105]
	v_mfma_f32_16x16x32_bf16 v[86:89], v[146:149], v[188:191], v[86:89]
	v_mfma_f32_16x16x32_bf16 v[82:85], v[154:157], v[188:191], v[82:85]
	v_mfma_f32_16x16x32_bf16 v[66:69], v[154:157], v[196:199], v[66:69]
	v_mfma_f32_16x16x32_bf16 v[70:73], v[146:149], v[196:199], v[70:73]
	v_mfma_f32_16x16x32_bf16 v[118:121], v[150:153], v[176:179], v[118:121]
	v_mfma_f32_16x16x32_bf16 v[114:117], v[168:171], v[176:179], v[114:117]
	v_mfma_f32_16x16x32_bf16 v[98:101], v[168:171], v[184:187], v[98:101]
	v_mfma_f32_16x16x32_bf16 v[102:105], v[150:153], v[184:187], v[102:105]
	s_setprio 0
	v_mfma_f32_16x16x32_bf16 v[86:89], v[150:153], v[192:195], v[86:89]
	v_mfma_f32_16x16x32_bf16 v[82:85], v[168:171], v[192:195], v[82:85]
	v_mfma_f32_16x16x32_bf16 v[66:69], v[168:171], v[204:207], v[66:69]
	v_mfma_f32_16x16x32_bf16 v[70:73], v[150:153], v[204:207], v[70:73]
	s_barrier
	s_add_i32 s89, s89, s39
	v_lshl_add_u64 v[208:209], s[28:29], 0, v[0:1]
	s_mov_b32 m0, s89
	ds_read_b128 v[172:175], v203 offset:16384
	ds_read_b128 v[176:179], v203 offset:17408
	ds_read_b128 v[180:183], v203 offset:18432
	ds_read_b128 v[184:187], v203 offset:19456
	ds_read_b128 v[188:191], v203 offset:20480
	ds_read_b128 v[192:195], v203 offset:21504
	ds_read_b128 v[196:199], v203 offset:22528
	ds_read_b128 v[204:207], v203 offset:23552
	global_load_lds_dwordx4 v[208:209], off
	s_add_i32 m0, s89, 0x2000
	s_add_u32 vcc_lo, s28, 0x40000
	v_lshl_add_u64 v[210:211], s[28:29], 0, v[158:159]
	s_addc_u32 vcc_hi, s29, 0
	s_add_i32 s89, s94, s39
	global_load_lds_dwordx4 v[210:211], off
	v_lshl_add_u64 v[212:213], vcc, 0, v[0:1]
	s_mov_b32 m0, s89
	v_lshl_add_u64 v[214:215], s[30:31], 0, v[160:161]
	global_load_lds_dwordx4 v[212:213], off
	v_lshl_add_u64 v[212:213], vcc, 0, v[158:159]
	s_add_i32 m0, s89, 0x2000
	s_nop 0
	global_load_lds_dwordx4 v[212:213], off
	v_lshl_add_u64 v[212:213], s[30:31], 0, v[162:163]
	s_mov_b32 m0, s44
	s_nop 0
	global_load_lds_dwordx4 v[212:213], off
	s_mov_b32 m0, s45
	s_nop 0
	global_load_lds_dwordx4 v[214:215], off
	s_waitcnt vmcnt(8)
	s_waitcnt lgkmcnt(0)
	s_barrier
; #define PG8_STAGE(bufoff, gbase, voff) do { _Pragma("unroll") for (int _i = 0; _i < 2; ++_i) \
;         __builtin_amdgcn_global_load_lds((const unsigned*)((const char*)(gbase) + (voff)[_i]), (PG8_LAS unsigned*)(lds + (bufoff) + ldsw + _i * 8192), 16, 0, 0); } while (0)
; #define PG8_WAIT_V(n) asm volatile("s_waitcnt vmcnt(" #n ")" ::: "memory")
; #define PG8_WAIT_L(n) asm volatile("s_waitcnt lgkmcnt(" #n ")" ::: "memory")
; #define PG8_BAR __builtin_amdgcn_s_barrier()
; #define PG8_SCHED __builtin_amdgcn_sched_barrier(0)
; template <class Epi, class Sched, bool ALIGN_EPI, bool F8 = false>
; __device__ __forceinline__ void gemm_phase(PG8_LAS unsigned char* lds, const Gemm g, const Sched& S, const Epi& E, int tid) {
;     ...
;         for (int t = 0; t < nt; t += 2) {
;             const bool last = (t == nt - 2);
;             const char* a1 = cA + (size_t)(t + 1) * kstep;
;             const char* a2 = last ? nA : cA + (size_t)(t + 2) * kstep; const char* b2 = last ? nB : cB + (size_t)(t + 2) * kstep;
;             const char* a3 = a2 + kstep; const char* b3 = b2 + kstep;
;             if (last && has_next) S.a_ready(nxt);
;             PG8_LDB(B0, 0, 0); PG8_LDB(B1, 0, 1); PG8_SCHED; PG8_LDA(At, 0, 0); PG8_STAGE(PG8_SA(1, 1), a1 + hstepA, voffA);
;             PG8_WAIT_V(8); PG8_WAIT_L(0); PG8_BAR; PG8_MMA(0, 0, At, B0); PG8_MMA(0, 1, At, B1); PG8_BAR; PG8_SCHED;
;             PG8_LDA(At, 0, 1); PG8_STAGE(PG8_SB(0, 0), b2, voffB); PG8_STAGE(PG8_SB(0, 1), b2 + hstepB, voffB); PG8_STAGE(PG8_SA(0, 0), a2, voffA);
;             PG8_WAIT_V(8); PG8_WAIT_L(0); PG8_BAR; PG8_MMA(1, 0, At, B0); PG8_MMA(1, 1, At, B1); PG8_BAR; PG8_SCHED;
;             PG8_LDB(B0, 1, 0); PG8_LDB(B1, 1, 1); PG8_SCHED; PG8_LDA(At, 1, 0); PG8_STAGE(PG8_SA(0, 1), a2 + hstepA, voffA);
;             PG8_WAIT_V(8); PG8_WAIT_L(0); PG8_BAR; PG8_MMA(0, 0, At, B0); PG8_MMA(0, 1, At, B1); PG8_BAR; PG8_SCHED;
;             PG8_LDA(At, 1, 1); PG8_STAGE(PG8_SB(1, 0), b3, voffB); PG8_STAGE(PG8_SB(1, 1), b3 + hstepB, voffB); PG8_STAGE(PG8_SA(1, 0), a3, voffA);
;             PG8_WAIT_V(8); PG8_WAIT_L(0); PG8_BAR; PG8_MMA(1, 0, At, B0); PG8_MMA(1, 1, At, B1); PG8_BAR; PG8_SCHED;
;         }
	s_setprio 1
	s_waitcnt lgkmcnt(0)
	v_mfma_f32_16x16x32_bf16 v[62:65], v[130:133], v[172:175], v[62:65]
	v_mfma_f32_16x16x32_bf16 v[58:61], v[138:141], v[172:175], v[58:61]
	v_mfma_f32_16x16x32_bf16 v[42:45], v[138:141], v[180:183], v[42:45]
	v_mfma_f32_16x16x32_bf16 v[46:49], v[130:133], v[180:183], v[46:49]
	v_mfma_f32_16x16x32_bf16 v[30:33], v[130:133], v[188:191], v[30:33]
	v_mfma_f32_16x16x32_bf16 v[26:29], v[138:141], v[188:191], v[26:29]
	v_mfma_f32_16x16x32_bf16 v[10:13], v[138:141], v[196:199], v[10:13]
	v_mfma_f32_16x16x32_bf16 v[14:17], v[130:133], v[196:199], v[14:17]
	v_mfma_f32_16x16x32_bf16 v[62:65], v[134:137], v[176:179], v[62:65]
	v_mfma_f32_16x16x32_bf16 v[58:61], v[142:145], v[176:179], v[58:61]
	v_mfma_f32_16x16x32_bf16 v[42:45], v[142:145], v[184:187], v[42:45]
	v_mfma_f32_16x16x32_bf16 v[46:49], v[134:137], v[184:187], v[46:49]
	v_mfma_f32_16x16x32_bf16 v[30:33], v[134:137], v[192:195], v[30:33]
	v_mfma_f32_16x16x32_bf16 v[26:29], v[142:145], v[192:195], v[26:29]
	v_mfma_f32_16x16x32_bf16 v[10:13], v[142:145], v[204:207], v[10:13]
	v_mfma_f32_16x16x32_bf16 v[14:17], v[134:137], v[204:207], v[14:17]
	s_setprio 0
	s_setprio 1
	v_mfma_f32_16x16x32_bf16 v[54:57], v[146:149], v[172:175], v[54:57]
	v_mfma_f32_16x16x32_bf16 v[50:53], v[154:157], v[172:175], v[50:53]
	v_mfma_f32_16x16x32_bf16 v[34:37], v[154:157], v[180:183], v[34:37]
	v_mfma_f32_16x16x32_bf16 v[38:41], v[146:149], v[180:183], v[38:41]
	v_mfma_f32_16x16x32_bf16 v[22:25], v[146:149], v[188:191], v[22:25]
	v_mfma_f32_16x16x32_bf16 v[18:21], v[154:157], v[188:191], v[18:21]
	v_mfma_f32_16x16x32_bf16 v[2:5], v[154:157], v[196:199], v[2:5]
	v_mfma_f32_16x16x32_bf16 v[6:9], v[146:149], v[196:199], v[6:9]
	v_mfma_f32_16x16x32_bf16 v[54:57], v[150:153], v[176:179], v[54:57]
	v_mfma_f32_16x16x32_bf16 v[50:53], v[168:171], v[176:179], v[50:53]
	v_mfma_f32_16x16x32_bf16 v[34:37], v[168:171], v[184:187], v[34:37]
	v_mfma_f32_16x16x32_bf16 v[38:41], v[150:153], v[184:187], v[38:41]
	s_setprio 0
	v_mfma_f32_16x16x32_bf16 v[22:25], v[150:153], v[192:195], v[22:25]
	v_mfma_f32_16x16x32_bf16 v[18:21], v[168:171], v[192:195], v[18:21]
	v_mfma_f32_16x16x32_bf16 v[2:5], v[168:171], v[204:207], v[2:5]
	v_mfma_f32_16x16x32_bf16 v[6:9], v[150:153], v[204:207], v[6:9]
	s_barrier
	s_add_i32 s89, 0, 0x18000
	s_add_i32 s94, 0, 0x1c000
	v_add_u32_e32 v142, s89, v201
	v_add_u32_e32 v168, s94, v201
	ds_read_b128 v[130:133], v142
	ds_read_b128 v[134:137], v142 offset:1024
	ds_read_b128 v[138:141], v142 offset:2048
	ds_read_b128 v[142:145], v142 offset:3072
	ds_read_b128 v[146:149], v168
	ds_read_b128 v[150:153], v168 offset:1024
	ds_read_b128 v[154:157], v168 offset:2048
	ds_read_b128 v[168:171], v168 offset:3072
	s_add_u32 s30, s30, 0x40000
	s_addc_u32 s31, s31, 0
	s_mov_b32 m0, s51
	v_lshl_add_u64 v[216:217], s[30:31], 0, v[162:163]
	ds_read_b128 v[172:175], v203 offset:32768
	ds_read_b128 v[176:179], v203 offset:33792
	ds_read_b128 v[180:183], v203 offset:34816
	ds_read_b128 v[184:187], v203 offset:35840
	ds_read_b128 v[188:191], v203 offset:36864
	ds_read_b128 v[192:195], v203 offset:37888
	ds_read_b128 v[196:199], v203 offset:38912
	ds_read_b128 v[204:207], v203 offset:39936
	global_load_lds_dwordx4 v[216:217], off
	v_lshl_add_u64 v[216:217], s[30:31], 0, v[160:161]
	s_mov_b32 m0, s68
	s_nop 0
	global_load_lds_dwordx4 v[216:217], off
	s_waitcnt vmcnt(8)
	s_waitcnt lgkmcnt(0)
	s_barrier
	s_setprio 1
	s_waitcnt lgkmcnt(0)
	v_mfma_f32_16x16x32_bf16 v[126:129], v[130:133], v[172:175], v[126:129]
	v_mfma_f32_16x16x32_bf16 v[122:125], v[138:141], v[172:175], v[122:125]
	v_mfma_f32_16x16x32_bf16 v[106:109], v[138:141], v[180:183], v[106:109]
	v_mfma_f32_16x16x32_bf16 v[110:113], v[130:133], v[180:183], v[110:113]
	v_mfma_f32_16x16x32_bf16 v[94:97], v[130:133], v[188:191], v[94:97]
	v_mfma_f32_16x16x32_bf16 v[90:93], v[138:141], v[188:191], v[90:93]
	v_mfma_f32_16x16x32_bf16 v[74:77], v[138:141], v[196:199], v[74:77]
	v_mfma_f32_16x16x32_bf16 v[78:81], v[130:133], v[196:199], v[78:81]
	v_mfma_f32_16x16x32_bf16 v[126:129], v[134:137], v[176:179], v[126:129]
	v_mfma_f32_16x16x32_bf16 v[122:125], v[142:145], v[176:179], v[122:125]
	v_mfma_f32_16x16x32_bf16 v[106:109], v[142:145], v[184:187], v[106:109]
	v_mfma_f32_16x16x32_bf16 v[110:113], v[134:137], v[184:187], v[110:113]
	v_mfma_f32_16x16x32_bf16 v[94:97], v[134:137], v[192:195], v[94:97]
	v_mfma_f32_16x16x32_bf16 v[90:93], v[142:145], v[192:195], v[90:93]
	v_mfma_f32_16x16x32_bf16 v[74:77], v[142:145], v[204:207], v[74:77]
	v_mfma_f32_16x16x32_bf16 v[78:81], v[134:137], v[204:207], v[78:81]
	s_setprio 0
	s_setprio 1
	v_mfma_f32_16x16x32_bf16 v[118:121], v[146:149], v[172:175], v[118:121]
	v_mfma_f32_16x16x32_bf16 v[114:117], v[154:157], v[172:175], v[114:117]
	v_mfma_f32_16x16x32_bf16 v[98:101], v[154:157], v[180:183], v[98:101]
	v_mfma_f32_16x16x32_bf16 v[102:105], v[146:149], v[180:183], v[102:105]
	v_mfma_f32_16x16x32_bf16 v[86:89], v[146:149], v[188:191], v[86:89]
	v_mfma_f32_16x16x32_bf16 v[82:85], v[154:157], v[188:191], v[82:85]
	v_mfma_f32_16x16x32_bf16 v[66:69], v[154:157], v[196:199], v[66:69]
	v_mfma_f32_16x16x32_bf16 v[70:73], v[146:149], v[196:199], v[70:73]
	v_mfma_f32_16x16x32_bf16 v[118:121], v[150:153], v[176:179], v[118:121]
	v_mfma_f32_16x16x32_bf16 v[114:117], v[168:171], v[176:179], v[114:117]
	v_mfma_f32_16x16x32_bf16 v[98:101], v[168:171], v[184:187], v[98:101]
	v_mfma_f32_16x16x32_bf16 v[102:105], v[150:153], v[184:187], v[102:105]
	s_setprio 0
	v_mfma_f32_16x16x32_bf16 v[86:89], v[150:153], v[192:195], v[86:89]
	v_mfma_f32_16x16x32_bf16 v[82:85], v[168:171], v[192:195], v[82:85]
	v_mfma_f32_16x16x32_bf16 v[66:69], v[168:171], v[204:207], v[66:69]
	v_mfma_f32_16x16x32_bf16 v[70:73], v[150:153], v[204:207], v[70:73]
	s_barrier
; #define PG8_STAGE(bufoff, gbase, voff) do { _Pragma("unroll") for (int _i = 0; _i < 2; ++_i) \
;         __builtin_amdgcn_global_load_lds((const unsigned*)((const char*)(gbase) + (voff)[_i]), (PG8_LAS unsigned*)(lds + (bufoff) + ldsw + _i * 8192), 16, 0, 0); } while (0)
; #define PG8_WAIT_V(n) asm volatile("s_waitcnt vmcnt(" #n ")" ::: "memory")
; #define PG8_WAIT_L(n) asm volatile("s_waitcnt lgkmcnt(" #n ")" ::: "memory")
; #define PG8_BAR __builtin_amdgcn_s_barrier()
; #define PG8_SCHED __builtin_amdgcn_sched_barrier(0)
; template <class Epi, class Sched, bool ALIGN_EPI, bool F8 = false>
; __device__ __forceinline__ void gemm_phase(PG8_LAS unsigned char* lds, const Gemm g, const Sched& S, const Epi& E, int tid) {
;     ...
;         for (int t = 0; t < nt; t += 2) {
;             const bool last = (t == nt - 2);
;             const char* a1 = cA + (size_t)(t + 1) * kstep;
;             const char* a2 = last ? nA : cA + (size_t)(t + 2) * kstep; const char* b2 = last ? nB : cB + (size_t)(t + 2) * kstep;
;             const char* a3 = a2 + kstep; const char* b3 = b2 + kstep;
;             if (last && has_next) S.a_ready(nxt);
;             PG8_LDB(B0, 0, 0); PG8_LDB(B1, 0, 1); PG8_SCHED; PG8_LDA(At, 0, 0); PG8_STAGE(PG8_SA(1, 1), a1 + hstepA, voffA);
;             PG8_WAIT_V(8); PG8_WAIT_L(0); PG8_BAR; PG8_MMA(0, 0, At, B0); PG8_MMA(0, 1, At, B1); PG8_BAR; PG8_SCHED;
;             PG8_LDA(At, 0, 1); PG8_STAGE(PG8_SB(0, 0), b2, voffB); PG8_STAGE(PG8_SB(0, 1), b2 + hstepB, voffB); PG8_STAGE(PG8_SA(0, 0), a2, voffA);
;             PG8_WAIT_V(8); PG8_WAIT_L(0); PG8_BAR; PG8_MMA(1, 0, At, B0); PG8_MMA(1, 1, At, B1); PG8_BAR; PG8_SCHED;
;             PG8_LDB(B0, 1, 0); PG8_LDB(B1, 1, 1); PG8_SCHED; PG8_LDA(At, 1, 0); PG8_STAGE(PG8_SA(0, 1), a2 + hstepA, voffA);
;             PG8_WAIT_V(8); PG8_WAIT_L(0); PG8_BAR; PG8_MMA(0, 0, At, B0); PG8_MMA(0, 1, At, B1); PG8_BAR; PG8_SCHED;
;             PG8_LDA(At, 1, 1); PG8_STAGE(PG8_SB(1, 0), b3, voffB); PG8_STAGE(PG8_SB(1, 1), b3 + hstepB, voffB); PG8_STAGE(PG8_SA(1, 0), a3, voffA);
;             PG8_WAIT_V(8); PG8_WAIT_L(0); PG8_BAR; PG8_MMA(1, 0, At, B0); PG8_MMA(1, 1, At, B1); PG8_BAR; PG8_SCHED;
;         }
;         if constexpr (ALIGN_EPI) { if (wr == 0) PG8_BAR; }
	s_add_i32 s30, s89, s39
	v_lshl_add_u64 v[208:209], v[208:209], 0, s[60:61]
	s_mov_b32 m0, s30
	ds_read_b128 v[172:175], v203 offset:49152
	ds_read_b128 v[176:179], v203 offset:50176
	ds_read_b128 v[180:183], v203 offset:51200
	ds_read_b128 v[184:187], v203 offset:52224
	ds_read_b128 v[188:191], v203 offset:53248
	ds_read_b128 v[192:195], v203 offset:54272
	ds_read_b128 v[196:199], v203 offset:55296
	ds_read_b128 v[204:207], v203 offset:56320
	global_load_lds_dwordx4 v[208:209], off
	s_add_i32 m0, s30, 0x2000
	s_add_u32 s28, s28, 0x40080
	v_lshl_add_u64 v[208:209], v[210:211], 0, s[60:61]
	s_addc_u32 s29, s29, 0
	s_add_i32 s30, s94, s39
	global_load_lds_dwordx4 v[208:209], off
	v_lshl_add_u64 v[208:209], s[28:29], 0, v[0:1]
	s_mov_b32 m0, s30
	s_nop 0
	global_load_lds_dwordx4 v[208:209], off
	v_lshl_add_u64 v[208:209], s[28:29], 0, v[158:159]
	s_add_i32 m0, s30, 0x2000
	s_nop 0
	global_load_lds_dwordx4 v[208:209], off
	v_lshl_add_u64 v[208:209], v[212:213], 0, s[60:61]
	s_mov_b32 m0, s82
	s_nop 0
	global_load_lds_dwordx4 v[208:209], off
	v_lshl_add_u64 v[208:209], v[214:215], 0, s[60:61]
	s_mov_b32 m0, s83
	s_nop 0
	global_load_lds_dwordx4 v[208:209], off
	s_waitcnt vmcnt(8)
	s_waitcnt lgkmcnt(0)
	s_barrier
	s_setprio 1
	s_waitcnt lgkmcnt(0)
	v_mfma_f32_16x16x32_bf16 v[62:65], v[130:133], v[172:175], v[62:65]
	v_mfma_f32_16x16x32_bf16 v[58:61], v[138:141], v[172:175], v[58:61]
	v_mfma_f32_16x16x32_bf16 v[42:45], v[138:141], v[180:183], v[42:45]
	v_mfma_f32_16x16x32_bf16 v[46:49], v[130:133], v[180:183], v[46:49]
	v_mfma_f32_16x16x32_bf16 v[30:33], v[130:133], v[188:191], v[30:33]
	v_mfma_f32_16x16x32_bf16 v[26:29], v[138:141], v[188:191], v[26:29]
	v_mfma_f32_16x16x32_bf16 v[10:13], v[138:141], v[196:199], v[10:13]
	v_mfma_f32_16x16x32_bf16 v[14:17], v[130:133], v[196:199], v[14:17]
	v_mfma_f32_16x16x32_bf16 v[62:65], v[134:137], v[176:179], v[62:65]
	v_mfma_f32_16x16x32_bf16 v[58:61], v[142:145], v[176:179], v[58:61]
	v_mfma_f32_16x16x32_bf16 v[42:45], v[142:145], v[184:187], v[42:45]
	v_mfma_f32_16x16x32_bf16 v[46:49], v[134:137], v[184:187], v[46:49]
	v_mfma_f32_16x16x32_bf16 v[30:33], v[134:137], v[192:195], v[30:33]
	v_mfma_f32_16x16x32_bf16 v[26:29], v[142:145], v[192:195], v[26:29]
	v_mfma_f32_16x16x32_bf16 v[10:13], v[142:145], v[204:207], v[10:13]
	v_mfma_f32_16x16x32_bf16 v[14:17], v[134:137], v[204:207], v[14:17]
	s_setprio 0
	s_setprio 1
	v_mfma_f32_16x16x32_bf16 v[54:57], v[146:149], v[172:175], v[54:57]
	v_mfma_f32_16x16x32_bf16 v[50:53], v[154:157], v[172:175], v[50:53]
	v_mfma_f32_16x16x32_bf16 v[34:37], v[154:157], v[180:183], v[34:37]
	v_mfma_f32_16x16x32_bf16 v[38:41], v[146:149], v[180:183], v[38:41]
	v_mfma_f32_16x16x32_bf16 v[22:25], v[146:149], v[188:191], v[22:25]
	v_mfma_f32_16x16x32_bf16 v[18:21], v[154:157], v[188:191], v[18:21]
	v_mfma_f32_16x16x32_bf16 v[2:5], v[154:157], v[196:199], v[2:5]
	v_mfma_f32_16x16x32_bf16 v[6:9], v[146:149], v[196:199], v[6:9]
	v_mfma_f32_16x16x32_bf16 v[54:57], v[150:153], v[176:179], v[54:57]
	v_mfma_f32_16x16x32_bf16 v[50:53], v[168:171], v[176:179], v[50:53]
	v_mfma_f32_16x16x32_bf16 v[34:37], v[168:171], v[184:187], v[34:37]
	v_mfma_f32_16x16x32_bf16 v[38:41], v[150:153], v[184:187], v[38:41]
	s_setprio 0
	v_mfma_f32_16x16x32_bf16 v[22:25], v[150:153], v[192:195], v[22:25]
	v_mfma_f32_16x16x32_bf16 v[18:21], v[168:171], v[192:195], v[18:21]
	v_mfma_f32_16x16x32_bf16 v[2:5], v[168:171], v[204:207], v[2:5]
	v_mfma_f32_16x16x32_bf16 v[6:9], v[150:153], v[204:207], v[6:9]
	s_barrier
	s_add_i32 s7, s7, 2
	s_add_u32 s26, s26, 0x100
	s_addc_u32 s27, s27, 0
	s_add_u32 s50, s50, 0x100
	s_addc_u32 s6, s6, 0
	s_cmp_gt_u32 s7, 13
	s_cbranch_scc0 .LBB0_1568
; __device__ __forceinline__ float sum_xor16(float v) { auto r = __builtin_amdgcn_permlane16_swap(__float_as_uint(v), __float_as_uint(v), false, false); return __uint_as_float(r[0]) + __uint_as_float(r[1]); }
; __device__ __forceinline__ float sum_xor32(float v) { auto r = __builtin_amdgcn_permlane32_swap(__float_as_uint(v), __float_as_uint(v), false, false); return __uint_as_float(r[0]) + __uint_as_float(r[1]); }
; __device__ __forceinline__ float bf_lo(unsigned w) { return __uint_as_float(w << 16); }
;     __device__ __forceinline__ void operator()(const f32x4 (&acc)[2][2][4][2], const Unit& u, int wr, int wc, int fr, int fq) const {
;         const int row0 = u.pm * BM + wr * 64 + fr, col0 = u.pn * BM + wc * 32 + 8 * fq;
; #pragma unroll
;         for (int ai = 0; ai < 2; ++ai) {
;             u32x4 old[4][2];
; #pragma unroll
;             for (int m = 0; m < 4; ++m)
; #pragma unroll
;                 for (int bj = 0; bj < 2; ++bj) old[m][bj] = *(const u32x4*)(xb + (size_t)(row0 + ai * HALF + m * 16) * 2048 + col0 + bj * HALF);
; #pragma unroll
;             for (int m = 0; m < 4; ++m) { const size_t row = (size_t)(row0 + ai * HALF + m * 16); bf16_t* rowp = xb + row * 2048 + col0; float ss = 0.f;
; #pragma unroll
;                 for (int bj = 0; bj < 2; ++bj) { const u32x4 oo = old[m][bj]; const f32x4 a0 = acc[ai][bj][m][0], a1 = acc[ai][bj][m][1];
;                     const float x0 = a0[0] + bf_lo(oo.x), x1 = a0[1] + bf_hi(oo.x), x2 = a0[2] + bf_lo(oo.y), x3 = a0[3] + bf_hi(oo.y), x4 = a1[0] + bf_lo(oo.z), x5 = a1[1] + bf_hi(oo.z), x6 = a1[2] + bf_lo(oo.w), x7 = a1[3] + bf_hi(oo.w);
;                     ss += (x0 * x0 + x1 * x1) + (x2 * x2 + x3 * x3) + (x4 * x4 + x5 * x5) + (x6 * x6 + x7 * x7);
;                     u32x4 w; w.x = cvt_pk_bf16(x0, x1); w.y = cvt_pk_bf16(x2, x3); w.z = cvt_pk_bf16(x4, x5); w.w = cvt_pk_bf16(x6, x7);
;                     *(u32x4*)(rowp + bj * HALF) = w;
;                     if (h8) { u32x2 q; q.x = pk4_fp8_(x0 * F8_SA_, x1 * F8_SA_, x2 * F8_SA_, x3 * F8_SA_); q.y = pk4_fp8_(x4 * F8_SA_, x5 * F8_SA_, x6 * F8_SA_, x7 * F8_SA_);
;                         *(u32x2*)(h8 + row * 2048 + col0 + bj * HALF) = q; } }
;                 ss = sum_xor32(sum_xor16(ss));
;                 if (fq == 0) SS[row * 32 + u.pn * 4 + wc] = ss; }
;             asm volatile("" ::: "memory"); }
	v_lshl_or_b32 v168, s85, 8, v202
	v_lshl_add_u32 v172, s86, 8, v200
	v_ashrrev_i32_e32 v169, 31, v168
	v_lshlrev_b64 v[182:183], 1, v[168:169]
	v_ashrrev_i32_e32 v173, 31, v172
	v_lshl_add_u64 v[170:171], s[12:13], 0, v[182:183]
	v_lshlrev_b64 v[184:185], 12, v[172:173]
	v_lshl_add_u64 v[130:131], v[170:171], 0, v[184:185]
	global_load_dwordx4 v[178:181], v[130:131], off
	global_load_dwordx4 v[154:157], v[130:131], off offset:256
	v_or_b32_e32 v192, 16, v172
	v_ashrrev_i32_e32 v193, 31, v192
	v_or_b32_e32 v176, 32, v172
	v_lshlrev_b64 v[196:197], 12, v[192:193]
	v_ashrrev_i32_e32 v177, 31, v176
	v_or_b32_e32 v174, 48, v172
	v_lshl_add_u64 v[130:131], v[170:171], 0, v[196:197]
	v_lshlrev_b64 v[194:195], 12, v[176:177]
	v_ashrrev_i32_e32 v175, 31, v174
	global_load_dwordx4 v[150:153], v[130:131], off
	global_load_dwordx4 v[146:149], v[130:131], off offset:256
	v_lshl_add_u64 v[130:131], v[170:171], 0, v[194:195]
	v_lshlrev_b64 v[190:191], 12, v[174:175]
	global_load_dwordx4 v[142:145], v[130:131], off
	global_load_dwordx4 v[138:141], v[130:131], off offset:256
	v_lshl_add_u64 v[130:131], v[170:171], 0, v[190:191]
	global_load_dwordx4 v[134:137], v[130:131], off
	s_nop 0
	global_load_dwordx4 v[130:133], v[130:131], off offset:256
	v_lshl_add_u64 v[184:185], s[12:13], 0, v[184:185]
	v_lshl_add_u64 v[198:199], v[184:185], 0, v[182:183]
	s_waitcnt vmcnt(0)
	v_lshlrev_b32_e32 v182, 16, v178
	v_and_b32_e32 v178, 0xffff0000, v178
	v_add_f32_e32 v127, v127, v178
	v_lshlrev_b32_e32 v178, 16, v179
	v_add_f32_e32 v128, v128, v178
	v_and_b32_e32 v178, 0xffff0000, v179
	v_add_f32_e32 v129, v129, v178
	v_lshlrev_b32_e32 v178, 16, v180
	v_add_f32_e32 v178, v122, v178
	v_and_b32_e32 v122, 0xffff0000, v180
	v_add_f32_e32 v179, v123, v122
	v_lshlrev_b32_e32 v122, 16, v181
	v_add_f32_e32 v180, v124, v122
	v_and_b32_e32 v122, 0xffff0000, v181
	v_add_f32_e32 v126, v126, v182
	v_add_f32_e32 v125, v125, v122
	v_mul_f32_e32 v122, v127, v127
	v_mul_f32_e32 v123, v129, v129
	v_fmac_f32_e32 v122, v126, v126
	v_fmac_f32_e32 v123, v128, v128
	v_add_f32_e32 v122, v122, v123
	v_mul_f32_e32 v123, v179, v179
	v_fmac_f32_e32 v123, v178, v178
	v_add_f32_e32 v122, v123, v122
	v_mul_f32_e32 v123, v125, v125
	v_fmac_f32_e32 v123, v180, v180
	v_add_f32_e32 v181, v123, v122
	v_cvt_pk_bf16_f32 v122, v126, v127
	v_cvt_pk_bf16_f32 v123, v128, v129
	v_cvt_pk_bf16_f32 v124, v178, v179
	v_cvt_pk_bf16_f32 v125, v180, v125
	global_store_dwordx4 v[198:199], v[122:125], off
	s_nop 1
	v_lshlrev_b32_e32 v122, 16, v154
	v_add_f32_e32 v118, v118, v122
	v_and_b32_e32 v122, 0xffff0000, v154
	v_add_f32_e32 v119, v119, v122
	v_lshlrev_b32_e32 v122, 16, v155
	v_add_f32_e32 v120, v120, v122
	v_and_b32_e32 v122, 0xffff0000, v155
	v_add_f32_e32 v121, v121, v122
	v_lshlrev_b32_e32 v122, 16, v156
	v_add_f32_e32 v122, v114, v122
	v_and_b32_e32 v114, 0xffff0000, v156
	v_add_f32_e32 v123, v115, v114
	v_lshlrev_b32_e32 v114, 16, v157
	v_add_f32_e32 v124, v116, v114
	v_and_b32_e32 v114, 0xffff0000, v157
	v_add_f32_e32 v117, v117, v114
	v_mul_f32_e32 v114, v119, v119
	v_mul_f32_e32 v115, v121, v121
	v_fmac_f32_e32 v114, v118, v118
	v_fmac_f32_e32 v115, v120, v120
	v_add_f32_e32 v114, v114, v115
	v_mul_f32_e32 v115, v123, v123
	v_fmac_f32_e32 v115, v122, v122
	v_add_f32_e32 v114, v115, v114
	v_mul_f32_e32 v115, v117, v117
	v_fmac_f32_e32 v115, v124, v124
	v_add_f32_e32 v114, v115, v114
	v_add_f32_e32 v125, v181, v114
	v_cvt_pk_bf16_f32 v114, v118, v119
	v_cvt_pk_bf16_f32 v115, v120, v121
	v_cvt_pk_bf16_f32 v116, v122, v123
	v_cvt_pk_bf16_f32 v117, v124, v117
	global_store_dwordx4 v[198:199], v[114:117], off offset:256
	s_nop 1
	v_mov_b32_e32 v114, v125
	s_nop 1
	v_permlane16_swap_b32_e32 v125, v114
	v_add_f32_e32 v114, v125, v114
	v_mov_b32_e32 v115, v114
	s_nop 1
	v_permlane32_swap_b32_e32 v114, v115
	s_and_saveexec_b64 s[26:27], s[8:9]
	s_cbranch_execz .LBB0_1571
	v_add_f32_e32 v116, v114, v115
	s_lshl_b32 s6, s85, 2
	v_lshlrev_b64 v[114:115], 7, v[172:173]
	s_ashr_i32 s7, s6, 31
	v_lshl_add_u64 v[114:115], s[14:15], 0, v[114:115]
	v_lshl_add_u64 v[114:115], s[6:7], 2, v[114:115]
	s_lshl_b32 s94, s69, 2
	v_lshl_add_u64 v[114:115], v[114:115], 0, s[94:95]
	global_store_dword v[114:115], v116, off

; #define PG8_STAGE(bufoff, gbase, voff) do { _Pragma("unroll") for (int _i = 0; _i < 2; ++_i) \
;         __builtin_amdgcn_global_load_lds((const unsigned*)((const char*)(gbase) + (voff)[_i]), (PG8_LAS unsigned*)(lds + (bufoff) + ldsw + _i * 8192), 16, 0, 0); } while (0)
; #define PG8_WAIT_V(n) asm volatile("s_waitcnt vmcnt(" #n ")" ::: "memory")
; #define PG8_WAIT_L(n) asm volatile("s_waitcnt lgkmcnt(" #n ")" ::: "memory")
; #define PG8_BAR __builtin_amdgcn_s_barrier()
; #define PG8_SCHED __builtin_amdgcn_sched_barrier(0)
; template <class Epi, class Sched, bool ALIGN_EPI, bool F8 = false>
; __device__ __forceinline__ void gemm_phase(PG8_LAS unsigned char* lds, const Gemm g, const Sched& S, const Epi& E, int tid) {
;     ...
;         for (int t = 0; t < nt; t += 2) {
;             const bool last = (t == nt - 2);
;             const char* a1 = cA + (size_t)(t + 1) * kstep;
;             const char* a2 = last ? nA : cA + (size_t)(t + 2) * kstep; const char* b2 = last ? nB : cB + (size_t)(t + 2) * kstep;
;             const char* a3 = a2 + kstep; const char* b3 = b2 + kstep;
;             if (last && has_next) S.a_ready(nxt);
;             PG8_LDB(B0, 0, 0); PG8_LDB(B1, 0, 1); PG8_SCHED; PG8_LDA(At, 0, 0); PG8_STAGE(PG8_SA(1, 1), a1 + hstepA, voffA);
;             PG8_WAIT_V(8); PG8_WAIT_L(0); PG8_BAR; PG8_MMA(0, 0, At, B0); PG8_MMA(0, 1, At, B1); PG8_BAR; PG8_SCHED;
;             PG8_LDA(At, 0, 1); PG8_STAGE(PG8_SB(0, 0), b2, voffB); PG8_STAGE(PG8_SB(0, 1), b2 + hstepB, voffB); PG8_STAGE(PG8_SA(0, 0), a2, voffA);
;             PG8_WAIT_V(8); PG8_WAIT_L(0); PG8_BAR; PG8_MMA(1, 0, At, B0); PG8_MMA(1, 1, At, B1); PG8_BAR; PG8_SCHED;
;             PG8_LDB(B0, 1, 0); PG8_LDB(B1, 1, 1); PG8_SCHED; PG8_LDA(At, 1, 0); PG8_STAGE(PG8_SA(0, 1), a2 + hstepA, voffA);
;             PG8_WAIT_V(8); PG8_WAIT_L(0); PG8_BAR; PG8_MMA(0, 0, At, B0); PG8_MMA(0, 1, At, B1); PG8_BAR; PG8_SCHED;
;             PG8_LDA(At, 1, 1); PG8_STAGE(PG8_SB(1, 0), b3, voffB); PG8_STAGE(PG8_SB(1, 1), b3 + hstepB, voffB); PG8_STAGE(PG8_SA(1, 0), a3, voffA);
;             PG8_WAIT_V(8); PG8_WAIT_L(0); PG8_BAR; PG8_MMA(1, 0, At, B0); PG8_MMA(1, 1, At, B1); PG8_BAR; PG8_SCHED;
;         }
;         if constexpr (ALIGN_EPI) { if (wr == 0) PG8_BAR; }
.LBB0_1619:
	s_add_u32 s28, s12, 0xfff80080
	s_addc_u32 s29, s13, -1
	s_add_i32 s88, 0, 0x10000
	s_cmp_eq_u32 s7, 28
	s_cselect_b32 s31, s23, s29
	s_cselect_b32 s30, s87, s28
	s_cselect_b32 s29, s25, s6
	s_cselect_b32 s28, s24, s50
	s_add_i32 s94, 0, 0x14000
	v_add_u32_e32 v154, s88, v169
	v_add_u32_e32 v158, s94, v169
	ds_read_b128 v[130:133], v154
	ds_read_b128 v[134:137], v154 offset:1024
	ds_read_b128 v[138:141], v154 offset:2048
	ds_read_b128 v[154:157], v154 offset:3072
	ds_read_b128 v[160:163], v158
	ds_read_b128 v[164:167], v158 offset:1024
	ds_read_b128 v[174:177], v158 offset:2048
	ds_read_b128 v[178:181], v158 offset:3072
	v_lshl_add_u64 v[214:215], s[12:13], 0, v[150:151]
	s_add_i32 m0, s39, 0xc000
	ds_read_b128 v[182:185], v172
	ds_read_b128 v[186:189], v172 offset:1024
	ds_read_b128 v[190:193], v172 offset:2048
	ds_read_b128 v[194:197], v172 offset:3072
	ds_read_b128 v[198:201], v172 offset:4096
	ds_read_b128 v[202:205], v172 offset:5120
	ds_read_b128 v[206:209], v172 offset:6144
	ds_read_b128 v[210:213], v172 offset:7168
	global_load_lds_dwordx4 v[214:215], off
	v_lshl_add_u64 v[214:215], s[12:13], 0, v[152:153]
	s_add_i32 m0, s39, 0xe000
	s_nop 0
	global_load_lds_dwordx4 v[214:215], off
	s_waitcnt vmcnt(8)
	s_waitcnt lgkmcnt(0)
	s_barrier
	s_setprio 1
	s_waitcnt lgkmcnt(0)
	v_mfma_f32_16x16x32_bf16 v[126:129], v[130:133], v[182:185], v[126:129]
	v_mfma_f32_16x16x32_bf16 v[122:125], v[138:141], v[182:185], v[122:125]
	v_mfma_f32_16x16x32_bf16 v[114:117], v[138:141], v[190:193], v[114:117]
	v_mfma_f32_16x16x32_bf16 v[118:121], v[130:133], v[190:193], v[118:121]
	v_mfma_f32_16x16x32_bf16 v[94:97], v[130:133], v[198:201], v[94:97]
	v_mfma_f32_16x16x32_bf16 v[90:93], v[138:141], v[198:201], v[90:93]
	v_mfma_f32_16x16x32_bf16 v[82:85], v[138:141], v[206:209], v[82:85]
	v_mfma_f32_16x16x32_bf16 v[86:89], v[130:133], v[206:209], v[86:89]
	v_mfma_f32_16x16x32_bf16 v[126:129], v[134:137], v[186:189], v[126:129]
	v_mfma_f32_16x16x32_bf16 v[122:125], v[154:157], v[186:189], v[122:125]
	v_mfma_f32_16x16x32_bf16 v[114:117], v[154:157], v[194:197], v[114:117]
	v_mfma_f32_16x16x32_bf16 v[118:121], v[134:137], v[194:197], v[118:121]
	v_mfma_f32_16x16x32_bf16 v[94:97], v[134:137], v[202:205], v[94:97]
	v_mfma_f32_16x16x32_bf16 v[90:93], v[154:157], v[202:205], v[90:93]
	v_mfma_f32_16x16x32_bf16 v[82:85], v[154:157], v[210:213], v[82:85]
	v_mfma_f32_16x16x32_bf16 v[86:89], v[134:137], v[210:213], v[86:89]
	s_setprio 0
	s_setprio 1
	v_mfma_f32_16x16x32_bf16 v[110:113], v[160:163], v[182:185], v[110:113]
	v_mfma_f32_16x16x32_bf16 v[106:109], v[174:177], v[182:185], v[106:109]
	v_mfma_f32_16x16x32_bf16 v[98:101], v[174:177], v[190:193], v[98:101]
	v_mfma_f32_16x16x32_bf16 v[102:105], v[160:163], v[190:193], v[102:105]
	v_mfma_f32_16x16x32_bf16 v[78:81], v[160:163], v[198:201], v[78:81]
	v_mfma_f32_16x16x32_bf16 v[74:77], v[174:177], v[198:201], v[74:77]
	v_mfma_f32_16x16x32_bf16 v[66:69], v[174:177], v[206:209], v[66:69]
	v_mfma_f32_16x16x32_bf16 v[70:73], v[160:163], v[206:209], v[70:73]
	v_mfma_f32_16x16x32_bf16 v[110:113], v[164:167], v[186:189], v[110:113]
	v_mfma_f32_16x16x32_bf16 v[106:109], v[178:181], v[186:189], v[106:109]
	v_mfma_f32_16x16x32_bf16 v[98:101], v[178:181], v[194:197], v[98:101]
	v_mfma_f32_16x16x32_bf16 v[102:105], v[164:167], v[194:197], v[102:105]
	s_setprio 0
	v_mfma_f32_16x16x32_bf16 v[78:81], v[164:167], v[202:205], v[78:81]
	v_mfma_f32_16x16x32_bf16 v[74:77], v[178:181], v[202:205], v[74:77]
	v_mfma_f32_16x16x32_bf16 v[66:69], v[178:181], v[210:213], v[66:69]
	v_mfma_f32_16x16x32_bf16 v[70:73], v[164:167], v[210:213], v[70:73]
	s_barrier
	s_add_i32 s88, s88, s38
	v_lshl_add_u64 v[214:215], s[28:29], 0, v[0:1]
	s_mov_b32 m0, s88
	ds_read_b128 v[182:185], v172 offset:16384
	ds_read_b128 v[186:189], v172 offset:17408
	ds_read_b128 v[190:193], v172 offset:18432
	ds_read_b128 v[194:197], v172 offset:19456
	ds_read_b128 v[198:201], v172 offset:20480
	ds_read_b128 v[202:205], v172 offset:21504
	ds_read_b128 v[206:209], v172 offset:22528
	ds_read_b128 v[210:213], v172 offset:23552
	global_load_lds_dwordx4 v[214:215], off
	s_add_i32 m0, s88, 0x2000
	s_add_u32 s88, s28, 0x84000
	v_lshl_add_u64 v[216:217], s[28:29], 0, v[142:143]
	s_addc_u32 s89, s29, 0
	s_add_i32 s94, s94, s38
	global_load_lds_dwordx4 v[216:217], off
	v_lshl_add_u64 v[218:219], s[88:89], 0, v[0:1]
	s_mov_b32 m0, s94
	v_lshl_add_u64 v[220:221], s[30:31], 0, v[144:145]
	global_load_lds_dwordx4 v[218:219], off
	v_lshl_add_u64 v[218:219], s[88:89], 0, v[142:143]
	s_add_i32 m0, s94, 0x2000
	s_nop 0
	global_load_lds_dwordx4 v[218:219], off
	v_lshl_add_u64 v[218:219], s[30:31], 0, v[146:147]
	s_mov_b32 m0, s39
	s_nop 0
	global_load_lds_dwordx4 v[218:219], off
	s_mov_b32 m0, s44
	s_nop 0
	global_load_lds_dwordx4 v[220:221], off
	s_waitcnt vmcnt(8)
	s_waitcnt lgkmcnt(0)
	s_barrier
; #define PG8_STAGE(bufoff, gbase, voff) do { _Pragma("unroll") for (int _i = 0; _i < 2; ++_i) \
;         __builtin_amdgcn_global_load_lds((const unsigned*)((const char*)(gbase) + (voff)[_i]), (PG8_LAS unsigned*)(lds + (bufoff) + ldsw + _i * 8192), 16, 0, 0); } while (0)
; #define PG8_WAIT_V(n) asm volatile("s_waitcnt vmcnt(" #n ")" ::: "memory")
; #define PG8_WAIT_L(n) asm volatile("s_waitcnt lgkmcnt(" #n ")" ::: "memory")
; #define PG8_BAR __builtin_amdgcn_s_barrier()
; #define PG8_SCHED __builtin_amdgcn_sched_barrier(0)
; template <class Epi, class Sched, bool ALIGN_EPI, bool F8 = false>
; __device__ __forceinline__ void gemm_phase(PG8_LAS unsigned char* lds, const Gemm g, const Sched& S, const Epi& E, int tid) {
;     ...
;         for (int t = 0; t < nt; t += 2) {
;             const bool last = (t == nt - 2);
;             const char* a1 = cA + (size_t)(t + 1) * kstep;
;             const char* a2 = last ? nA : cA + (size_t)(t + 2) * kstep; const char* b2 = last ? nB : cB + (size_t)(t + 2) * kstep;
;             const char* a3 = a2 + kstep; const char* b3 = b2 + kstep;
;             if (last && has_next) S.a_ready(nxt);
;             PG8_LDB(B0, 0, 0); PG8_LDB(B1, 0, 1); PG8_SCHED; PG8_LDA(At, 0, 0); PG8_STAGE(PG8_SA(1, 1), a1 + hstepA, voffA);
;             PG8_WAIT_V(8); PG8_WAIT_L(0); PG8_BAR; PG8_MMA(0, 0, At, B0); PG8_MMA(0, 1, At, B1); PG8_BAR; PG8_SCHED;
;             PG8_LDA(At, 0, 1); PG8_STAGE(PG8_SB(0, 0), b2, voffB); PG8_STAGE(PG8_SB(0, 1), b2 + hstepB, voffB); PG8_STAGE(PG8_SA(0, 0), a2, voffA);
;             PG8_WAIT_V(8); PG8_WAIT_L(0); PG8_BAR; PG8_MMA(1, 0, At, B0); PG8_MMA(1, 1, At, B1); PG8_BAR; PG8_SCHED;
;             PG8_LDB(B0, 1, 0); PG8_LDB(B1, 1, 1); PG8_SCHED; PG8_LDA(At, 1, 0); PG8_STAGE(PG8_SA(0, 1), a2 + hstepA, voffA);
;             PG8_WAIT_V(8); PG8_WAIT_L(0); PG8_BAR; PG8_MMA(0, 0, At, B0); PG8_MMA(0, 1, At, B1); PG8_BAR; PG8_SCHED;
;             PG8_LDA(At, 1, 1); PG8_STAGE(PG8_SB(1, 0), b3, voffB); PG8_STAGE(PG8_SB(1, 1), b3 + hstepB, voffB); PG8_STAGE(PG8_SA(1, 0), a3, voffA);
;             PG8_WAIT_V(8); PG8_WAIT_L(0); PG8_BAR; PG8_MMA(1, 0, At, B0); PG8_MMA(1, 1, At, B1); PG8_BAR; PG8_SCHED;
;         }
	s_setprio 1
	s_waitcnt lgkmcnt(0)
	v_mfma_f32_16x16x32_bf16 v[62:65], v[130:133], v[182:185], v[62:65]
	v_mfma_f32_16x16x32_bf16 v[58:61], v[138:141], v[182:185], v[58:61]
	v_mfma_f32_16x16x32_bf16 v[50:53], v[138:141], v[190:193], v[50:53]
	v_mfma_f32_16x16x32_bf16 v[54:57], v[130:133], v[190:193], v[54:57]
	v_mfma_f32_16x16x32_bf16 v[30:33], v[130:133], v[198:201], v[30:33]
	v_mfma_f32_16x16x32_bf16 v[26:29], v[138:141], v[198:201], v[26:29]
	v_mfma_f32_16x16x32_bf16 v[18:21], v[138:141], v[206:209], v[18:21]
	v_mfma_f32_16x16x32_bf16 v[22:25], v[130:133], v[206:209], v[22:25]
	v_mfma_f32_16x16x32_bf16 v[62:65], v[134:137], v[186:189], v[62:65]
	v_mfma_f32_16x16x32_bf16 v[58:61], v[154:157], v[186:189], v[58:61]
	v_mfma_f32_16x16x32_bf16 v[50:53], v[154:157], v[194:197], v[50:53]
	v_mfma_f32_16x16x32_bf16 v[54:57], v[134:137], v[194:197], v[54:57]
	v_mfma_f32_16x16x32_bf16 v[30:33], v[134:137], v[202:205], v[30:33]
	v_mfma_f32_16x16x32_bf16 v[26:29], v[154:157], v[202:205], v[26:29]
	v_mfma_f32_16x16x32_bf16 v[18:21], v[154:157], v[210:213], v[18:21]
	v_mfma_f32_16x16x32_bf16 v[22:25], v[134:137], v[210:213], v[22:25]
	s_setprio 0
	s_setprio 1
	v_mfma_f32_16x16x32_bf16 v[46:49], v[160:163], v[182:185], v[46:49]
	v_mfma_f32_16x16x32_bf16 v[42:45], v[174:177], v[182:185], v[42:45]
	v_mfma_f32_16x16x32_bf16 v[34:37], v[174:177], v[190:193], v[34:37]
	v_mfma_f32_16x16x32_bf16 v[38:41], v[160:163], v[190:193], v[38:41]
	v_mfma_f32_16x16x32_bf16 v[14:17], v[160:163], v[198:201], v[14:17]
	v_mfma_f32_16x16x32_bf16 v[10:13], v[174:177], v[198:201], v[10:13]
	v_mfma_f32_16x16x32_bf16 v[2:5], v[174:177], v[206:209], v[2:5]
	v_mfma_f32_16x16x32_bf16 v[6:9], v[160:163], v[206:209], v[6:9]
	v_mfma_f32_16x16x32_bf16 v[46:49], v[164:167], v[186:189], v[46:49]
	v_mfma_f32_16x16x32_bf16 v[42:45], v[178:181], v[186:189], v[42:45]
	v_mfma_f32_16x16x32_bf16 v[34:37], v[178:181], v[194:197], v[34:37]
	v_mfma_f32_16x16x32_bf16 v[38:41], v[164:167], v[194:197], v[38:41]
	s_setprio 0
	v_mfma_f32_16x16x32_bf16 v[14:17], v[164:167], v[202:205], v[14:17]
	v_mfma_f32_16x16x32_bf16 v[10:13], v[178:181], v[202:205], v[10:13]
	v_mfma_f32_16x16x32_bf16 v[2:5], v[178:181], v[210:213], v[2:5]
	v_mfma_f32_16x16x32_bf16 v[6:9], v[164:167], v[210:213], v[6:9]
	s_barrier
	s_add_i32 s88, 0, 0x18000
	s_add_i32 s89, 0, 0x1c000
	v_add_u32_e32 v154, s88, v169
	v_add_u32_e32 v158, s89, v169
	ds_read_b128 v[130:133], v154
	ds_read_b128 v[134:137], v154 offset:1024
	ds_read_b128 v[138:141], v154 offset:2048
	ds_read_b128 v[154:157], v154 offset:3072
	ds_read_b128 v[160:163], v158
	ds_read_b128 v[164:167], v158 offset:1024
	ds_read_b128 v[174:177], v158 offset:2048
	ds_read_b128 v[178:181], v158 offset:3072
	s_add_u32 s30, s30, 0x80000
	s_addc_u32 s31, s31, 0
	s_mov_b32 m0, s45
	v_lshl_add_u64 v[226:227], s[30:31], 0, v[146:147]
	ds_read_b128 v[182:185], v172 offset:32768
	ds_read_b128 v[186:189], v172 offset:33792
	ds_read_b128 v[190:193], v172 offset:34816
	ds_read_b128 v[194:197], v172 offset:35840
	ds_read_b128 v[198:201], v172 offset:36864
	ds_read_b128 v[202:205], v172 offset:37888
	ds_read_b128 v[206:209], v172 offset:38912
	ds_read_b128 v[210:213], v172 offset:39936
	global_load_lds_dwordx4 v[226:227], off
	v_lshl_add_u64 v[226:227], s[30:31], 0, v[144:145]
	s_mov_b32 m0, s51
	s_nop 0
	global_load_lds_dwordx4 v[226:227], off
	s_waitcnt vmcnt(8)
	s_waitcnt lgkmcnt(0)
	s_barrier
	s_setprio 1
	s_waitcnt lgkmcnt(0)
	v_mfma_f32_16x16x32_bf16 v[126:129], v[130:133], v[182:185], v[126:129]
	v_mfma_f32_16x16x32_bf16 v[122:125], v[138:141], v[182:185], v[122:125]
	v_mfma_f32_16x16x32_bf16 v[114:117], v[138:141], v[190:193], v[114:117]
	v_mfma_f32_16x16x32_bf16 v[118:121], v[130:133], v[190:193], v[118:121]
	v_mfma_f32_16x16x32_bf16 v[94:97], v[130:133], v[198:201], v[94:97]
	v_mfma_f32_16x16x32_bf16 v[90:93], v[138:141], v[198:201], v[90:93]
	v_mfma_f32_16x16x32_bf16 v[82:85], v[138:141], v[206:209], v[82:85]
	v_mfma_f32_16x16x32_bf16 v[86:89], v[130:133], v[206:209], v[86:89]
	v_mfma_f32_16x16x32_bf16 v[126:129], v[134:137], v[186:189], v[126:129]
	v_mfma_f32_16x16x32_bf16 v[122:125], v[154:157], v[186:189], v[122:125]
	v_mfma_f32_16x16x32_bf16 v[114:117], v[154:157], v[194:197], v[114:117]
	v_mfma_f32_16x16x32_bf16 v[118:121], v[134:137], v[194:197], v[118:121]
	v_mfma_f32_16x16x32_bf16 v[94:97], v[134:137], v[202:205], v[94:97]
	v_mfma_f32_16x16x32_bf16 v[90:93], v[154:157], v[202:205], v[90:93]
	v_mfma_f32_16x16x32_bf16 v[82:85], v[154:157], v[210:213], v[82:85]
	v_mfma_f32_16x16x32_bf16 v[86:89], v[134:137], v[210:213], v[86:89]
	s_setprio 0
	s_setprio 1
	v_mfma_f32_16x16x32_bf16 v[110:113], v[160:163], v[182:185], v[110:113]
	v_mfma_f32_16x16x32_bf16 v[106:109], v[174:177], v[182:185], v[106:109]
	v_mfma_f32_16x16x32_bf16 v[98:101], v[174:177], v[190:193], v[98:101]
	v_mfma_f32_16x16x32_bf16 v[102:105], v[160:163], v[190:193], v[102:105]
	v_mfma_f32_16x16x32_bf16 v[78:81], v[160:163], v[198:201], v[78:81]
	v_mfma_f32_16x16x32_bf16 v[74:77], v[174:177], v[198:201], v[74:77]
	v_mfma_f32_16x16x32_bf16 v[66:69], v[174:177], v[206:209], v[66:69]
	v_mfma_f32_16x16x32_bf16 v[70:73], v[160:163], v[206:209], v[70:73]
	v_mfma_f32_16x16x32_bf16 v[110:113], v[164:167], v[186:189], v[110:113]
	v_mfma_f32_16x16x32_bf16 v[106:109], v[178:181], v[186:189], v[106:109]
	v_mfma_f32_16x16x32_bf16 v[98:101], v[178:181], v[194:197], v[98:101]
	v_mfma_f32_16x16x32_bf16 v[102:105], v[164:167], v[194:197], v[102:105]
	s_setprio 0
	v_mfma_f32_16x16x32_bf16 v[78:81], v[164:167], v[202:205], v[78:81]
	v_mfma_f32_16x16x32_bf16 v[74:77], v[178:181], v[202:205], v[74:77]
	v_mfma_f32_16x16x32_bf16 v[66:69], v[178:181], v[210:213], v[66:69]
	v_mfma_f32_16x16x32_bf16 v[70:73], v[164:167], v[210:213], v[70:73]
	s_barrier
; #define PG8_STAGE(bufoff, gbase, voff) do { _Pragma("unroll") for (int _i = 0; _i < 2; ++_i) \
;         __builtin_amdgcn_global_load_lds((const unsigned*)((const char*)(gbase) + (voff)[_i]), (PG8_LAS unsigned*)(lds + (bufoff) + ldsw + _i * 8192), 16, 0, 0); } while (0)
; #define PG8_WAIT_V(n) asm volatile("s_waitcnt vmcnt(" #n ")" ::: "memory")
; #define PG8_WAIT_L(n) asm volatile("s_waitcnt lgkmcnt(" #n ")" ::: "memory")
; #define PG8_BAR __builtin_amdgcn_s_barrier()
; #define PG8_SCHED __builtin_amdgcn_sched_barrier(0)
; template <class Epi, class Sched, bool ALIGN_EPI, bool F8 = false>
; __device__ __forceinline__ void gemm_phase(PG8_LAS unsigned char* lds, const Gemm g, const Sched& S, const Epi& E, int tid) {
;     ...
;         for (int t = 0; t < nt; t += 2) {
;             const bool last = (t == nt - 2);
;             const char* a1 = cA + (size_t)(t + 1) * kstep;
;             const char* a2 = last ? nA : cA + (size_t)(t + 2) * kstep; const char* b2 = last ? nB : cB + (size_t)(t + 2) * kstep;
;             const char* a3 = a2 + kstep; const char* b3 = b2 + kstep;
;             if (last && has_next) S.a_ready(nxt);
;             PG8_LDB(B0, 0, 0); PG8_LDB(B1, 0, 1); PG8_SCHED; PG8_LDA(At, 0, 0); PG8_STAGE(PG8_SA(1, 1), a1 + hstepA, voffA);
;             PG8_WAIT_V(8); PG8_WAIT_L(0); PG8_BAR; PG8_MMA(0, 0, At, B0); PG8_MMA(0, 1, At, B1); PG8_BAR; PG8_SCHED;
;             PG8_LDA(At, 0, 1); PG8_STAGE(PG8_SB(0, 0), b2, voffB); PG8_STAGE(PG8_SB(0, 1), b2 + hstepB, voffB); PG8_STAGE(PG8_SA(0, 0), a2, voffA);
;             PG8_WAIT_V(8); PG8_WAIT_L(0); PG8_BAR; PG8_MMA(1, 0, At, B0); PG8_MMA(1, 1, At, B1); PG8_BAR; PG8_SCHED;
;             PG8_LDB(B0, 1, 0); PG8_LDB(B1, 1, 1); PG8_SCHED; PG8_LDA(At, 1, 0); PG8_STAGE(PG8_SA(0, 1), a2 + hstepA, voffA);
;             PG8_WAIT_V(8); PG8_WAIT_L(0); PG8_BAR; PG8_MMA(0, 0, At, B0); PG8_MMA(0, 1, At, B1); PG8_BAR; PG8_SCHED;
;             PG8_LDA(At, 1, 1); PG8_STAGE(PG8_SB(1, 0), b3, voffB); PG8_STAGE(PG8_SB(1, 1), b3 + hstepB, voffB); PG8_STAGE(PG8_SA(1, 0), a3, voffA);
;             PG8_WAIT_V(8); PG8_WAIT_L(0); PG8_BAR; PG8_MMA(1, 0, At, B0); PG8_MMA(1, 1, At, B1); PG8_BAR; PG8_SCHED;
;         }
;         if constexpr (ALIGN_EPI) { if (wr == 0) PG8_BAR; }
	s_add_i32 s30, s88, s38
	v_lshl_add_u64 v[214:215], v[214:215], 0, s[60:61]
	s_mov_b32 m0, s30
	ds_read_b128 v[182:185], v172 offset:49152
	ds_read_b128 v[186:189], v172 offset:50176
	ds_read_b128 v[190:193], v172 offset:51200
	ds_read_b128 v[194:197], v172 offset:52224
	ds_read_b128 v[198:201], v172 offset:53248
	ds_read_b128 v[202:205], v172 offset:54272
	ds_read_b128 v[206:209], v172 offset:55296
	ds_read_b128 v[210:213], v172 offset:56320
	global_load_lds_dwordx4 v[214:215], off
	s_add_i32 m0, s30, 0x2000
	s_add_u32 s28, s28, 0x84080
	v_lshl_add_u64 v[214:215], v[216:217], 0, s[60:61]
	s_addc_u32 s29, s29, 0
	s_add_i32 s30, s89, s38
	global_load_lds_dwordx4 v[214:215], off
	v_lshl_add_u64 v[214:215], s[28:29], 0, v[0:1]
	s_mov_b32 m0, s30
	s_nop 0
	global_load_lds_dwordx4 v[214:215], off
	v_lshl_add_u64 v[214:215], s[28:29], 0, v[142:143]
	s_add_i32 m0, s30, 0x2000
	s_nop 0
	global_load_lds_dwordx4 v[214:215], off
	v_lshl_add_u64 v[214:215], v[218:219], 0, s[60:61]
	s_mov_b32 m0, s68
	s_nop 0
	global_load_lds_dwordx4 v[214:215], off
	v_lshl_add_u64 v[214:215], v[220:221], 0, s[60:61]
	s_mov_b32 m0, s69
	s_nop 0
	global_load_lds_dwordx4 v[214:215], off
	s_waitcnt vmcnt(8)
	s_waitcnt lgkmcnt(0)
	s_barrier
	s_setprio 1
	s_waitcnt lgkmcnt(0)
	v_mfma_f32_16x16x32_bf16 v[62:65], v[130:133], v[182:185], v[62:65]
	v_mfma_f32_16x16x32_bf16 v[58:61], v[138:141], v[182:185], v[58:61]
	v_mfma_f32_16x16x32_bf16 v[50:53], v[138:141], v[190:193], v[50:53]
	v_mfma_f32_16x16x32_bf16 v[54:57], v[130:133], v[190:193], v[54:57]
	v_mfma_f32_16x16x32_bf16 v[30:33], v[130:133], v[198:201], v[30:33]
	v_mfma_f32_16x16x32_bf16 v[26:29], v[138:141], v[198:201], v[26:29]
	v_mfma_f32_16x16x32_bf16 v[18:21], v[138:141], v[206:209], v[18:21]
	v_mfma_f32_16x16x32_bf16 v[22:25], v[130:133], v[206:209], v[22:25]
	v_mfma_f32_16x16x32_bf16 v[62:65], v[134:137], v[186:189], v[62:65]
	v_mfma_f32_16x16x32_bf16 v[58:61], v[154:157], v[186:189], v[58:61]
	v_mfma_f32_16x16x32_bf16 v[50:53], v[154:157], v[194:197], v[50:53]
	v_mfma_f32_16x16x32_bf16 v[54:57], v[134:137], v[194:197], v[54:57]
	v_mfma_f32_16x16x32_bf16 v[30:33], v[134:137], v[202:205], v[30:33]
	v_mfma_f32_16x16x32_bf16 v[26:29], v[154:157], v[202:205], v[26:29]
	v_mfma_f32_16x16x32_bf16 v[18:21], v[154:157], v[210:213], v[18:21]
	v_mfma_f32_16x16x32_bf16 v[22:25], v[134:137], v[210:213], v[22:25]
	s_setprio 0
	s_setprio 1
	v_mfma_f32_16x16x32_bf16 v[46:49], v[160:163], v[182:185], v[46:49]
	v_mfma_f32_16x16x32_bf16 v[42:45], v[174:177], v[182:185], v[42:45]
	v_mfma_f32_16x16x32_bf16 v[34:37], v[174:177], v[190:193], v[34:37]
	v_mfma_f32_16x16x32_bf16 v[38:41], v[160:163], v[190:193], v[38:41]
	v_mfma_f32_16x16x32_bf16 v[14:17], v[160:163], v[198:201], v[14:17]
	v_mfma_f32_16x16x32_bf16 v[10:13], v[174:177], v[198:201], v[10:13]
	v_mfma_f32_16x16x32_bf16 v[2:5], v[174:177], v[206:209], v[2:5]
	v_mfma_f32_16x16x32_bf16 v[6:9], v[160:163], v[206:209], v[6:9]
	v_mfma_f32_16x16x32_bf16 v[46:49], v[164:167], v[186:189], v[46:49]
	v_mfma_f32_16x16x32_bf16 v[42:45], v[178:181], v[186:189], v[42:45]
	v_mfma_f32_16x16x32_bf16 v[34:37], v[178:181], v[194:197], v[34:37]
	v_mfma_f32_16x16x32_bf16 v[38:41], v[164:167], v[194:197], v[38:41]
	s_setprio 0
	v_mfma_f32_16x16x32_bf16 v[14:17], v[164:167], v[202:205], v[14:17]
	v_mfma_f32_16x16x32_bf16 v[10:13], v[178:181], v[202:205], v[10:13]
	v_mfma_f32_16x16x32_bf16 v[2:5], v[178:181], v[210:213], v[2:5]
	v_mfma_f32_16x16x32_bf16 v[6:9], v[164:167], v[210:213], v[6:9]
	s_barrier
	s_add_i32 s7, s7, 2
	s_add_u32 s12, s12, 0x100
	s_addc_u32 s13, s13, 0
	s_add_u32 s50, s50, 0x100
	s_addc_u32 s6, s6, 0
	s_cmp_gt_u32 s7, 29
	s_cbranch_scc0 .LBB0_1619
	s_and_b64 vcc, exec, s[20:21]
	s_cbranch_vccz .LBB0_1622
	s_barrier

; #define PG8_STAGE(bufoff, gbase, voff) do { _Pragma("unroll") for (int _i = 0; _i < 2; ++_i) \
;         __builtin_amdgcn_global_load_lds((const unsigned*)((const char*)(gbase) + (voff)[_i]), (PG8_LAS unsigned*)(lds + (bufoff) + ldsw + _i * 8192), 16, 0, 0); } while (0)
; #define PG8_WAIT_V(n) asm volatile("s_waitcnt vmcnt(" #n ")" ::: "memory")
; #define PG8_WAIT_L(n) asm volatile("s_waitcnt lgkmcnt(" #n ")" ::: "memory")
; #define PG8_BAR __builtin_amdgcn_s_barrier()
; #define PG8_SCHED __builtin_amdgcn_sched_barrier(0)
; template <class Epi, class Sched, bool ALIGN_EPI, bool F8 = false>
; __device__ __forceinline__ void gemm_phase(PG8_LAS unsigned char* lds, const Gemm g, const Sched& S, const Epi& E, int tid) {
;     ...
;         for (int t = 0; t < nt; t += 2) {
;             const bool last = (t == nt - 2);
;             const char* a1 = cA + (size_t)(t + 1) * kstep;
;             const char* a2 = last ? nA : cA + (size_t)(t + 2) * kstep; const char* b2 = last ? nB : cB + (size_t)(t + 2) * kstep;
;             const char* a3 = a2 + kstep; const char* b3 = b2 + kstep;
;             if (last && has_next) S.a_ready(nxt);
;             PG8_LDB(B0, 0, 0); PG8_LDB(B1, 0, 1); PG8_SCHED; PG8_LDA(At, 0, 0); PG8_STAGE(PG8_SA(1, 1), a1 + hstepA, voffA);
;             PG8_WAIT_V(8); PG8_WAIT_L(0); PG8_BAR; PG8_MMA(0, 0, At, B0); PG8_MMA(0, 1, At, B1); PG8_BAR; PG8_SCHED;
;             PG8_LDA(At, 0, 1); PG8_STAGE(PG8_SB(0, 0), b2, voffB); PG8_STAGE(PG8_SB(0, 1), b2 + hstepB, voffB); PG8_STAGE(PG8_SA(0, 0), a2, voffA);
;             PG8_WAIT_V(8); PG8_WAIT_L(0); PG8_BAR; PG8_MMA(1, 0, At, B0); PG8_MMA(1, 1, At, B1); PG8_BAR; PG8_SCHED;
;             PG8_LDB(B0, 1, 0); PG8_LDB(B1, 1, 1); PG8_SCHED; PG8_LDA(At, 1, 0); PG8_STAGE(PG8_SA(0, 1), a2 + hstepA, voffA);
;             PG8_WAIT_V(8); PG8_WAIT_L(0); PG8_BAR; PG8_MMA(0, 0, At, B0); PG8_MMA(0, 1, At, B1); PG8_BAR; PG8_SCHED;
;             PG8_LDA(At, 1, 1); PG8_STAGE(PG8_SB(1, 0), b3, voffB); PG8_STAGE(PG8_SB(1, 1), b3 + hstepB, voffB); PG8_STAGE(PG8_SA(1, 0), a3, voffA);
;             PG8_WAIT_V(8); PG8_WAIT_L(0); PG8_BAR; PG8_MMA(1, 0, At, B0); PG8_MMA(1, 1, At, B1); PG8_BAR; PG8_SCHED;
;         }
;         if constexpr (ALIGN_EPI) { if (wr == 0) PG8_BAR; }
.LBB0_1639:
	s_add_u32 s22, s10, 0xfff80080
	s_addc_u32 s23, s11, -1
	s_add_i32 s82, 0, 0x10000
	s_cmp_eq_u32 s7, 28
	s_cselect_b32 s25, s15, s23
	s_cselect_b32 s24, s69, s22
	s_cselect_b32 s23, s19, s6
	s_cselect_b32 s22, s18, s50
	s_add_i32 s84, 0, 0x14000
	v_add_u32_e32 v160, s82, v147
	v_add_u32_e32 v176, s84, v147
	ds_read_b128 v[142:145], v160
	ds_read_b128 v[152:155], v160 offset:1024
	ds_read_b128 v[156:159], v160 offset:2048
	ds_read_b128 v[160:163], v160 offset:3072
	ds_read_b128 v[164:167], v176
	ds_read_b128 v[168:171], v176 offset:1024
	ds_read_b128 v[172:175], v176 offset:2048
	ds_read_b128 v[176:179], v176 offset:3072
	v_lshl_add_u64 v[212:213], s[10:11], 0, v[138:139]
	s_add_i32 m0, s27, 0xc000
	ds_read_b128 v[180:183], v151
	ds_read_b128 v[184:187], v151 offset:1024
	ds_read_b128 v[188:191], v151 offset:2048
	ds_read_b128 v[192:195], v151 offset:3072
	ds_read_b128 v[196:199], v151 offset:4096
	ds_read_b128 v[200:203], v151 offset:5120
	ds_read_b128 v[204:207], v151 offset:6144
	ds_read_b128 v[208:211], v151 offset:7168
	global_load_lds_dwordx4 v[212:213], off
	v_lshl_add_u64 v[212:213], s[10:11], 0, v[140:141]
	s_add_i32 m0, s27, 0xe000
	s_nop 0
	global_load_lds_dwordx4 v[212:213], off
	s_waitcnt vmcnt(8)
	s_waitcnt lgkmcnt(0)
	s_barrier
	s_setprio 1
	s_waitcnt lgkmcnt(0)
	v_mfma_f32_16x16x32_bf16 v[126:129], v[142:145], v[180:183], v[126:129]
	v_mfma_f32_16x16x32_bf16 v[122:125], v[156:159], v[180:183], v[122:125]
	v_mfma_f32_16x16x32_bf16 v[114:117], v[156:159], v[188:191], v[114:117]
	v_mfma_f32_16x16x32_bf16 v[118:121], v[142:145], v[188:191], v[118:121]
	v_mfma_f32_16x16x32_bf16 v[94:97], v[142:145], v[196:199], v[94:97]
	v_mfma_f32_16x16x32_bf16 v[90:93], v[156:159], v[196:199], v[90:93]
	v_mfma_f32_16x16x32_bf16 v[82:85], v[156:159], v[204:207], v[82:85]
	v_mfma_f32_16x16x32_bf16 v[86:89], v[142:145], v[204:207], v[86:89]
	v_mfma_f32_16x16x32_bf16 v[126:129], v[152:155], v[184:187], v[126:129]
	v_mfma_f32_16x16x32_bf16 v[122:125], v[160:163], v[184:187], v[122:125]
	v_mfma_f32_16x16x32_bf16 v[114:117], v[160:163], v[192:195], v[114:117]
	v_mfma_f32_16x16x32_bf16 v[118:121], v[152:155], v[192:195], v[118:121]
	v_mfma_f32_16x16x32_bf16 v[94:97], v[152:155], v[200:203], v[94:97]
	v_mfma_f32_16x16x32_bf16 v[90:93], v[160:163], v[200:203], v[90:93]
	v_mfma_f32_16x16x32_bf16 v[82:85], v[160:163], v[208:211], v[82:85]
	v_mfma_f32_16x16x32_bf16 v[86:89], v[152:155], v[208:211], v[86:89]
	s_setprio 0
	s_setprio 1
	v_mfma_f32_16x16x32_bf16 v[110:113], v[164:167], v[180:183], v[110:113]
	v_mfma_f32_16x16x32_bf16 v[106:109], v[172:175], v[180:183], v[106:109]
	v_mfma_f32_16x16x32_bf16 v[98:101], v[172:175], v[188:191], v[98:101]
	v_mfma_f32_16x16x32_bf16 v[102:105], v[164:167], v[188:191], v[102:105]
	v_mfma_f32_16x16x32_bf16 v[78:81], v[164:167], v[196:199], v[78:81]
	v_mfma_f32_16x16x32_bf16 v[74:77], v[172:175], v[196:199], v[74:77]
	v_mfma_f32_16x16x32_bf16 v[66:69], v[172:175], v[204:207], v[66:69]
	v_mfma_f32_16x16x32_bf16 v[70:73], v[164:167], v[204:207], v[70:73]
	v_mfma_f32_16x16x32_bf16 v[110:113], v[168:171], v[184:187], v[110:113]
	v_mfma_f32_16x16x32_bf16 v[106:109], v[176:179], v[184:187], v[106:109]
	v_mfma_f32_16x16x32_bf16 v[98:101], v[176:179], v[192:195], v[98:101]
	v_mfma_f32_16x16x32_bf16 v[102:105], v[168:171], v[192:195], v[102:105]
	s_setprio 0
	v_mfma_f32_16x16x32_bf16 v[78:81], v[168:171], v[200:203], v[78:81]
	v_mfma_f32_16x16x32_bf16 v[74:77], v[176:179], v[200:203], v[74:77]
	v_mfma_f32_16x16x32_bf16 v[66:69], v[176:179], v[208:211], v[66:69]
	v_mfma_f32_16x16x32_bf16 v[70:73], v[168:171], v[208:211], v[70:73]
	s_barrier
	s_add_i32 s82, s82, s26
	v_lshl_add_u64 v[212:213], s[22:23], 0, v[0:1]
	s_mov_b32 m0, s82
	ds_read_b128 v[180:183], v151 offset:16384
	ds_read_b128 v[184:187], v151 offset:17408
	ds_read_b128 v[188:191], v151 offset:18432
	ds_read_b128 v[192:195], v151 offset:19456
	ds_read_b128 v[196:199], v151 offset:20480
	ds_read_b128 v[200:203], v151 offset:21504
	ds_read_b128 v[204:207], v151 offset:22528
	ds_read_b128 v[208:211], v151 offset:23552
	global_load_lds_dwordx4 v[212:213], off
	s_add_i32 m0, s82, 0x2000
	s_add_u32 s82, s22, 0x84000
	v_lshl_add_u64 v[214:215], s[22:23], 0, v[130:131]
	s_addc_u32 s83, s23, 0
	s_add_i32 s84, s84, s26
	global_load_lds_dwordx4 v[214:215], off
	v_lshl_add_u64 v[216:217], s[82:83], 0, v[0:1]
	s_mov_b32 m0, s84
	v_lshl_add_u64 v[218:219], s[24:25], 0, v[132:133]
	global_load_lds_dwordx4 v[216:217], off
	v_lshl_add_u64 v[216:217], s[82:83], 0, v[130:131]
	s_add_i32 m0, s84, 0x2000
	s_nop 0
	global_load_lds_dwordx4 v[216:217], off
	v_lshl_add_u64 v[216:217], s[24:25], 0, v[134:135]
	s_mov_b32 m0, s27
	s_nop 0
	global_load_lds_dwordx4 v[216:217], off
	s_mov_b32 m0, s28
	s_nop 0
	global_load_lds_dwordx4 v[218:219], off
	s_waitcnt vmcnt(8)
	s_waitcnt lgkmcnt(0)
	s_barrier
; #define PG8_STAGE(bufoff, gbase, voff) do { _Pragma("unroll") for (int _i = 0; _i < 2; ++_i) \
;         __builtin_amdgcn_global_load_lds((const unsigned*)((const char*)(gbase) + (voff)[_i]), (PG8_LAS unsigned*)(lds + (bufoff) + ldsw + _i * 8192), 16, 0, 0); } while (0)
; #define PG8_WAIT_V(n) asm volatile("s_waitcnt vmcnt(" #n ")" ::: "memory")
; #define PG8_WAIT_L(n) asm volatile("s_waitcnt lgkmcnt(" #n ")" ::: "memory")
; #define PG8_BAR __builtin_amdgcn_s_barrier()
; #define PG8_SCHED __builtin_amdgcn_sched_barrier(0)
; template <class Epi, class Sched, bool ALIGN_EPI, bool F8 = false>
; __device__ __forceinline__ void gemm_phase(PG8_LAS unsigned char* lds, const Gemm g, const Sched& S, const Epi& E, int tid) {
;     ...
;         for (int t = 0; t < nt; t += 2) {
;             const bool last = (t == nt - 2);
;             const char* a1 = cA + (size_t)(t + 1) * kstep;
;             const char* a2 = last ? nA : cA + (size_t)(t + 2) * kstep; const char* b2 = last ? nB : cB + (size_t)(t + 2) * kstep;
;             const char* a3 = a2 + kstep; const char* b3 = b2 + kstep;
;             if (last && has_next) S.a_ready(nxt);
;             PG8_LDB(B0, 0, 0); PG8_LDB(B1, 0, 1); PG8_SCHED; PG8_LDA(At, 0, 0); PG8_STAGE(PG8_SA(1, 1), a1 + hstepA, voffA);
;             PG8_WAIT_V(8); PG8_WAIT_L(0); PG8_BAR; PG8_MMA(0, 0, At, B0); PG8_MMA(0, 1, At, B1); PG8_BAR; PG8_SCHED;
;             PG8_LDA(At, 0, 1); PG8_STAGE(PG8_SB(0, 0), b2, voffB); PG8_STAGE(PG8_SB(0, 1), b2 + hstepB, voffB); PG8_STAGE(PG8_SA(0, 0), a2, voffA);
;             PG8_WAIT_V(8); PG8_WAIT_L(0); PG8_BAR; PG8_MMA(1, 0, At, B0); PG8_MMA(1, 1, At, B1); PG8_BAR; PG8_SCHED;
;             PG8_LDB(B0, 1, 0); PG8_LDB(B1, 1, 1); PG8_SCHED; PG8_LDA(At, 1, 0); PG8_STAGE(PG8_SA(0, 1), a2 + hstepA, voffA);
;             PG8_WAIT_V(8); PG8_WAIT_L(0); PG8_BAR; PG8_MMA(0, 0, At, B0); PG8_MMA(0, 1, At, B1); PG8_BAR; PG8_SCHED;
;             PG8_LDA(At, 1, 1); PG8_STAGE(PG8_SB(1, 0), b3, voffB); PG8_STAGE(PG8_SB(1, 1), b3 + hstepB, voffB); PG8_STAGE(PG8_SA(1, 0), a3, voffA);
;             PG8_WAIT_V(8); PG8_WAIT_L(0); PG8_BAR; PG8_MMA(1, 0, At, B0); PG8_MMA(1, 1, At, B1); PG8_BAR; PG8_SCHED;
;         }
	s_setprio 1
	s_waitcnt lgkmcnt(0)
	v_mfma_f32_16x16x32_bf16 v[62:65], v[142:145], v[180:183], v[62:65]
	v_mfma_f32_16x16x32_bf16 v[58:61], v[156:159], v[180:183], v[58:61]
	v_mfma_f32_16x16x32_bf16 v[50:53], v[156:159], v[188:191], v[50:53]
	v_mfma_f32_16x16x32_bf16 v[54:57], v[142:145], v[188:191], v[54:57]
	v_mfma_f32_16x16x32_bf16 v[30:33], v[142:145], v[196:199], v[30:33]
	v_mfma_f32_16x16x32_bf16 v[26:29], v[156:159], v[196:199], v[26:29]
	v_mfma_f32_16x16x32_bf16 v[18:21], v[156:159], v[204:207], v[18:21]
	v_mfma_f32_16x16x32_bf16 v[22:25], v[142:145], v[204:207], v[22:25]
	v_mfma_f32_16x16x32_bf16 v[62:65], v[152:155], v[184:187], v[62:65]
	v_mfma_f32_16x16x32_bf16 v[58:61], v[160:163], v[184:187], v[58:61]
	v_mfma_f32_16x16x32_bf16 v[50:53], v[160:163], v[192:195], v[50:53]
	v_mfma_f32_16x16x32_bf16 v[54:57], v[152:155], v[192:195], v[54:57]
	v_mfma_f32_16x16x32_bf16 v[30:33], v[152:155], v[200:203], v[30:33]
	v_mfma_f32_16x16x32_bf16 v[26:29], v[160:163], v[200:203], v[26:29]
	v_mfma_f32_16x16x32_bf16 v[18:21], v[160:163], v[208:211], v[18:21]
	v_mfma_f32_16x16x32_bf16 v[22:25], v[152:155], v[208:211], v[22:25]
	s_setprio 0
	s_setprio 1
	v_mfma_f32_16x16x32_bf16 v[46:49], v[164:167], v[180:183], v[46:49]
	v_mfma_f32_16x16x32_bf16 v[42:45], v[172:175], v[180:183], v[42:45]
	v_mfma_f32_16x16x32_bf16 v[34:37], v[172:175], v[188:191], v[34:37]
	v_mfma_f32_16x16x32_bf16 v[38:41], v[164:167], v[188:191], v[38:41]
	v_mfma_f32_16x16x32_bf16 v[14:17], v[164:167], v[196:199], v[14:17]
	v_mfma_f32_16x16x32_bf16 v[10:13], v[172:175], v[196:199], v[10:13]
	v_mfma_f32_16x16x32_bf16 v[2:5], v[172:175], v[204:207], v[2:5]
	v_mfma_f32_16x16x32_bf16 v[6:9], v[164:167], v[204:207], v[6:9]
	v_mfma_f32_16x16x32_bf16 v[46:49], v[168:171], v[184:187], v[46:49]
	v_mfma_f32_16x16x32_bf16 v[42:45], v[176:179], v[184:187], v[42:45]
	v_mfma_f32_16x16x32_bf16 v[34:37], v[176:179], v[192:195], v[34:37]
	v_mfma_f32_16x16x32_bf16 v[38:41], v[168:171], v[192:195], v[38:41]
	s_setprio 0
	v_mfma_f32_16x16x32_bf16 v[14:17], v[168:171], v[200:203], v[14:17]
	v_mfma_f32_16x16x32_bf16 v[10:13], v[176:179], v[200:203], v[10:13]
	v_mfma_f32_16x16x32_bf16 v[2:5], v[176:179], v[208:211], v[2:5]
	v_mfma_f32_16x16x32_bf16 v[6:9], v[168:171], v[208:211], v[6:9]
	s_barrier
	s_add_i32 s82, 0, 0x18000
	s_add_i32 s83, 0, 0x1c000
	v_add_u32_e32 v160, s82, v147
	v_add_u32_e32 v176, s83, v147
	ds_read_b128 v[142:145], v160
	ds_read_b128 v[152:155], v160 offset:1024
	ds_read_b128 v[156:159], v160 offset:2048
	ds_read_b128 v[160:163], v160 offset:3072
	ds_read_b128 v[164:167], v176
	ds_read_b128 v[168:171], v176 offset:1024
	ds_read_b128 v[172:175], v176 offset:2048
	ds_read_b128 v[176:179], v176 offset:3072
	s_add_u32 s24, s24, 0x80000
	s_addc_u32 s25, s25, 0
	s_mov_b32 m0, s29
	v_lshl_add_u64 v[220:221], s[24:25], 0, v[134:135]
	ds_read_b128 v[180:183], v151 offset:32768
	ds_read_b128 v[184:187], v151 offset:33792
	ds_read_b128 v[188:191], v151 offset:34816
	ds_read_b128 v[192:195], v151 offset:35840
	ds_read_b128 v[196:199], v151 offset:36864
	ds_read_b128 v[200:203], v151 offset:37888
	ds_read_b128 v[204:207], v151 offset:38912
	ds_read_b128 v[208:211], v151 offset:39936
	global_load_lds_dwordx4 v[220:221], off
	v_lshl_add_u64 v[220:221], s[24:25], 0, v[132:133]
	s_mov_b32 m0, s30
	s_nop 0
	global_load_lds_dwordx4 v[220:221], off
	s_waitcnt vmcnt(8)
	s_waitcnt lgkmcnt(0)
	s_barrier
	s_setprio 1
	s_waitcnt lgkmcnt(0)
	v_mfma_f32_16x16x32_bf16 v[126:129], v[142:145], v[180:183], v[126:129]
	v_mfma_f32_16x16x32_bf16 v[122:125], v[156:159], v[180:183], v[122:125]
	v_mfma_f32_16x16x32_bf16 v[114:117], v[156:159], v[188:191], v[114:117]
	v_mfma_f32_16x16x32_bf16 v[118:121], v[142:145], v[188:191], v[118:121]
	v_mfma_f32_16x16x32_bf16 v[94:97], v[142:145], v[196:199], v[94:97]
	v_mfma_f32_16x16x32_bf16 v[90:93], v[156:159], v[196:199], v[90:93]
	v_mfma_f32_16x16x32_bf16 v[82:85], v[156:159], v[204:207], v[82:85]
	v_mfma_f32_16x16x32_bf16 v[86:89], v[142:145], v[204:207], v[86:89]
	v_mfma_f32_16x16x32_bf16 v[126:129], v[152:155], v[184:187], v[126:129]
	v_mfma_f32_16x16x32_bf16 v[122:125], v[160:163], v[184:187], v[122:125]
	v_mfma_f32_16x16x32_bf16 v[114:117], v[160:163], v[192:195], v[114:117]
	v_mfma_f32_16x16x32_bf16 v[118:121], v[152:155], v[192:195], v[118:121]
	v_mfma_f32_16x16x32_bf16 v[94:97], v[152:155], v[200:203], v[94:97]
	v_mfma_f32_16x16x32_bf16 v[90:93], v[160:163], v[200:203], v[90:93]
	v_mfma_f32_16x16x32_bf16 v[82:85], v[160:163], v[208:211], v[82:85]
	v_mfma_f32_16x16x32_bf16 v[86:89], v[152:155], v[208:211], v[86:89]
	s_setprio 0
	s_setprio 1
	v_mfma_f32_16x16x32_bf16 v[110:113], v[164:167], v[180:183], v[110:113]
	v_mfma_f32_16x16x32_bf16 v[106:109], v[172:175], v[180:183], v[106:109]
	v_mfma_f32_16x16x32_bf16 v[98:101], v[172:175], v[188:191], v[98:101]
	v_mfma_f32_16x16x32_bf16 v[102:105], v[164:167], v[188:191], v[102:105]
	v_mfma_f32_16x16x32_bf16 v[78:81], v[164:167], v[196:199], v[78:81]
	v_mfma_f32_16x16x32_bf16 v[74:77], v[172:175], v[196:199], v[74:77]
	v_mfma_f32_16x16x32_bf16 v[66:69], v[172:175], v[204:207], v[66:69]
	v_mfma_f32_16x16x32_bf16 v[70:73], v[164:167], v[204:207], v[70:73]
	v_mfma_f32_16x16x32_bf16 v[110:113], v[168:171], v[184:187], v[110:113]
	v_mfma_f32_16x16x32_bf16 v[106:109], v[176:179], v[184:187], v[106:109]
	v_mfma_f32_16x16x32_bf16 v[98:101], v[176:179], v[192:195], v[98:101]
	v_mfma_f32_16x16x32_bf16 v[102:105], v[168:171], v[192:195], v[102:105]
	s_setprio 0
	v_mfma_f32_16x16x32_bf16 v[78:81], v[168:171], v[200:203], v[78:81]
	v_mfma_f32_16x16x32_bf16 v[74:77], v[176:179], v[200:203], v[74:77]
	v_mfma_f32_16x16x32_bf16 v[66:69], v[176:179], v[208:211], v[66:69]
	v_mfma_f32_16x16x32_bf16 v[70:73], v[168:171], v[208:211], v[70:73]
	s_barrier
; #define PG8_STAGE(bufoff, gbase, voff) do { _Pragma("unroll") for (int _i = 0; _i < 2; ++_i) \
;         __builtin_amdgcn_global_load_lds((const unsigned*)((const char*)(gbase) + (voff)[_i]), (PG8_LAS unsigned*)(lds + (bufoff) + ldsw + _i * 8192), 16, 0, 0); } while (0)
; #define PG8_WAIT_V(n) asm volatile("s_waitcnt vmcnt(" #n ")" ::: "memory")
; #define PG8_WAIT_L(n) asm volatile("s_waitcnt lgkmcnt(" #n ")" ::: "memory")
; #define PG8_BAR __builtin_amdgcn_s_barrier()
; #define PG8_SCHED __builtin_amdgcn_sched_barrier(0)
; template <class Epi, class Sched, bool ALIGN_EPI, bool F8 = false>
; __device__ __forceinline__ void gemm_phase(PG8_LAS unsigned char* lds, const Gemm g, const Sched& S, const Epi& E, int tid) {
;     ...
;         for (int t = 0; t < nt; t += 2) {
;             const bool last = (t == nt - 2);
;             const char* a1 = cA + (size_t)(t + 1) * kstep;
;             const char* a2 = last ? nA : cA + (size_t)(t + 2) * kstep; const char* b2 = last ? nB : cB + (size_t)(t + 2) * kstep;
;             const char* a3 = a2 + kstep; const char* b3 = b2 + kstep;
;             if (last && has_next) S.a_ready(nxt);
;             PG8_LDB(B0, 0, 0); PG8_LDB(B1, 0, 1); PG8_SCHED; PG8_LDA(At, 0, 0); PG8_STAGE(PG8_SA(1, 1), a1 + hstepA, voffA);
;             PG8_WAIT_V(8); PG8_WAIT_L(0); PG8_BAR; PG8_MMA(0, 0, At, B0); PG8_MMA(0, 1, At, B1); PG8_BAR; PG8_SCHED;
;             PG8_LDA(At, 0, 1); PG8_STAGE(PG8_SB(0, 0), b2, voffB); PG8_STAGE(PG8_SB(0, 1), b2 + hstepB, voffB); PG8_STAGE(PG8_SA(0, 0), a2, voffA);
;             PG8_WAIT_V(8); PG8_WAIT_L(0); PG8_BAR; PG8_MMA(1, 0, At, B0); PG8_MMA(1, 1, At, B1); PG8_BAR; PG8_SCHED;
;             PG8_LDB(B0, 1, 0); PG8_LDB(B1, 1, 1); PG8_SCHED; PG8_LDA(At, 1, 0); PG8_STAGE(PG8_SA(0, 1), a2 + hstepA, voffA);
;             PG8_WAIT_V(8); PG8_WAIT_L(0); PG8_BAR; PG8_MMA(0, 0, At, B0); PG8_MMA(0, 1, At, B1); PG8_BAR; PG8_SCHED;
;             PG8_LDA(At, 1, 1); PG8_STAGE(PG8_SB(1, 0), b3, voffB); PG8_STAGE(PG8_SB(1, 1), b3 + hstepB, voffB); PG8_STAGE(PG8_SA(1, 0), a3, voffA);
;             PG8_WAIT_V(8); PG8_WAIT_L(0); PG8_BAR; PG8_MMA(1, 0, At, B0); PG8_MMA(1, 1, At, B1); PG8_BAR; PG8_SCHED;
;         }
;         if constexpr (ALIGN_EPI) { if (wr == 0) PG8_BAR; }
	s_add_i32 s24, s82, s26
	v_lshl_add_u64 v[212:213], v[212:213], 0, s[60:61]
	s_mov_b32 m0, s24
	ds_read_b128 v[180:183], v151 offset:49152
	ds_read_b128 v[184:187], v151 offset:50176
	ds_read_b128 v[188:191], v151 offset:51200
	ds_read_b128 v[192:195], v151 offset:52224
	ds_read_b128 v[196:199], v151 offset:53248
	ds_read_b128 v[200:203], v151 offset:54272
	ds_read_b128 v[204:207], v151 offset:55296
	ds_read_b128 v[208:211], v151 offset:56320
	global_load_lds_dwordx4 v[212:213], off
	s_add_i32 m0, s24, 0x2000
	s_add_u32 s22, s22, 0x84080
	v_lshl_add_u64 v[212:213], v[214:215], 0, s[60:61]
	s_addc_u32 s23, s23, 0
	s_add_i32 s24, s83, s26
	global_load_lds_dwordx4 v[212:213], off
	v_lshl_add_u64 v[212:213], s[22:23], 0, v[0:1]
	s_mov_b32 m0, s24
	s_nop 0
	global_load_lds_dwordx4 v[212:213], off
	v_lshl_add_u64 v[212:213], s[22:23], 0, v[130:131]
	s_add_i32 m0, s24, 0x2000
	s_nop 0
	global_load_lds_dwordx4 v[212:213], off
	v_lshl_add_u64 v[212:213], v[216:217], 0, s[60:61]
	s_mov_b32 m0, s31
	s_nop 0
	global_load_lds_dwordx4 v[212:213], off
	v_lshl_add_u64 v[212:213], v[218:219], 0, s[60:61]
	s_mov_b32 m0, s38
	s_nop 0
	global_load_lds_dwordx4 v[212:213], off
	s_waitcnt vmcnt(8)
	s_waitcnt lgkmcnt(0)
	s_barrier
	s_setprio 1
	s_waitcnt lgkmcnt(0)
	v_mfma_f32_16x16x32_bf16 v[62:65], v[142:145], v[180:183], v[62:65]
	v_mfma_f32_16x16x32_bf16 v[58:61], v[156:159], v[180:183], v[58:61]
	v_mfma_f32_16x16x32_bf16 v[50:53], v[156:159], v[188:191], v[50:53]
	v_mfma_f32_16x16x32_bf16 v[54:57], v[142:145], v[188:191], v[54:57]
	v_mfma_f32_16x16x32_bf16 v[30:33], v[142:145], v[196:199], v[30:33]
	v_mfma_f32_16x16x32_bf16 v[26:29], v[156:159], v[196:199], v[26:29]
	v_mfma_f32_16x16x32_bf16 v[18:21], v[156:159], v[204:207], v[18:21]
	v_mfma_f32_16x16x32_bf16 v[22:25], v[142:145], v[204:207], v[22:25]
	v_mfma_f32_16x16x32_bf16 v[62:65], v[152:155], v[184:187], v[62:65]
	v_mfma_f32_16x16x32_bf16 v[58:61], v[160:163], v[184:187], v[58:61]
	v_mfma_f32_16x16x32_bf16 v[50:53], v[160:163], v[192:195], v[50:53]
	v_mfma_f32_16x16x32_bf16 v[54:57], v[152:155], v[192:195], v[54:57]
	v_mfma_f32_16x16x32_bf16 v[30:33], v[152:155], v[200:203], v[30:33]
	v_mfma_f32_16x16x32_bf16 v[26:29], v[160:163], v[200:203], v[26:29]
	v_mfma_f32_16x16x32_bf16 v[18:21], v[160:163], v[208:211], v[18:21]
	v_mfma_f32_16x16x32_bf16 v[22:25], v[152:155], v[208:211], v[22:25]
	s_setprio 0
	s_setprio 1
	v_mfma_f32_16x16x32_bf16 v[46:49], v[164:167], v[180:183], v[46:49]
	v_mfma_f32_16x16x32_bf16 v[42:45], v[172:175], v[180:183], v[42:45]
	v_mfma_f32_16x16x32_bf16 v[34:37], v[172:175], v[188:191], v[34:37]
	v_mfma_f32_16x16x32_bf16 v[38:41], v[164:167], v[188:191], v[38:41]
	v_mfma_f32_16x16x32_bf16 v[14:17], v[164:167], v[196:199], v[14:17]
	v_mfma_f32_16x16x32_bf16 v[10:13], v[172:175], v[196:199], v[10:13]
	v_mfma_f32_16x16x32_bf16 v[2:5], v[172:175], v[204:207], v[2:5]
	v_mfma_f32_16x16x32_bf16 v[6:9], v[164:167], v[204:207], v[6:9]
	v_mfma_f32_16x16x32_bf16 v[46:49], v[168:171], v[184:187], v[46:49]
	v_mfma_f32_16x16x32_bf16 v[42:45], v[176:179], v[184:187], v[42:45]
	v_mfma_f32_16x16x32_bf16 v[34:37], v[176:179], v[192:195], v[34:37]
	v_mfma_f32_16x16x32_bf16 v[38:41], v[168:171], v[192:195], v[38:41]
	s_setprio 0
	v_mfma_f32_16x16x32_bf16 v[14:17], v[168:171], v[200:203], v[14:17]
	v_mfma_f32_16x16x32_bf16 v[10:13], v[176:179], v[200:203], v[10:13]
	v_mfma_f32_16x16x32_bf16 v[2:5], v[176:179], v[208:211], v[2:5]
	v_mfma_f32_16x16x32_bf16 v[6:9], v[168:171], v[208:211], v[6:9]
	s_barrier
	s_add_i32 s7, s7, 2
	s_add_u32 s10, s10, 0x100
	s_addc_u32 s11, s11, 0
	s_add_u32 s50, s50, 0x100
	s_addc_u32 s6, s6, 0
	s_cmp_gt_u32 s7, 29
	s_cbranch_scc0 .LBB0_1639
	s_and_b64 vcc, exec, s[16:17]
	s_cbranch_vccz .LBB0_1642
	s_barrier

; #define PG8_STAGE(bufoff, gbase, voff) do { _Pragma("unroll") for (int _i = 0; _i < 2; ++_i) \
;         __builtin_amdgcn_global_load_lds((const unsigned*)((const char*)(gbase) + (voff)[_i]), (PG8_LAS unsigned*)(lds + (bufoff) + ldsw + _i * 8192), 16, 0, 0); } while (0)
; #define PG8_WAIT_V(n) asm volatile("s_waitcnt vmcnt(" #n ")" ::: "memory")
; #define PG8_WAIT_L(n) asm volatile("s_waitcnt lgkmcnt(" #n ")" ::: "memory")
; #define PG8_BAR __builtin_amdgcn_s_barrier()
; #define PG8_SCHED __builtin_amdgcn_sched_barrier(0)
; template <class Epi, class Sched, bool ALIGN_EPI, bool F8 = false>
; __device__ __forceinline__ void gemm_phase(PG8_LAS unsigned char* lds, const Gemm g, const Sched& S, const Epi& E, int tid) {
;     ...
;         for (int t = 0; t < nt; t += 2) {
;             const bool last = (t == nt - 2);
;             const char* a1 = cA + (size_t)(t + 1) * kstep;
;             const char* a2 = last ? nA : cA + (size_t)(t + 2) * kstep; const char* b2 = last ? nB : cB + (size_t)(t + 2) * kstep;
;             const char* a3 = a2 + kstep; const char* b3 = b2 + kstep;
;             if (last && has_next) S.a_ready(nxt);
;             PG8_LDB(B0, 0, 0); PG8_LDB(B1, 0, 1); PG8_SCHED; PG8_LDA(At, 0, 0); PG8_STAGE(PG8_SA(1, 1), a1 + hstepA, voffA);
;             PG8_WAIT_V(8); PG8_WAIT_L(0); PG8_BAR; PG8_MMA(0, 0, At, B0); PG8_MMA(0, 1, At, B1); PG8_BAR; PG8_SCHED;
;             PG8_LDA(At, 0, 1); PG8_STAGE(PG8_SB(0, 0), b2, voffB); PG8_STAGE(PG8_SB(0, 1), b2 + hstepB, voffB); PG8_STAGE(PG8_SA(0, 0), a2, voffA);
;             PG8_WAIT_V(8); PG8_WAIT_L(0); PG8_BAR; PG8_MMA(1, 0, At, B0); PG8_MMA(1, 1, At, B1); PG8_BAR; PG8_SCHED;
;             PG8_LDB(B0, 1, 0); PG8_LDB(B1, 1, 1); PG8_SCHED; PG8_LDA(At, 1, 0); PG8_STAGE(PG8_SA(0, 1), a2 + hstepA, voffA);
;             PG8_WAIT_V(8); PG8_WAIT_L(0); PG8_BAR; PG8_MMA(0, 0, At, B0); PG8_MMA(0, 1, At, B1); PG8_BAR; PG8_SCHED;
;             PG8_LDA(At, 1, 1); PG8_STAGE(PG8_SB(1, 0), b3, voffB); PG8_STAGE(PG8_SB(1, 1), b3 + hstepB, voffB); PG8_STAGE(PG8_SA(1, 0), a3, voffA);
;             PG8_WAIT_V(8); PG8_WAIT_L(0); PG8_BAR; PG8_MMA(1, 0, At, B0); PG8_MMA(1, 1, At, B1); PG8_BAR; PG8_SCHED;
;         }
.LBB0_1671:
	s_add_u32 s22, s20, 0x100
	s_addc_u32 s23, s21, 0
	s_add_i32 s87, 0, 0x10000
	s_cmpk_eq_i32 s86, 0x54
	s_cselect_b32 s27, s11, s23
	s_cselect_b32 s26, s10, s22
	s_cselect_b32 s25, s13, s85
	s_cselect_b32 s24, s12, s50
	s_add_i32 s88, 0, 0x14000
	v_add_u32_e32 v142, s87, v201
	v_add_u32_e32 v168, s88, v201
	ds_read_b128 v[130:133], v142
	ds_read_b128 v[134:137], v142 offset:1024
	ds_read_b128 v[138:141], v142 offset:2048
	ds_read_b128 v[142:145], v142 offset:3072
	ds_read_b128 v[146:149], v168
	ds_read_b128 v[150:153], v168 offset:1024
	ds_read_b128 v[154:157], v168 offset:2048
	ds_read_b128 v[168:171], v168 offset:3072
	v_lshl_add_u64 v[208:209], s[20:21], 0, v[164:165]
	s_add_i32 m0, s34, 0xc000
	ds_read_b128 v[172:175], v203
	ds_read_b128 v[176:179], v203 offset:1024
	ds_read_b128 v[180:183], v203 offset:2048
	ds_read_b128 v[184:187], v203 offset:3072
	ds_read_b128 v[188:191], v203 offset:4096
	ds_read_b128 v[192:195], v203 offset:5120
	ds_read_b128 v[196:199], v203 offset:6144
	ds_read_b128 v[204:207], v203 offset:7168
	global_load_lds_dwordx4 v[208:209], off
	v_lshl_add_u64 v[208:209], s[20:21], 0, v[166:167]
	s_add_i32 m0, s34, 0xe000
	s_nop 0
	global_load_lds_dwordx4 v[208:209], off
	s_waitcnt vmcnt(8)
	s_waitcnt lgkmcnt(0)
	s_barrier
	s_setprio 1
	s_waitcnt lgkmcnt(0)
	v_mfma_f32_16x16x32_bf16 v[126:129], v[130:133], v[172:175], v[126:129]
	v_mfma_f32_16x16x32_bf16 v[122:125], v[138:141], v[172:175], v[122:125]
	v_mfma_f32_16x16x32_bf16 v[106:109], v[138:141], v[180:183], v[106:109]
	v_mfma_f32_16x16x32_bf16 v[110:113], v[130:133], v[180:183], v[110:113]
	v_mfma_f32_16x16x32_bf16 v[94:97], v[130:133], v[188:191], v[94:97]
	v_mfma_f32_16x16x32_bf16 v[90:93], v[138:141], v[188:191], v[90:93]
	v_mfma_f32_16x16x32_bf16 v[74:77], v[138:141], v[196:199], v[74:77]
	v_mfma_f32_16x16x32_bf16 v[78:81], v[130:133], v[196:199], v[78:81]
	v_mfma_f32_16x16x32_bf16 v[126:129], v[134:137], v[176:179], v[126:129]
	v_mfma_f32_16x16x32_bf16 v[122:125], v[142:145], v[176:179], v[122:125]
	v_mfma_f32_16x16x32_bf16 v[106:109], v[142:145], v[184:187], v[106:109]
	v_mfma_f32_16x16x32_bf16 v[110:113], v[134:137], v[184:187], v[110:113]
	v_mfma_f32_16x16x32_bf16 v[94:97], v[134:137], v[192:195], v[94:97]
	v_mfma_f32_16x16x32_bf16 v[90:93], v[142:145], v[192:195], v[90:93]
	v_mfma_f32_16x16x32_bf16 v[74:77], v[142:145], v[204:207], v[74:77]
	v_mfma_f32_16x16x32_bf16 v[78:81], v[134:137], v[204:207], v[78:81]
	s_setprio 0
	s_setprio 1
	v_mfma_f32_16x16x32_bf16 v[118:121], v[146:149], v[172:175], v[118:121]
	v_mfma_f32_16x16x32_bf16 v[114:117], v[154:157], v[172:175], v[114:117]
	v_mfma_f32_16x16x32_bf16 v[98:101], v[154:157], v[180:183], v[98:101]
	v_mfma_f32_16x16x32_bf16 v[102:105], v[146:149], v[180:183], v[102:105]
	v_mfma_f32_16x16x32_bf16 v[86:89], v[146:149], v[188:191], v[86:89]
	v_mfma_f32_16x16x32_bf16 v[82:85], v[154:157], v[188:191], v[82:85]
	v_mfma_f32_16x16x32_bf16 v[66:69], v[154:157], v[196:199], v[66:69]
	v_mfma_f32_16x16x32_bf16 v[70:73], v[146:149], v[196:199], v[70:73]
	v_mfma_f32_16x16x32_bf16 v[118:121], v[150:153], v[176:179], v[118:121]
	v_mfma_f32_16x16x32_bf16 v[114:117], v[168:171], v[176:179], v[114:117]
	v_mfma_f32_16x16x32_bf16 v[98:101], v[168:171], v[184:187], v[98:101]
	v_mfma_f32_16x16x32_bf16 v[102:105], v[150:153], v[184:187], v[102:105]
	s_setprio 0
	v_mfma_f32_16x16x32_bf16 v[86:89], v[150:153], v[192:195], v[86:89]
	v_mfma_f32_16x16x32_bf16 v[82:85], v[168:171], v[192:195], v[82:85]
	v_mfma_f32_16x16x32_bf16 v[66:69], v[168:171], v[204:207], v[66:69]
	v_mfma_f32_16x16x32_bf16 v[70:73], v[150:153], v[204:207], v[70:73]
	s_barrier
	s_add_i32 s20, s87, s31
	v_lshl_add_u64 v[208:209], s[24:25], 0, v[0:1]
	s_mov_b32 m0, s20
	ds_read_b128 v[172:175], v203 offset:16384
	ds_read_b128 v[176:179], v203 offset:17408
	ds_read_b128 v[180:183], v203 offset:18432
	ds_read_b128 v[184:187], v203 offset:19456
	ds_read_b128 v[188:191], v203 offset:20480
	ds_read_b128 v[192:195], v203 offset:21504
	ds_read_b128 v[196:199], v203 offset:22528
	ds_read_b128 v[204:207], v203 offset:23552
	global_load_lds_dwordx4 v[208:209], off
	s_add_i32 m0, s20, 0x2000
	s_add_u32 s20, s24, 0x164000
	v_lshl_add_u64 v[210:211], s[24:25], 0, v[158:159]
	s_addc_u32 s21, s25, 0
	s_add_i32 s87, s88, s31
	global_load_lds_dwordx4 v[210:211], off
	v_lshl_add_u64 v[212:213], s[20:21], 0, v[0:1]
	s_mov_b32 m0, s87
	v_lshl_add_u64 v[214:215], s[26:27], 0, v[160:161]
	global_load_lds_dwordx4 v[212:213], off
	v_lshl_add_u64 v[212:213], s[20:21], 0, v[158:159]
	s_add_i32 m0, s87, 0x2000
	s_nop 0
	global_load_lds_dwordx4 v[212:213], off
	v_lshl_add_u64 v[212:213], s[26:27], 0, v[162:163]
	s_mov_b32 m0, s34
	s_nop 0
	global_load_lds_dwordx4 v[212:213], off
	s_mov_b32 m0, s35
	s_nop 0
	global_load_lds_dwordx4 v[214:215], off
	s_waitcnt vmcnt(8)
	s_waitcnt lgkmcnt(0)
	s_barrier
; #define PG8_STAGE(bufoff, gbase, voff) do { _Pragma("unroll") for (int _i = 0; _i < 2; ++_i) \
;         __builtin_amdgcn_global_load_lds((const unsigned*)((const char*)(gbase) + (voff)[_i]), (PG8_LAS unsigned*)(lds + (bufoff) + ldsw + _i * 8192), 16, 0, 0); } while (0)
; #define PG8_WAIT_V(n) asm volatile("s_waitcnt vmcnt(" #n ")" ::: "memory")
; #define PG8_WAIT_L(n) asm volatile("s_waitcnt lgkmcnt(" #n ")" ::: "memory")
; #define PG8_BAR __builtin_amdgcn_s_barrier()
; #define PG8_SCHED __builtin_amdgcn_sched_barrier(0)
; template <class Epi, class Sched, bool ALIGN_EPI, bool F8 = false>
; __device__ __forceinline__ void gemm_phase(PG8_LAS unsigned char* lds, const Gemm g, const Sched& S, const Epi& E, int tid) {
;     ...
;         for (int t = 0; t < nt; t += 2) {
;             const bool last = (t == nt - 2);
;             const char* a1 = cA + (size_t)(t + 1) * kstep;
;             const char* a2 = last ? nA : cA + (size_t)(t + 2) * kstep; const char* b2 = last ? nB : cB + (size_t)(t + 2) * kstep;
;             const char* a3 = a2 + kstep; const char* b3 = b2 + kstep;
;             if (last && has_next) S.a_ready(nxt);
;             PG8_LDB(B0, 0, 0); PG8_LDB(B1, 0, 1); PG8_SCHED; PG8_LDA(At, 0, 0); PG8_STAGE(PG8_SA(1, 1), a1 + hstepA, voffA);
;             PG8_WAIT_V(8); PG8_WAIT_L(0); PG8_BAR; PG8_MMA(0, 0, At, B0); PG8_MMA(0, 1, At, B1); PG8_BAR; PG8_SCHED;
;             PG8_LDA(At, 0, 1); PG8_STAGE(PG8_SB(0, 0), b2, voffB); PG8_STAGE(PG8_SB(0, 1), b2 + hstepB, voffB); PG8_STAGE(PG8_SA(0, 0), a2, voffA);
;             PG8_WAIT_V(8); PG8_WAIT_L(0); PG8_BAR; PG8_MMA(1, 0, At, B0); PG8_MMA(1, 1, At, B1); PG8_BAR; PG8_SCHED;
;             PG8_LDB(B0, 1, 0); PG8_LDB(B1, 1, 1); PG8_SCHED; PG8_LDA(At, 1, 0); PG8_STAGE(PG8_SA(0, 1), a2 + hstepA, voffA);
;             PG8_WAIT_V(8); PG8_WAIT_L(0); PG8_BAR; PG8_MMA(0, 0, At, B0); PG8_MMA(0, 1, At, B1); PG8_BAR; PG8_SCHED;
;             PG8_LDA(At, 1, 1); PG8_STAGE(PG8_SB(1, 0), b3, voffB); PG8_STAGE(PG8_SB(1, 1), b3 + hstepB, voffB); PG8_STAGE(PG8_SA(1, 0), a3, voffA);
;             PG8_WAIT_V(8); PG8_WAIT_L(0); PG8_BAR; PG8_MMA(1, 0, At, B0); PG8_MMA(1, 1, At, B1); PG8_BAR; PG8_SCHED;
;         }
	s_setprio 1
	s_waitcnt lgkmcnt(0)
	v_mfma_f32_16x16x32_bf16 v[62:65], v[130:133], v[172:175], v[62:65]
	v_mfma_f32_16x16x32_bf16 v[58:61], v[138:141], v[172:175], v[58:61]
	v_mfma_f32_16x16x32_bf16 v[42:45], v[138:141], v[180:183], v[42:45]
	v_mfma_f32_16x16x32_bf16 v[46:49], v[130:133], v[180:183], v[46:49]
	v_mfma_f32_16x16x32_bf16 v[30:33], v[130:133], v[188:191], v[30:33]
	v_mfma_f32_16x16x32_bf16 v[26:29], v[138:141], v[188:191], v[26:29]
	v_mfma_f32_16x16x32_bf16 v[10:13], v[138:141], v[196:199], v[10:13]
	v_mfma_f32_16x16x32_bf16 v[14:17], v[130:133], v[196:199], v[14:17]
	v_mfma_f32_16x16x32_bf16 v[62:65], v[134:137], v[176:179], v[62:65]
	v_mfma_f32_16x16x32_bf16 v[58:61], v[142:145], v[176:179], v[58:61]
	v_mfma_f32_16x16x32_bf16 v[42:45], v[142:145], v[184:187], v[42:45]
	v_mfma_f32_16x16x32_bf16 v[46:49], v[134:137], v[184:187], v[46:49]
	v_mfma_f32_16x16x32_bf16 v[30:33], v[134:137], v[192:195], v[30:33]
	v_mfma_f32_16x16x32_bf16 v[26:29], v[142:145], v[192:195], v[26:29]
	v_mfma_f32_16x16x32_bf16 v[10:13], v[142:145], v[204:207], v[10:13]
	v_mfma_f32_16x16x32_bf16 v[14:17], v[134:137], v[204:207], v[14:17]
	s_setprio 0
	s_setprio 1
	v_mfma_f32_16x16x32_bf16 v[54:57], v[146:149], v[172:175], v[54:57]
	v_mfma_f32_16x16x32_bf16 v[50:53], v[154:157], v[172:175], v[50:53]
	v_mfma_f32_16x16x32_bf16 v[34:37], v[154:157], v[180:183], v[34:37]
	v_mfma_f32_16x16x32_bf16 v[38:41], v[146:149], v[180:183], v[38:41]
	v_mfma_f32_16x16x32_bf16 v[22:25], v[146:149], v[188:191], v[22:25]
	v_mfma_f32_16x16x32_bf16 v[18:21], v[154:157], v[188:191], v[18:21]
	v_mfma_f32_16x16x32_bf16 v[2:5], v[154:157], v[196:199], v[2:5]
	v_mfma_f32_16x16x32_bf16 v[6:9], v[146:149], v[196:199], v[6:9]
	v_mfma_f32_16x16x32_bf16 v[54:57], v[150:153], v[176:179], v[54:57]
	v_mfma_f32_16x16x32_bf16 v[50:53], v[168:171], v[176:179], v[50:53]
	v_mfma_f32_16x16x32_bf16 v[34:37], v[168:171], v[184:187], v[34:37]
	v_mfma_f32_16x16x32_bf16 v[38:41], v[150:153], v[184:187], v[38:41]
	s_setprio 0
	v_mfma_f32_16x16x32_bf16 v[22:25], v[150:153], v[192:195], v[22:25]
	v_mfma_f32_16x16x32_bf16 v[18:21], v[168:171], v[192:195], v[18:21]
	v_mfma_f32_16x16x32_bf16 v[2:5], v[168:171], v[204:207], v[2:5]
	v_mfma_f32_16x16x32_bf16 v[6:9], v[150:153], v[204:207], v[6:9]
	s_barrier
	s_add_i32 s87, 0, 0x18000
	s_add_i32 s88, 0, 0x1c000
	v_add_u32_e32 v142, s87, v201
	v_add_u32_e32 v168, s88, v201
	ds_read_b128 v[130:133], v142
	ds_read_b128 v[134:137], v142 offset:1024
	ds_read_b128 v[138:141], v142 offset:2048
	ds_read_b128 v[142:145], v142 offset:3072
	ds_read_b128 v[146:149], v168
	ds_read_b128 v[150:153], v168 offset:1024
	ds_read_b128 v[154:157], v168 offset:2048
	ds_read_b128 v[168:171], v168 offset:3072
	s_add_u32 s20, s26, 0x180000
	s_addc_u32 s21, s27, 0
	s_mov_b32 m0, s38
	v_lshl_add_u64 v[216:217], s[20:21], 0, v[162:163]
	ds_read_b128 v[172:175], v203 offset:32768
	ds_read_b128 v[176:179], v203 offset:33792
	ds_read_b128 v[180:183], v203 offset:34816
	ds_read_b128 v[184:187], v203 offset:35840
	ds_read_b128 v[188:191], v203 offset:36864
	ds_read_b128 v[192:195], v203 offset:37888
	ds_read_b128 v[196:199], v203 offset:38912
	ds_read_b128 v[204:207], v203 offset:39936
	global_load_lds_dwordx4 v[216:217], off
	v_lshl_add_u64 v[216:217], s[20:21], 0, v[160:161]
	s_mov_b32 m0, s39
	s_nop 0
	global_load_lds_dwordx4 v[216:217], off
	s_waitcnt vmcnt(8)
	s_waitcnt lgkmcnt(0)
	s_barrier
	s_setprio 1
	s_waitcnt lgkmcnt(0)
	v_mfma_f32_16x16x32_bf16 v[126:129], v[130:133], v[172:175], v[126:129]
	v_mfma_f32_16x16x32_bf16 v[122:125], v[138:141], v[172:175], v[122:125]
	v_mfma_f32_16x16x32_bf16 v[106:109], v[138:141], v[180:183], v[106:109]
	v_mfma_f32_16x16x32_bf16 v[110:113], v[130:133], v[180:183], v[110:113]
	v_mfma_f32_16x16x32_bf16 v[94:97], v[130:133], v[188:191], v[94:97]
	v_mfma_f32_16x16x32_bf16 v[90:93], v[138:141], v[188:191], v[90:93]
	v_mfma_f32_16x16x32_bf16 v[74:77], v[138:141], v[196:199], v[74:77]
	v_mfma_f32_16x16x32_bf16 v[78:81], v[130:133], v[196:199], v[78:81]
	v_mfma_f32_16x16x32_bf16 v[126:129], v[134:137], v[176:179], v[126:129]
	v_mfma_f32_16x16x32_bf16 v[122:125], v[142:145], v[176:179], v[122:125]
	v_mfma_f32_16x16x32_bf16 v[106:109], v[142:145], v[184:187], v[106:109]
	v_mfma_f32_16x16x32_bf16 v[110:113], v[134:137], v[184:187], v[110:113]
	v_mfma_f32_16x16x32_bf16 v[94:97], v[134:137], v[192:195], v[94:97]
	v_mfma_f32_16x16x32_bf16 v[90:93], v[142:145], v[192:195], v[90:93]
	v_mfma_f32_16x16x32_bf16 v[74:77], v[142:145], v[204:207], v[74:77]
	v_mfma_f32_16x16x32_bf16 v[78:81], v[134:137], v[204:207], v[78:81]
	s_setprio 0
	s_setprio 1
	v_mfma_f32_16x16x32_bf16 v[118:121], v[146:149], v[172:175], v[118:121]
	v_mfma_f32_16x16x32_bf16 v[114:117], v[154:157], v[172:175], v[114:117]
	v_mfma_f32_16x16x32_bf16 v[98:101], v[154:157], v[180:183], v[98:101]
	v_mfma_f32_16x16x32_bf16 v[102:105], v[146:149], v[180:183], v[102:105]
	v_mfma_f32_16x16x32_bf16 v[86:89], v[146:149], v[188:191], v[86:89]
	v_mfma_f32_16x16x32_bf16 v[82:85], v[154:157], v[188:191], v[82:85]
	v_mfma_f32_16x16x32_bf16 v[66:69], v[154:157], v[196:199], v[66:69]
	v_mfma_f32_16x16x32_bf16 v[70:73], v[146:149], v[196:199], v[70:73]
	v_mfma_f32_16x16x32_bf16 v[118:121], v[150:153], v[176:179], v[118:121]
	v_mfma_f32_16x16x32_bf16 v[114:117], v[168:171], v[176:179], v[114:117]
	v_mfma_f32_16x16x32_bf16 v[98:101], v[168:171], v[184:187], v[98:101]
	v_mfma_f32_16x16x32_bf16 v[102:105], v[150:153], v[184:187], v[102:105]
	s_setprio 0
	v_mfma_f32_16x16x32_bf16 v[86:89], v[150:153], v[192:195], v[86:89]
	v_mfma_f32_16x16x32_bf16 v[82:85], v[168:171], v[192:195], v[82:85]
	v_mfma_f32_16x16x32_bf16 v[66:69], v[168:171], v[204:207], v[66:69]
	v_mfma_f32_16x16x32_bf16 v[70:73], v[150:153], v[204:207], v[70:73]
	s_barrier
;     __device__ __forceinline__ void operator()(const f32x4 (&acc)[2][2][4][2], const Unit& u, int wr, int wc, int fr, int fq) const {
;         const int row0 = u.pm * BM + wr * 64 + fr, col0 = u.pn * BM + wc * 32 + 8 * fq;
; #pragma unroll
;         for (int ai = 0; ai < 2; ++ai) {
;             u32x4 old[4][2];
; #pragma unroll
;             for (int m = 0; m < 4; ++m)
; #pragma unroll
;                 for (int bj = 0; bj < 2; ++bj) old[m][bj] = *(const u32x4*)(xb + (size_t)(row0 + ai * HALF + m * 16) * 2048 + col0 + bj * HALF);
; #pragma unroll
;             for (int m = 0; m < 4; ++m) { const size_t row = (size_t)(row0 + ai * HALF + m * 16); bf16_t* rowp = xb + row * 2048 + col0; float ss = 0.f;
; #pragma unroll
; template <class Epi, class Sched, bool ALIGN_EPI, bool F8 = false>
; __device__ __forceinline__ void gemm_phase(PG8_LAS unsigned char* lds, const Gemm g, const Sched& S, const Epi& E, int tid) {
;     ...
;         for (int t = 0; t < nt; t += 2) {
;             const bool last = (t == nt - 2);
;             const char* a1 = cA + (size_t)(t + 1) * kstep;
;             const char* a2 = last ? nA : cA + (size_t)(t + 2) * kstep; const char* b2 = last ? nB : cB + (size_t)(t + 2) * kstep;
;             const char* a3 = a2 + kstep; const char* b3 = b2 + kstep;
;             if (last && has_next) S.a_ready(nxt);
;             PG8_LDB(B0, 0, 0); PG8_LDB(B1, 0, 1); PG8_SCHED; PG8_LDA(At, 0, 0); PG8_STAGE(PG8_SA(1, 1), a1 + hstepA, voffA);
;             PG8_WAIT_V(8); PG8_WAIT_L(0); PG8_BAR; PG8_MMA(0, 0, At, B0); PG8_MMA(0, 1, At, B1); PG8_BAR; PG8_SCHED;
;             PG8_LDA(At, 0, 1); PG8_STAGE(PG8_SB(0, 0), b2, voffB); PG8_STAGE(PG8_SB(0, 1), b2 + hstepB, voffB); PG8_STAGE(PG8_SA(0, 0), a2, voffA);
;             PG8_WAIT_V(8); PG8_WAIT_L(0); PG8_BAR; PG8_MMA(1, 0, At, B0); PG8_MMA(1, 1, At, B1); PG8_BAR; PG8_SCHED;
;             PG8_LDB(B0, 1, 0); PG8_LDB(B1, 1, 1); PG8_SCHED; PG8_LDA(At, 1, 0); PG8_STAGE(PG8_SA(0, 1), a2 + hstepA, voffA);
;             PG8_WAIT_V(8); PG8_WAIT_L(0); PG8_BAR; PG8_MMA(0, 0, At, B0); PG8_MMA(0, 1, At, B1); PG8_BAR; PG8_SCHED;
;             PG8_LDA(At, 1, 1); PG8_STAGE(PG8_SB(1, 0), b3, voffB); PG8_STAGE(PG8_SB(1, 1), b3 + hstepB, voffB); PG8_STAGE(PG8_SA(1, 0), a3, voffA);
;             PG8_WAIT_V(8); PG8_WAIT_L(0); PG8_BAR; PG8_MMA(1, 0, At, B0); PG8_MMA(1, 1, At, B1); PG8_BAR; PG8_SCHED;
;         }
	s_add_i32 s20, s87, s31
	v_lshl_add_u64 v[208:209], v[208:209], 0, s[60:61]
	s_mov_b32 m0, s20
	ds_read_b128 v[172:175], v203 offset:49152
	ds_read_b128 v[176:179], v203 offset:50176
	ds_read_b128 v[180:183], v203 offset:51200
	ds_read_b128 v[184:187], v203 offset:52224
	ds_read_b128 v[188:191], v203 offset:53248
	ds_read_b128 v[192:195], v203 offset:54272
	ds_read_b128 v[196:199], v203 offset:55296
	ds_read_b128 v[204:207], v203 offset:56320
	global_load_lds_dwordx4 v[208:209], off
	s_add_i32 m0, s20, 0x2000
	s_add_u32 s20, s24, 0x164080
	v_lshl_add_u64 v[208:209], v[210:211], 0, s[60:61]
	s_addc_u32 s21, s25, 0
	s_add_i32 s24, s88, s31
	global_load_lds_dwordx4 v[208:209], off
	v_lshl_add_u64 v[208:209], s[20:21], 0, v[0:1]
	s_mov_b32 m0, s24
	s_nop 0
	global_load_lds_dwordx4 v[208:209], off
	v_lshl_add_u64 v[208:209], s[20:21], 0, v[158:159]
	s_add_i32 m0, s24, 0x2000
	s_nop 0
	global_load_lds_dwordx4 v[208:209], off
	v_lshl_add_u64 v[208:209], v[212:213], 0, s[60:61]
	s_mov_b32 m0, s45
	s_nop 0
	global_load_lds_dwordx4 v[208:209], off
	v_lshl_add_u64 v[208:209], v[214:215], 0, s[60:61]
	s_mov_b32 m0, s51
	s_nop 0
	global_load_lds_dwordx4 v[208:209], off
	s_waitcnt vmcnt(8)
	s_waitcnt lgkmcnt(0)
	s_barrier
	s_setprio 1
	s_waitcnt lgkmcnt(0)
	v_mfma_f32_16x16x32_bf16 v[62:65], v[130:133], v[172:175], v[62:65]
	v_mfma_f32_16x16x32_bf16 v[58:61], v[138:141], v[172:175], v[58:61]
	v_mfma_f32_16x16x32_bf16 v[42:45], v[138:141], v[180:183], v[42:45]
	v_mfma_f32_16x16x32_bf16 v[46:49], v[130:133], v[180:183], v[46:49]
	v_mfma_f32_16x16x32_bf16 v[30:33], v[130:133], v[188:191], v[30:33]
	v_mfma_f32_16x16x32_bf16 v[26:29], v[138:141], v[188:191], v[26:29]
	v_mfma_f32_16x16x32_bf16 v[10:13], v[138:141], v[196:199], v[10:13]
	v_mfma_f32_16x16x32_bf16 v[14:17], v[130:133], v[196:199], v[14:17]
	v_mfma_f32_16x16x32_bf16 v[62:65], v[134:137], v[176:179], v[62:65]
	v_mfma_f32_16x16x32_bf16 v[58:61], v[142:145], v[176:179], v[58:61]
	v_mfma_f32_16x16x32_bf16 v[42:45], v[142:145], v[184:187], v[42:45]
	v_mfma_f32_16x16x32_bf16 v[46:49], v[134:137], v[184:187], v[46:49]
	v_mfma_f32_16x16x32_bf16 v[30:33], v[134:137], v[192:195], v[30:33]
	v_mfma_f32_16x16x32_bf16 v[26:29], v[142:145], v[192:195], v[26:29]
	v_mfma_f32_16x16x32_bf16 v[10:13], v[142:145], v[204:207], v[10:13]
	v_mfma_f32_16x16x32_bf16 v[14:17], v[134:137], v[204:207], v[14:17]
	s_setprio 0
	s_setprio 1
	v_mfma_f32_16x16x32_bf16 v[54:57], v[146:149], v[172:175], v[54:57]
	v_mfma_f32_16x16x32_bf16 v[50:53], v[154:157], v[172:175], v[50:53]
	v_mfma_f32_16x16x32_bf16 v[34:37], v[154:157], v[180:183], v[34:37]
	v_mfma_f32_16x16x32_bf16 v[38:41], v[146:149], v[180:183], v[38:41]
	v_mfma_f32_16x16x32_bf16 v[22:25], v[146:149], v[188:191], v[22:25]
	v_mfma_f32_16x16x32_bf16 v[18:21], v[154:157], v[188:191], v[18:21]
	v_mfma_f32_16x16x32_bf16 v[2:5], v[154:157], v[196:199], v[2:5]
	v_mfma_f32_16x16x32_bf16 v[6:9], v[146:149], v[196:199], v[6:9]
	v_mfma_f32_16x16x32_bf16 v[54:57], v[150:153], v[176:179], v[54:57]
	v_mfma_f32_16x16x32_bf16 v[50:53], v[168:171], v[176:179], v[50:53]
	v_mfma_f32_16x16x32_bf16 v[34:37], v[168:171], v[184:187], v[34:37]
	v_mfma_f32_16x16x32_bf16 v[38:41], v[150:153], v[184:187], v[38:41]
	s_setprio 0
	v_mfma_f32_16x16x32_bf16 v[22:25], v[150:153], v[192:195], v[22:25]
	v_mfma_f32_16x16x32_bf16 v[18:21], v[168:171], v[192:195], v[18:21]
	v_mfma_f32_16x16x32_bf16 v[2:5], v[168:171], v[204:207], v[2:5]
	v_mfma_f32_16x16x32_bf16 v[6:9], v[150:153], v[204:207], v[6:9]
	s_barrier
	s_add_i32 s86, s86, 2
	s_add_u32 s50, s50, 0x100
	s_addc_u32 s85, s85, 0
	s_cmpk_gt_u32 s86, 0x55
	s_mov_b64 s[20:21], s[22:23]
	s_cbranch_scc0 .LBB0_1671
	v_lshl_or_b32 v168, s69, 8, v202
	v_lshl_add_u32 v172, s84, 8, v200
	v_ashrrev_i32_e32 v169, 31, v168
	v_lshlrev_b64 v[182:183], 1, v[168:169]
	v_ashrrev_i32_e32 v173, 31, v172
	v_lshl_add_u64 v[170:171], s[14:15], 0, v[182:183]
	v_lshlrev_b64 v[184:185], 12, v[172:173]
	v_lshl_add_u64 v[130:131], v[170:171], 0, v[184:185]
	global_load_dwordx4 v[178:181], v[130:131], off
	global_load_dwordx4 v[154:157], v[130:131], off offset:256
	v_or_b32_e32 v192, 16, v172
	v_ashrrev_i32_e32 v193, 31, v192
	v_or_b32_e32 v176, 32, v172
	v_lshlrev_b64 v[196:197], 12, v[192:193]
	v_ashrrev_i32_e32 v177, 31, v176
	v_or_b32_e32 v174, 48, v172
	v_lshl_add_u64 v[130:131], v[170:171], 0, v[196:197]
	v_lshlrev_b64 v[194:195], 12, v[176:177]
	v_ashrrev_i32_e32 v175, 31, v174
	global_load_dwordx4 v[150:153], v[130:131], off
	global_load_dwordx4 v[146:149], v[130:131], off offset:256
	v_lshl_add_u64 v[130:131], v[170:171], 0, v[194:195]
	v_lshlrev_b64 v[190:191], 12, v[174:175]
	global_load_dwordx4 v[142:145], v[130:131], off
	global_load_dwordx4 v[138:141], v[130:131], off offset:256
	v_lshl_add_u64 v[130:131], v[170:171], 0, v[190:191]
	global_load_dwordx4 v[134:137], v[130:131], off
	s_nop 0
	global_load_dwordx4 v[130:133], v[130:131], off offset:256
	v_lshl_add_u64 v[184:185], s[14:15], 0, v[184:185]
	v_lshl_add_u64 v[198:199], v[184:185], 0, v[182:183]
	v_lshlrev_b64 v[186:187], 11, v[172:173]
	s_and_b64 vcc, exec, s[4:5]
	s_waitcnt vmcnt(0)
	v_lshlrev_b32_e32 v182, 16, v178
	v_and_b32_e32 v178, 0xffff0000, v178
	v_add_f32_e32 v204, v127, v178
	v_lshlrev_b32_e32 v127, 16, v179
	v_add_f32_e32 v127, v128, v127
	v_and_b32_e32 v128, 0xffff0000, v179
	v_add_f32_e32 v129, v129, v128
	v_lshlrev_b32_e32 v128, 16, v180
	v_add_f32_e32 v128, v122, v128
	v_and_b32_e32 v122, 0xffff0000, v180
	v_add_f32_e32 v205, v123, v122
	v_lshlrev_b32_e32 v122, 16, v181
	v_add_f32_e32 v124, v124, v122
	v_and_b32_e32 v122, 0xffff0000, v181
	v_add_f32_e32 v125, v125, v122
	v_lshl_add_u64 v[122:123], s[18:19], 0, v[186:187]
	v_add_f32_e32 v126, v126, v182
	v_lshl_add_u64 v[122:123], v[122:123], 0, v[168:169]
	v_cvt_pk_bf16_f32 v178, v126, v204
	v_cvt_pk_bf16_f32 v179, v127, v129
	v_cvt_pk_bf16_f32 v180, v128, v205
	v_cvt_pk_bf16_f32 v181, v124, v125
	global_store_dwordx4 v[198:199], v[178:181], off
	s_cbranch_vccnz .LBB0_1674
	s_nop 0
	v_add_f32_e32 v179, v126, v126
	v_add_f32_e32 v180, v204, v204
	v_mov_b32_e32 v178, v1
	v_cvt_pk_fp8_f32 v178, v179, v180
	v_add_f32_e32 v180, v128, v128
	v_add_f32_e32 v183, v205, v205
	v_mov_b32_e32 v179, v1
	v_cvt_pk_fp8_f32 v179, v180, v183
	v_add_f32_e32 v181, v127, v127
	v_add_f32_e32 v182, v129, v129
	v_cvt_pk_fp8_f32 v178, v181, v182 op_sel:[0,0,1]
	v_add_f32_e32 v180, v124, v124
	v_add_f32_e32 v181, v125, v125
	v_cvt_pk_fp8_f32 v179, v180, v181 op_sel:[0,0,1]
	global_store_dwordx2 v[122:123], v[178:179], off
